# speedup vs baseline: 1.0867x; 1.0088x over previous
_Z11jacobi_mainPKfS0_S0_PyPf:
	s_lshl_b32 s3, s2, 3
	s_load_dwordx4 s[12:15], s[0:1], 0x0
	s_load_dwordx2 s[4:5], s[0:1], 0x10
	s_and_b32 s3, s3, 56
	s_ashr_i32 s33, s2, 5
	v_readfirstlane_b32 s40, v0
	s_add_i32 s18, s3, s33
	s_bfe_u32 s3, s2, 0x20003
	s_lshl_b32 s7, s3, 8
	s_and_b32 s10, s40, 0xffffffc0
	s_ashr_i32 s19, s18, 31
	s_lshr_b32 s34, s2, 3
	s_add_i32 s11, s10, s7
	s_lshl_b64 s[8:9], s[18:19], 22
	v_and_b32_e32 v206, 63, v0
	s_waitcnt lgkmcnt(0)
	s_add_u32 s8, s12, s8
	s_addc_u32 s9, s13, s9
	v_or_b32_e32 v154, s11, v206
	s_lshl_b32 s6, s18, 10
	v_add_u32_e32 v2, s6, v154
	v_ashrrev_i32_e32 v3, 31, v2
	v_lshlrev_b64 v[2:3], 2, v[2:3]
	v_lshl_add_u64 v[4:5], s[14:15], 0, v[2:3]
	global_load_dword v1, v[4:5], off
	s_movk_i32 s12, 0x1004
	v_mov_b64_e32 v[4:5], s[8:9]
	v_mad_i64_i32 v[4:5], s[12:13], v154, s12, v[4:5]
	v_lshl_add_u64 v[2:3], s[4:5], 0, v[2:3]
	global_load_dword v207, v[4:5], off
	global_load_dword v66, v[2:3], off
	s_lshl_b32 s76, s6, 2
	s_add_u32 s76, s4, s76
	s_addc_u32 s77, s5, 0
	v_lshlrev_b32_e32 v220, 4, v0
	global_load_dwordx4 v[224:227], v220, s[76:77]
	v_mbcnt_lo_u32_b32 v2, -1, 0
	v_mbcnt_hi_u32_b32 v2, -1, v2
	v_and_b32_e32 v3, 64, v2
	v_xor_b32_e32 v4, 32, v2
	v_add_u32_e32 v3, 64, v3
	v_cmp_lt_i32_e32 vcc, v4, v3
	v_xor_b32_e32 v6, 8, v2
	s_load_dwordx2 s[16:17], s[0:1], 0x20
	v_cndmask_b32_e32 v4, v2, v4, vcc
	v_lshlrev_b32_e32 v4, 2, v4
	v_ashrrev_i32_e32 v155, 31, v154
	s_mov_b32 s21, 0
	s_lshr_b32 s35, s40, 6
	v_cmp_eq_u32_e64 s[12:13], 0, v206
	s_waitcnt vmcnt(2)
	v_mul_f32_e32 v5, v1, v1
	ds_bpermute_b32 v4, v4, v5
	v_xor_b32_e32 v5, 16, v2
	v_cmp_lt_i32_e32 vcc, v5, v3
	s_waitcnt lgkmcnt(0)
	v_fmac_f32_e32 v4, v1, v1
	v_cndmask_b32_e32 v5, v2, v5, vcc
	v_lshlrev_b32_e32 v5, 2, v5
	ds_bpermute_b32 v5, v5, v4
	v_cmp_lt_i32_e32 vcc, v6, v3
	s_waitcnt lgkmcnt(0)
	v_add_f32_e32 v4, v4, v5
	v_cndmask_b32_e32 v6, v2, v6, vcc
	v_lshlrev_b32_e32 v6, 2, v6
	ds_bpermute_b32 v5, v6, v4
	v_xor_b32_e32 v6, 4, v2
	v_cmp_lt_i32_e32 vcc, v6, v3
	s_waitcnt lgkmcnt(0)
	v_add_f32_e32 v4, v4, v5
	v_cndmask_b32_e32 v6, v2, v6, vcc
	v_lshlrev_b32_e32 v6, 2, v6
	ds_bpermute_b32 v5, v6, v4
	v_xor_b32_e32 v6, 2, v2
	v_cmp_lt_i32_e32 vcc, v6, v3
	s_waitcnt lgkmcnt(0)
	v_add_f32_e32 v4, v4, v5
	v_cndmask_b32_e32 v6, v2, v6, vcc
	v_lshlrev_b32_e32 v6, 2, v6
	ds_bpermute_b32 v5, v6, v4
	v_xor_b32_e32 v6, 1, v2
	v_cmp_lt_i32_e32 vcc, v6, v3
	s_nop 1
	v_cndmask_b32_e32 v3, v2, v6, vcc
	s_waitcnt lgkmcnt(0)
	v_add_f32_e32 v2, v4, v5
	v_lshlrev_b32_e32 v3, 2, v3
	ds_bpermute_b32 v3, v3, v2
	s_and_saveexec_b64 s[14:15], s[12:13]
	s_cbranch_execz .LBB0_2
	s_lshl_b32 s20, s35, 2
	s_add_i32 s20, s20, 0x26a00
	s_waitcnt lgkmcnt(0)
	v_add_f32_e32 v2, v2, v3
	v_mov_b32_e32 v3, s20
	ds_write_b32 v3, v2
.LBB0_2:
	s_or_b64 exec, exec, s[14:15]
	s_load_dwordx2 s[0:1], s[0:1], 0x18
	v_lshrrev_b32_e32 v67, 5, v206
	v_or_b32_e32 v132, s11, v67
	s_lshl_b64 s[14:15], s[18:19], 14
	v_ashrrev_i32_e32 v133, 31, v132
	v_and_b32_e32 v124, 31, v0
	s_waitcnt lgkmcnt(0)
	s_add_u32 s14, s0, s14
	v_lshlrev_b64 v[2:3], 12, v[132:133]
	s_addc_u32 s15, s1, s15
	s_add_i32 s0, s7, 0x100
	v_lshl_add_u64 v[2:3], s[8:9], 0, v[2:3]
	v_lshlrev_b32_e32 v190, 4, v124
	v_mov_b32_e32 v191, 0
	s_and_b32 s26, s0, 0x300
	v_lshl_add_u64 v[130:131], v[2:3], 0, v[190:191]
	s_mov_b64 s[0:1], 0x30000
	v_lshl_add_u64 v[126:127], v[130:131], 0, s[0:1]
	s_mov_b64 s[0:1], 0x32000
	v_lshl_add_u64 v[128:129], v[130:131], 0, s[0:1]
	s_mov_b64 s[0:1], 0x34000
	v_lshl_add_u64 v[134:135], v[130:131], 0, s[0:1]
	s_mov_b64 s[0:1], 0x36000
	v_lshl_add_u64 v[136:137], v[130:131], 0, s[0:1]
	s_mov_b64 s[0:1], 0x38000
	v_lshl_add_u64 v[138:139], v[130:131], 0, s[0:1]
	s_mov_b64 s[0:1], 0x3a000
	v_lshl_add_u64 v[140:141], v[130:131], 0, s[0:1]
	s_mov_b64 s[0:1], 0x3c000
	s_or_b32 s24, s7, 0x80
	v_lshl_add_u64 v[142:143], v[130:131], 0, s[0:1]
	s_mov_b64 s[0:1], 0x3e000
	s_lshl_b32 s20, s7, 2
	v_lshl_add_u64 v[144:145], v[130:131], 0, s[0:1]
	s_lshl_b32 s8, s24, 2
	s_mov_b32 s9, s21
	v_lshl_add_u64 v[2:3], v[126:127], 0, s[20:21]
	v_lshl_add_u64 v[4:5], v[128:129], 0, s[20:21]
	v_lshl_add_u64 v[6:7], v[134:135], 0, s[20:21]
	v_lshl_add_u64 v[8:9], v[136:137], 0, s[20:21]
	v_lshl_add_u64 v[10:11], v[138:139], 0, s[20:21]
	v_lshl_add_u64 v[12:13], v[140:141], 0, s[20:21]
	v_lshl_add_u64 v[14:15], v[142:143], 0, s[20:21]
	v_lshl_add_u64 v[16:17], v[144:145], 0, s[20:21]
	v_lshl_add_u64 v[18:19], v[126:127], 0, s[8:9]
	v_lshl_add_u64 v[20:21], v[128:129], 0, s[8:9]
	v_lshl_add_u64 v[22:23], v[134:135], 0, s[8:9]
	v_lshl_add_u64 v[24:25], v[136:137], 0, s[8:9]
	s_lshl_b32 s0, s26, 2
	s_mov_b32 s1, s21
	v_lshl_add_u64 v[72:73], v[138:139], 0, s[8:9]
	v_lshl_add_u64 v[102:103], v[140:141], 0, s[8:9]
	v_lshl_add_u64 v[104:105], v[142:143], 0, s[8:9]
	v_lshl_add_u64 v[106:107], v[144:145], 0, s[8:9]
	v_lshl_add_u64 v[108:109], v[126:127], 0, s[0:1]
	v_lshl_add_u64 v[110:111], v[128:129], 0, s[0:1]
	v_lshl_add_u64 v[112:113], v[134:135], 0, s[0:1]
	v_lshl_add_u64 v[114:115], v[136:137], 0, s[0:1]
	v_lshl_add_u64 v[116:117], v[138:139], 0, s[0:1]
	v_lshl_add_u64 v[118:119], v[140:141], 0, s[0:1]
	v_lshl_add_u64 v[120:121], v[142:143], 0, s[0:1]
	v_lshl_add_u64 v[122:123], v[144:145], 0, s[0:1]
	global_load_dwordx4 v[68:71], v[2:3], off nt
	global_load_dwordx4 v[78:81], v[4:5], off nt
	global_load_dwordx4 v[82:85], v[6:7], off nt
	global_load_dwordx4 v[90:93], v[8:9], off nt
	global_load_dwordx4 v[98:101], v[10:11], off nt
	global_load_dwordx4 v[62:65], v[12:13], off nt
	global_load_dwordx4 v[54:57], v[14:15], off nt
	global_load_dwordx4 v[46:49], v[16:17], off nt
	global_load_dwordx4 v[94:97], v[18:19], off nt
	global_load_dwordx4 v[86:89], v[20:21], off nt
	global_load_dwordx4 v[74:77], v[22:23], off nt
	global_load_dwordx4 v[58:61], v[24:25], off nt
	global_load_dwordx4 v[50:53], v[72:73], off nt
	global_load_dwordx4 v[42:45], v[102:103], off nt
	global_load_dwordx4 v[38:41], v[104:105], off nt
	global_load_dwordx4 v[34:37], v[106:107], off nt
	global_load_dwordx4 v[30:33], v[108:109], off nt
	global_load_dwordx4 v[26:29], v[110:111], off nt
	s_nop 0
	global_load_dwordx4 v[22:25], v[112:113], off nt
	global_load_dwordx4 v[18:21], v[114:115], off nt
	global_load_dwordx4 v[14:17], v[116:117], off nt
	global_load_dwordx4 v[10:13], v[118:119], off nt
	global_load_dwordx4 v[6:9], v[120:121], off nt
	global_load_dwordx4 v[2:5], v[122:123], off nt
	s_waitcnt vmcnt(25)
	v_div_scale_f32 v72, s[22:23], v207, v207, 1.0
	v_rcp_f32_e32 v73, v72
	s_lshl_b32 s11, s10, 2
	s_mul_i32 s19, s35, 0x1100
	s_add_i32 s22, s11, 0x26600
	v_fma_f32 v103, -v72, v73, 1.0
	v_fmac_f32_e32 v73, v103, v73
	v_div_scale_f32 v103, vcc, 1.0, v207, 1.0
	v_mul_f32_e32 v104, v103, v73
	v_fma_f32 v105, -v72, v104, v103
	v_fmac_f32_e32 v104, v105, v73
	v_fma_f32 v72, -v72, v104, v103
	v_div_fmas_f32 v72, v72, v73, v104
	v_div_fixup_f32 v72, v72, v207, 1.0
	s_waitcnt vmcnt(24)
	v_fma_f32 v208, v72, v1, -v66
	v_lshl_add_u32 v1, v206, 2, s22
	s_add_i32 s19, s19, 0x22200
	ds_write_b32 v1, v72
	v_lshl_or_b32 v1, v124, 3, s19
	v_lshl_add_u32 v187, v67, 2, s22
	s_movk_i32 s22, 0x110
	v_mad_u32_u24 v186, v67, s22, v1
	s_add_i32 s22, s7, 0x180
	v_and_b32_e32 v102, 15, v0
	s_lshl_b32 s27, s34, 8
	s_and_b32 s25, s22, 0x380
	s_add_i32 s22, s7, 0x280
	v_lshlrev_b32_e32 v66, 2, v124
	v_mul_u32_u24_e32 v1, 0x110, v102
	v_and_b32_e32 v209, 48, v0
	s_and_b32 s23, s22, 0x380
	s_add_i32 s22, s7, 0x300
	v_mov_b32_e32 v67, 0x200
	s_addk_i32 s27, 0x380
	v_or_b32_e32 v133, s7, v66
	v_add3_u32 v1, s19, v1, v209
	s_lshl_b32 s19, s35, 15
	v_lshlrev_b32_e32 v210, 4, v206
	v_or_b32_e32 v189, s24, v66
	s_xor_b32 s24, s7, 0x200
	s_and_b32 s22, s22, 0x300
	v_bitop3_b32 v197, s7, v66, v67 bitop3:0xde
	s_and_b32 s7, s27, 0x380
	v_lshrrev_b32_e32 v185, 4, v206
	s_ashr_i32 s11, s10, 31
	v_or_b32_e32 v184, s19, v210
	v_or_b32_e32 v188, s26, v66
	v_or_b32_e32 v198, s25, v66
	v_or_b32_e32 v196, s23, v66
	v_or_b32_e32 v195, s22, v66
	v_or_b32_e32 v194, s7, v66
	v_mov_b32_e32 v102, v133
	s_waitcnt vmcnt(23)
	s_waitcnt vmcnt(22)
	s_waitcnt vmcnt(21)
	s_waitcnt vmcnt(20)
	s_waitcnt vmcnt(19)
	s_waitcnt vmcnt(18)
	s_waitcnt vmcnt(17)
	s_waitcnt vmcnt(16)
	ds_read_b32 v66, v187 offset:192
	v_or_b32_e32 v103, 48, v132
	v_add_u32_e32 v104, 1, v102
	v_cmp_eq_u32_e32 vcc, v102, v103
	v_add_u32_e32 v105, 3, v102
	v_add_u32_e32 v106, 2, v102
	v_cndmask_b32_e64 v72, 0, 1.0, vcc
	v_cmp_eq_u32_e32 vcc, v104, v103
	v_or_b32_e32 v107, 50, v132
	v_or_b32_e32 v108, 52, v132
	v_cndmask_b32_e64 v73, 0, 1.0, vcc
	v_cmp_eq_u32_e32 vcc, v105, v103
	s_waitcnt lgkmcnt(0)
	v_pk_fma_f32 v[68:69], v[66:67], v[68:69], v[72:73] op_sel_hi:[0,1,1] neg_lo:[1,0,0] neg_hi:[1,0,0]
	v_cvt_pk_bf16_f32 v68, v68, v69
	v_cndmask_b32_e64 v73, 0, 1.0, vcc
	v_cmp_eq_u32_e32 vcc, v106, v103
	v_or_b32_e32 v109, 54, v132
	v_or_b32_e32 v110, 56, v132
	v_cndmask_b32_e64 v72, 0, 1.0, vcc
	v_pk_fma_f32 v[66:67], v[66:67], v[70:71], v[72:73] op_sel_hi:[0,1,1] neg_lo:[1,0,0] neg_hi:[1,0,0]
	v_cvt_pk_bf16_f32 v69, v66, v67
	ds_write_b64 v186, v[68:69]
	ds_read_b32 v66, v187 offset:200
	v_cmp_eq_u32_e32 vcc, v102, v107
	v_or_b32_e32 v111, 58, v132
	v_or_b32_e32 v112, 60, v132
	v_cndmask_b32_e64 v68, 0, 1.0, vcc
	v_cmp_eq_u32_e32 vcc, v104, v107
	v_or_b32_e32 v113, 62, v132
	v_or_b32_e32 v193, 2, v132
	v_cndmask_b32_e64 v69, 0, 1.0, vcc
	v_cmp_eq_u32_e32 vcc, v105, v107
	s_waitcnt lgkmcnt(0)
	v_pk_fma_f32 v[68:69], v[66:67], v[78:79], v[68:69] op_sel_hi:[0,1,1] neg_lo:[1,0,0] neg_hi:[1,0,0]
	v_cvt_pk_bf16_f32 v68, v68, v69
	v_cndmask_b32_e64 v71, 0, 1.0, vcc
	v_cmp_eq_u32_e32 vcc, v106, v107
	v_or_b32_e32 v192, 4, v132
	v_or_b32_e32 v190, 6, v132
	v_cndmask_b32_e64 v70, 0, 1.0, vcc
	v_pk_fma_f32 v[66:67], v[66:67], v[80:81], v[70:71] op_sel_hi:[0,1,1] neg_lo:[1,0,0] neg_hi:[1,0,0]
	v_cvt_pk_bf16_f32 v69, v66, v67
	ds_write_b64 v186, v[68:69] offset:544
	ds_read_b32 v66, v187 offset:208
	v_cmp_eq_u32_e32 vcc, v102, v108
	v_or_b32_e32 v149, 8, v132
	v_or_b32_e32 v148, 10, v132
	v_cndmask_b32_e64 v68, 0, 1.0, vcc
	v_cmp_eq_u32_e32 vcc, v104, v108
	v_or_b32_e32 v147, 12, v132
	v_or_b32_e32 v146, 14, v132
	v_cndmask_b32_e64 v69, 0, 1.0, vcc
	v_cmp_eq_u32_e32 vcc, v105, v108
	s_waitcnt lgkmcnt(0)
	v_pk_fma_f32 v[68:69], v[66:67], v[82:83], v[68:69] op_sel_hi:[0,1,1] neg_lo:[1,0,0] neg_hi:[1,0,0]
	v_cvt_pk_bf16_f32 v68, v68, v69
	v_cndmask_b32_e64 v71, 0, 1.0, vcc
	v_cmp_eq_u32_e32 vcc, v106, v108
	s_nop 1
	v_cndmask_b32_e64 v70, 0, 1.0, vcc
	v_pk_fma_f32 v[66:67], v[66:67], v[84:85], v[70:71] op_sel_hi:[0,1,1] neg_lo:[1,0,0] neg_hi:[1,0,0]
	v_cvt_pk_bf16_f32 v69, v66, v67
	ds_write_b64 v186, v[68:69] offset:1088
	ds_read_b32 v66, v187 offset:216
	v_cmp_eq_u32_e32 vcc, v102, v109
	s_nop 1
	v_cndmask_b32_e64 v68, 0, 1.0, vcc
	v_cmp_eq_u32_e32 vcc, v104, v109
	s_nop 1
	v_cndmask_b32_e64 v69, 0, 1.0, vcc
	v_cmp_eq_u32_e32 vcc, v105, v109
	s_waitcnt lgkmcnt(0)
	v_pk_fma_f32 v[68:69], v[66:67], v[90:91], v[68:69] op_sel_hi:[0,1,1] neg_lo:[1,0,0] neg_hi:[1,0,0]
	v_cvt_pk_bf16_f32 v68, v68, v69
	v_cndmask_b32_e64 v71, 0, 1.0, vcc
	v_cmp_eq_u32_e32 vcc, v106, v109
	s_nop 1
	v_cndmask_b32_e64 v70, 0, 1.0, vcc
	v_pk_fma_f32 v[66:67], v[66:67], v[92:93], v[70:71] op_sel_hi:[0,1,1] neg_lo:[1,0,0] neg_hi:[1,0,0]
	v_cvt_pk_bf16_f32 v69, v66, v67
	ds_write_b64 v186, v[68:69] offset:1632
	ds_read_b32 v66, v187 offset:224
	v_cmp_eq_u32_e32 vcc, v102, v110
	s_nop 1
	v_cndmask_b32_e64 v68, 0, 1.0, vcc
	v_cmp_eq_u32_e32 vcc, v104, v110
	s_nop 1
	v_cndmask_b32_e64 v69, 0, 1.0, vcc
	v_cmp_eq_u32_e32 vcc, v105, v110
	s_waitcnt lgkmcnt(0)
	v_pk_fma_f32 v[68:69], v[66:67], v[98:99], v[68:69] op_sel_hi:[0,1,1] neg_lo:[1,0,0] neg_hi:[1,0,0]
	v_cvt_pk_bf16_f32 v68, v68, v69
	v_cndmask_b32_e64 v71, 0, 1.0, vcc
	v_cmp_eq_u32_e32 vcc, v106, v110
	s_nop 1
	v_cndmask_b32_e64 v70, 0, 1.0, vcc
	v_pk_fma_f32 v[66:67], v[66:67], v[100:101], v[70:71] op_sel_hi:[0,1,1] neg_lo:[1,0,0] neg_hi:[1,0,0]
	v_cvt_pk_bf16_f32 v69, v66, v67
	ds_write_b64 v186, v[68:69] offset:2176
	ds_read_b32 v66, v187 offset:232
	v_cmp_eq_u32_e32 vcc, v102, v111
	s_nop 1
	v_cndmask_b32_e64 v68, 0, 1.0, vcc
	v_cmp_eq_u32_e32 vcc, v104, v111
	s_nop 1
	v_cndmask_b32_e64 v69, 0, 1.0, vcc
	v_cmp_eq_u32_e32 vcc, v105, v111
	s_waitcnt lgkmcnt(0)
	v_pk_fma_f32 v[62:63], v[66:67], v[62:63], v[68:69] op_sel_hi:[0,1,1] neg_lo:[1,0,0] neg_hi:[1,0,0]
	v_cvt_pk_bf16_f32 v62, v62, v63
	v_cndmask_b32_e64 v69, 0, 1.0, vcc
	v_cmp_eq_u32_e32 vcc, v106, v111
	s_nop 1
	v_cndmask_b32_e64 v68, 0, 1.0, vcc
	v_pk_fma_f32 v[64:65], v[66:67], v[64:65], v[68:69] op_sel_hi:[0,1,1] neg_lo:[1,0,0] neg_hi:[1,0,0]
	v_cvt_pk_bf16_f32 v63, v64, v65
	ds_write_b64 v186, v[62:63] offset:2720
	ds_read_b32 v62, v187 offset:240
	v_cmp_eq_u32_e32 vcc, v102, v112
	s_nop 1
	v_cndmask_b32_e64 v64, 0, 1.0, vcc
	v_cmp_eq_u32_e32 vcc, v104, v112
	s_nop 1
	v_cndmask_b32_e64 v65, 0, 1.0, vcc
	v_cmp_eq_u32_e32 vcc, v105, v112
	s_waitcnt lgkmcnt(0)
	v_pk_fma_f32 v[54:55], v[62:63], v[54:55], v[64:65] op_sel_hi:[0,1,1] neg_lo:[1,0,0] neg_hi:[1,0,0]
	v_cvt_pk_bf16_f32 v54, v54, v55
	v_cndmask_b32_e64 v65, 0, 1.0, vcc
	v_cmp_eq_u32_e32 vcc, v106, v112
	s_nop 1
	v_cndmask_b32_e64 v64, 0, 1.0, vcc
	v_pk_fma_f32 v[56:57], v[62:63], v[56:57], v[64:65] op_sel_hi:[0,1,1] neg_lo:[1,0,0] neg_hi:[1,0,0]
	v_cvt_pk_bf16_f32 v55, v56, v57
	ds_write_b64 v186, v[54:55] offset:3264
	ds_read_b32 v54, v187 offset:248
	v_cmp_eq_u32_e32 vcc, v102, v113
	s_nop 1
	v_cndmask_b32_e64 v56, 0, 1.0, vcc
	v_cmp_eq_u32_e32 vcc, v104, v113
	s_nop 1
	v_cndmask_b32_e64 v57, 0, 1.0, vcc
	v_cmp_eq_u32_e32 vcc, v105, v113
	s_waitcnt lgkmcnt(0)
	v_pk_fma_f32 v[46:47], v[54:55], v[46:47], v[56:57] op_sel_hi:[0,1,1] neg_lo:[1,0,0] neg_hi:[1,0,0]
	v_cvt_pk_bf16_f32 v46, v46, v47
	v_cndmask_b32_e64 v57, 0, 1.0, vcc
	v_cmp_eq_u32_e32 vcc, v106, v113
	s_nop 1
	v_cndmask_b32_e64 v56, 0, 1.0, vcc
	v_pk_fma_f32 v[48:49], v[54:55], v[48:49], v[56:57] op_sel_hi:[0,1,1] neg_lo:[1,0,0] neg_hi:[1,0,0]
	v_cvt_pk_bf16_f32 v47, v48, v49
	ds_write_b64 v186, v[46:47] offset:3808
	ds_read_b128 v[46:49], v1
	s_waitcnt lgkmcnt(0)
	ds_write_b128 v184, v[46:49]
	ds_read_b128 v[46:49], v1 offset:64
	s_waitcnt lgkmcnt(0)
	ds_write_b128 v184, v[46:49] offset:1024
	ds_read_b128 v[46:49], v1 offset:128
	s_waitcnt lgkmcnt(0)
	ds_write_b128 v184, v[46:49] offset:2048
	ds_read_b128 v[46:49], v1 offset:192
	s_waitcnt lgkmcnt(0)
	ds_write_b128 v184, v[46:49] offset:3072
	s_lshl_b32 s30, s25, 2
	s_mov_b32 s31, s21
	v_lshl_add_u64 v[46:47], v[126:127], 0, s[30:31]
	v_lshl_add_u64 v[48:49], v[128:129], 0, s[30:31]
	v_lshl_add_u64 v[54:55], v[134:135], 0, s[30:31]
	v_lshl_add_u64 v[56:57], v[136:137], 0, s[30:31]
	v_lshl_add_u64 v[62:63], v[138:139], 0, s[30:31]
	v_lshl_add_u64 v[64:65], v[140:141], 0, s[30:31]
	v_lshl_add_u64 v[98:99], v[142:143], 0, s[30:31]
	v_lshl_add_u64 v[100:101], v[144:145], 0, s[30:31]
	global_load_dwordx4 v[90:93], v[46:47], off nt
	global_load_dwordx4 v[82:85], v[48:49], off nt
	global_load_dwordx4 v[78:81], v[54:55], off nt
	global_load_dwordx4 v[70:73], v[56:57], off nt
	global_load_dwordx4 v[66:69], v[62:63], off nt
	s_nop 0
	global_load_dwordx4 v[62:65], v[64:65], off nt
	s_nop 0
	global_load_dwordx4 v[54:57], v[98:99], off nt
	global_load_dwordx4 v[46:49], v[100:101], off nt
	v_mov_b32_e32 v99, v189
	s_waitcnt vmcnt(23)
	s_waitcnt vmcnt(22)
	s_waitcnt vmcnt(21)
	s_waitcnt vmcnt(20)
	s_waitcnt vmcnt(19)
	s_waitcnt vmcnt(18)
	s_waitcnt vmcnt(17)
	s_waitcnt vmcnt(16)
	ds_read_b32 v98, v187 offset:192
	v_add_u32_e32 v102, 1, v99
	v_cmp_eq_u32_e32 vcc, v99, v103
	v_add_u32_e32 v104, 3, v99
	v_add_u32_e32 v105, 2, v99
	v_cndmask_b32_e64 v100, 0, 1.0, vcc
	v_cmp_eq_u32_e32 vcc, v102, v103
	s_nop 1
	v_cndmask_b32_e64 v101, 0, 1.0, vcc
	v_cmp_eq_u32_e32 vcc, v104, v103
	s_waitcnt lgkmcnt(0)
	v_pk_fma_f32 v[94:95], v[98:99], v[94:95], v[100:101] op_sel_hi:[0,1,1] neg_lo:[1,0,0] neg_hi:[1,0,0]
	v_cvt_pk_bf16_f32 v94, v94, v95
	v_cndmask_b32_e64 v101, 0, 1.0, vcc
	v_cmp_eq_u32_e32 vcc, v105, v103
	s_nop 1
	v_cndmask_b32_e64 v100, 0, 1.0, vcc
	v_pk_fma_f32 v[96:97], v[98:99], v[96:97], v[100:101] op_sel_hi:[0,1,1] neg_lo:[1,0,0] neg_hi:[1,0,0]
	v_cvt_pk_bf16_f32 v95, v96, v97
	ds_write_b64 v186, v[94:95]
	ds_read_b32 v94, v187 offset:200
	v_cmp_eq_u32_e32 vcc, v99, v107
	s_nop 1
	v_cndmask_b32_e64 v96, 0, 1.0, vcc
	v_cmp_eq_u32_e32 vcc, v102, v107
	s_nop 1
	v_cndmask_b32_e64 v97, 0, 1.0, vcc
	v_cmp_eq_u32_e32 vcc, v104, v107
	s_waitcnt lgkmcnt(0)
	v_pk_fma_f32 v[86:87], v[94:95], v[86:87], v[96:97] op_sel_hi:[0,1,1] neg_lo:[1,0,0] neg_hi:[1,0,0]
	v_cvt_pk_bf16_f32 v86, v86, v87
	v_cndmask_b32_e64 v97, 0, 1.0, vcc
	v_cmp_eq_u32_e32 vcc, v105, v107
	s_nop 1
	v_cndmask_b32_e64 v96, 0, 1.0, vcc
	v_pk_fma_f32 v[88:89], v[94:95], v[88:89], v[96:97] op_sel_hi:[0,1,1] neg_lo:[1,0,0] neg_hi:[1,0,0]
	v_cvt_pk_bf16_f32 v87, v88, v89
	ds_write_b64 v186, v[86:87] offset:544
	ds_read_b32 v86, v187 offset:208
	v_cmp_eq_u32_e32 vcc, v99, v108
	s_nop 1
	v_cndmask_b32_e64 v88, 0, 1.0, vcc
	v_cmp_eq_u32_e32 vcc, v102, v108
	s_nop 1
	v_cndmask_b32_e64 v89, 0, 1.0, vcc
	v_cmp_eq_u32_e32 vcc, v104, v108
	s_waitcnt lgkmcnt(0)
	v_pk_fma_f32 v[74:75], v[86:87], v[74:75], v[88:89] op_sel_hi:[0,1,1] neg_lo:[1,0,0] neg_hi:[1,0,0]
	v_cvt_pk_bf16_f32 v74, v74, v75
	v_cndmask_b32_e64 v89, 0, 1.0, vcc
	v_cmp_eq_u32_e32 vcc, v105, v108
	s_nop 1
	v_cndmask_b32_e64 v88, 0, 1.0, vcc
	v_pk_fma_f32 v[76:77], v[86:87], v[76:77], v[88:89] op_sel_hi:[0,1,1] neg_lo:[1,0,0] neg_hi:[1,0,0]
	v_cvt_pk_bf16_f32 v75, v76, v77
	ds_write_b64 v186, v[74:75] offset:1088
	ds_read_b32 v74, v187 offset:216
	v_cmp_eq_u32_e32 vcc, v99, v109
	s_nop 1
	v_cndmask_b32_e64 v76, 0, 1.0, vcc
	v_cmp_eq_u32_e32 vcc, v102, v109
	s_nop 1
	v_cndmask_b32_e64 v77, 0, 1.0, vcc
	v_cmp_eq_u32_e32 vcc, v104, v109
	s_waitcnt lgkmcnt(0)
	v_pk_fma_f32 v[58:59], v[74:75], v[58:59], v[76:77] op_sel_hi:[0,1,1] neg_lo:[1,0,0] neg_hi:[1,0,0]
	v_cvt_pk_bf16_f32 v58, v58, v59
	v_cndmask_b32_e64 v77, 0, 1.0, vcc
	v_cmp_eq_u32_e32 vcc, v105, v109
	s_nop 1
	v_cndmask_b32_e64 v76, 0, 1.0, vcc
	v_pk_fma_f32 v[60:61], v[74:75], v[60:61], v[76:77] op_sel_hi:[0,1,1] neg_lo:[1,0,0] neg_hi:[1,0,0]
	v_cvt_pk_bf16_f32 v59, v60, v61
	ds_write_b64 v186, v[58:59] offset:1632
	ds_read_b32 v58, v187 offset:224
	v_cmp_eq_u32_e32 vcc, v99, v110
	s_nop 1
	v_cndmask_b32_e64 v60, 0, 1.0, vcc
	v_cmp_eq_u32_e32 vcc, v102, v110
	s_nop 1
	v_cndmask_b32_e64 v61, 0, 1.0, vcc
	v_cmp_eq_u32_e32 vcc, v104, v110
	s_waitcnt lgkmcnt(0)
	v_pk_fma_f32 v[50:51], v[58:59], v[50:51], v[60:61] op_sel_hi:[0,1,1] neg_lo:[1,0,0] neg_hi:[1,0,0]
	v_cvt_pk_bf16_f32 v50, v50, v51
	v_cndmask_b32_e64 v61, 0, 1.0, vcc
	v_cmp_eq_u32_e32 vcc, v105, v110
	s_nop 1
	v_cndmask_b32_e64 v60, 0, 1.0, vcc
	v_pk_fma_f32 v[52:53], v[58:59], v[52:53], v[60:61] op_sel_hi:[0,1,1] neg_lo:[1,0,0] neg_hi:[1,0,0]
	v_cvt_pk_bf16_f32 v51, v52, v53
	ds_write_b64 v186, v[50:51] offset:2176
	ds_read_b32 v50, v187 offset:232
	v_cmp_eq_u32_e32 vcc, v99, v111
	s_nop 1
	v_cndmask_b32_e64 v52, 0, 1.0, vcc
	v_cmp_eq_u32_e32 vcc, v102, v111
	s_nop 1
	v_cndmask_b32_e64 v53, 0, 1.0, vcc
	v_cmp_eq_u32_e32 vcc, v104, v111
	s_waitcnt lgkmcnt(0)
	v_pk_fma_f32 v[42:43], v[50:51], v[42:43], v[52:53] op_sel_hi:[0,1,1] neg_lo:[1,0,0] neg_hi:[1,0,0]
	v_cvt_pk_bf16_f32 v42, v42, v43
	v_cndmask_b32_e64 v53, 0, 1.0, vcc
	v_cmp_eq_u32_e32 vcc, v105, v111
	s_nop 1
	v_cndmask_b32_e64 v52, 0, 1.0, vcc
	v_pk_fma_f32 v[44:45], v[50:51], v[44:45], v[52:53] op_sel_hi:[0,1,1] neg_lo:[1,0,0] neg_hi:[1,0,0]
	v_cvt_pk_bf16_f32 v43, v44, v45
	ds_write_b64 v186, v[42:43] offset:2720
	ds_read_b32 v42, v187 offset:240
	v_cmp_eq_u32_e32 vcc, v99, v112
	s_nop 1
	v_cndmask_b32_e64 v44, 0, 1.0, vcc
	v_cmp_eq_u32_e32 vcc, v102, v112
	s_nop 1
	v_cndmask_b32_e64 v45, 0, 1.0, vcc
	v_cmp_eq_u32_e32 vcc, v104, v112
	s_waitcnt lgkmcnt(0)
	v_pk_fma_f32 v[38:39], v[42:43], v[38:39], v[44:45] op_sel_hi:[0,1,1] neg_lo:[1,0,0] neg_hi:[1,0,0]
	v_cvt_pk_bf16_f32 v38, v38, v39
	v_cndmask_b32_e64 v45, 0, 1.0, vcc
	v_cmp_eq_u32_e32 vcc, v105, v112
	s_nop 1
	v_cndmask_b32_e64 v44, 0, 1.0, vcc
	v_pk_fma_f32 v[40:41], v[42:43], v[40:41], v[44:45] op_sel_hi:[0,1,1] neg_lo:[1,0,0] neg_hi:[1,0,0]
	v_cvt_pk_bf16_f32 v39, v40, v41
	ds_write_b64 v186, v[38:39] offset:3264
	ds_read_b32 v38, v187 offset:248
	v_cmp_eq_u32_e32 vcc, v99, v113
	s_nop 1
	v_cndmask_b32_e64 v40, 0, 1.0, vcc
	v_cmp_eq_u32_e32 vcc, v102, v113
	s_nop 1
	v_cndmask_b32_e64 v41, 0, 1.0, vcc
	v_cmp_eq_u32_e32 vcc, v104, v113
	s_waitcnt lgkmcnt(0)
	v_pk_fma_f32 v[34:35], v[38:39], v[34:35], v[40:41] op_sel_hi:[0,1,1] neg_lo:[1,0,0] neg_hi:[1,0,0]
	v_cvt_pk_bf16_f32 v34, v34, v35
	v_cndmask_b32_e64 v41, 0, 1.0, vcc
	v_cmp_eq_u32_e32 vcc, v105, v113
	s_nop 1
	v_cndmask_b32_e64 v40, 0, 1.0, vcc
	v_pk_fma_f32 v[36:37], v[38:39], v[36:37], v[40:41] op_sel_hi:[0,1,1] neg_lo:[1,0,0] neg_hi:[1,0,0]
	v_cvt_pk_bf16_f32 v35, v36, v37
	ds_write_b64 v186, v[34:35] offset:3808
	ds_read_b128 v[34:37], v1
	s_waitcnt lgkmcnt(0)
	ds_write_b128 v184, v[34:37] offset:4096
	ds_read_b128 v[34:37], v1 offset:64
	s_waitcnt lgkmcnt(0)
	ds_write_b128 v184, v[34:37] offset:5120
	ds_read_b128 v[34:37], v1 offset:128
	s_waitcnt lgkmcnt(0)
	ds_write_b128 v184, v[34:37] offset:6144
	ds_read_b128 v[34:37], v1 offset:192
	s_waitcnt lgkmcnt(0)
	ds_write_b128 v184, v[34:37] offset:7168
	s_lshl_b32 s28, s24, 2
	s_mov_b32 s29, s21
	v_lshl_add_u64 v[34:35], v[126:127], 0, s[28:29]
	v_lshl_add_u64 v[36:37], v[128:129], 0, s[28:29]
	v_lshl_add_u64 v[38:39], v[134:135], 0, s[28:29]
	v_lshl_add_u64 v[40:41], v[136:137], 0, s[28:29]
	v_lshl_add_u64 v[42:43], v[138:139], 0, s[28:29]
	v_lshl_add_u64 v[44:45], v[140:141], 0, s[28:29]
	v_lshl_add_u64 v[50:51], v[142:143], 0, s[28:29]
	v_lshl_add_u64 v[52:53], v[144:145], 0, s[28:29]
	global_load_dwordx4 v[122:125], v[34:35], off nt
	global_load_dwordx4 v[114:117], v[36:37], off nt
	global_load_dwordx4 v[106:109], v[38:39], off nt
	global_load_dwordx4 v[86:89], v[40:41], off nt
	global_load_dwordx4 v[74:77], v[42:43], off nt
	s_nop 0
	global_load_dwordx4 v[42:45], v[44:45], off nt
	s_nop 0
	global_load_dwordx4 v[38:41], v[50:51], off nt
	global_load_dwordx4 v[34:37], v[52:53], off nt
	v_mov_b32_e32 v50, v188
	s_waitcnt vmcnt(23)
	s_waitcnt vmcnt(22)
	s_waitcnt vmcnt(21)
	s_waitcnt vmcnt(20)
	s_waitcnt vmcnt(19)
	s_waitcnt vmcnt(18)
	s_waitcnt vmcnt(17)
	s_waitcnt vmcnt(16)
	ds_read_b32 v50, v187 offset:192
	s_waitcnt lgkmcnt(0)
	v_pk_fma_f32 v[30:31], v[50:51], v[30:31], 0 op_sel_hi:[0,1,0] neg_lo:[1,0,0] neg_hi:[1,0,0]
	v_pk_fma_f32 v[32:33], v[50:51], v[32:33], 0 op_sel_hi:[0,1,0] neg_lo:[1,0,0] neg_hi:[1,0,0]
	v_cvt_pk_bf16_f32 v30, v30, v31
	v_cvt_pk_bf16_f32 v31, v32, v33
	ds_write_b64 v186, v[30:31]
	ds_read_b32 v30, v187 offset:200
	s_waitcnt lgkmcnt(0)
	v_pk_fma_f32 v[26:27], v[30:31], v[26:27], 0 op_sel_hi:[0,1,0] neg_lo:[1,0,0] neg_hi:[1,0,0]
	v_pk_fma_f32 v[28:29], v[30:31], v[28:29], 0 op_sel_hi:[0,1,0] neg_lo:[1,0,0] neg_hi:[1,0,0]
	v_cvt_pk_bf16_f32 v26, v26, v27
	v_cvt_pk_bf16_f32 v27, v28, v29
	ds_write_b64 v186, v[26:27] offset:544
	ds_read_b32 v26, v187 offset:208
	s_waitcnt lgkmcnt(0)
	v_pk_fma_f32 v[22:23], v[26:27], v[22:23], 0 op_sel_hi:[0,1,0] neg_lo:[1,0,0] neg_hi:[1,0,0]
	v_pk_fma_f32 v[24:25], v[26:27], v[24:25], 0 op_sel_hi:[0,1,0] neg_lo:[1,0,0] neg_hi:[1,0,0]
	v_cvt_pk_bf16_f32 v22, v22, v23
	v_cvt_pk_bf16_f32 v23, v24, v25
	ds_write_b64 v186, v[22:23] offset:1088
	ds_read_b32 v22, v187 offset:216
	s_waitcnt lgkmcnt(0)
	v_pk_fma_f32 v[18:19], v[22:23], v[18:19], 0 op_sel_hi:[0,1,0] neg_lo:[1,0,0] neg_hi:[1,0,0]
	v_pk_fma_f32 v[20:21], v[22:23], v[20:21], 0 op_sel_hi:[0,1,0] neg_lo:[1,0,0] neg_hi:[1,0,0]
	v_cvt_pk_bf16_f32 v18, v18, v19
	v_cvt_pk_bf16_f32 v19, v20, v21
	ds_write_b64 v186, v[18:19] offset:1632
	ds_read_b32 v18, v187 offset:224
	s_waitcnt lgkmcnt(0)
	v_pk_fma_f32 v[14:15], v[18:19], v[14:15], 0 op_sel_hi:[0,1,0] neg_lo:[1,0,0] neg_hi:[1,0,0]
	v_pk_fma_f32 v[16:17], v[18:19], v[16:17], 0 op_sel_hi:[0,1,0] neg_lo:[1,0,0] neg_hi:[1,0,0]
	v_cvt_pk_bf16_f32 v14, v14, v15
	v_cvt_pk_bf16_f32 v15, v16, v17
	ds_write_b64 v186, v[14:15] offset:2176
	ds_read_b32 v14, v187 offset:232
	s_waitcnt lgkmcnt(0)
	v_pk_fma_f32 v[10:11], v[14:15], v[10:11], 0 op_sel_hi:[0,1,0] neg_lo:[1,0,0] neg_hi:[1,0,0]
	v_pk_fma_f32 v[12:13], v[14:15], v[12:13], 0 op_sel_hi:[0,1,0] neg_lo:[1,0,0] neg_hi:[1,0,0]
	v_cvt_pk_bf16_f32 v10, v10, v11
	v_cvt_pk_bf16_f32 v11, v12, v13
	ds_write_b64 v186, v[10:11] offset:2720
	ds_read_b32 v10, v187 offset:240
	s_waitcnt lgkmcnt(0)
	v_pk_fma_f32 v[6:7], v[10:11], v[6:7], 0 op_sel_hi:[0,1,0] neg_lo:[1,0,0] neg_hi:[1,0,0]
	v_pk_fma_f32 v[8:9], v[10:11], v[8:9], 0 op_sel_hi:[0,1,0] neg_lo:[1,0,0] neg_hi:[1,0,0]
	v_cvt_pk_bf16_f32 v6, v6, v7
	v_cvt_pk_bf16_f32 v7, v8, v9
	ds_write_b64 v186, v[6:7] offset:3264
	ds_read_b32 v6, v187 offset:248
	s_waitcnt lgkmcnt(0)
	v_pk_fma_f32 v[2:3], v[6:7], v[2:3], 0 op_sel_hi:[0,1,0] neg_lo:[1,0,0] neg_hi:[1,0,0]
	v_pk_fma_f32 v[4:5], v[6:7], v[4:5], 0 op_sel_hi:[0,1,0] neg_lo:[1,0,0] neg_hi:[1,0,0]
	v_cvt_pk_bf16_f32 v2, v2, v3
	v_cvt_pk_bf16_f32 v3, v4, v5
	ds_write_b64 v186, v[2:3] offset:3808
	ds_read_b128 v[2:5], v1
	s_waitcnt lgkmcnt(0)
	ds_write_b128 v184, v[2:5] offset:8192
	ds_read_b128 v[2:5], v1 offset:64
	s_waitcnt lgkmcnt(0)
	ds_write_b128 v184, v[2:5] offset:9216
	ds_read_b128 v[2:5], v1 offset:128
	s_waitcnt lgkmcnt(0)
	ds_write_b128 v184, v[2:5] offset:10240
	ds_read_b128 v[2:5], v1 offset:192
	s_waitcnt lgkmcnt(0)
	ds_write_b128 v184, v[2:5] offset:11264
	s_lshl_b32 s26, s23, 2
	s_mov_b32 s27, s21
	v_lshl_add_u64 v[2:3], v[126:127], 0, s[26:27]
	v_lshl_add_u64 v[4:5], v[128:129], 0, s[26:27]
	v_lshl_add_u64 v[6:7], v[134:135], 0, s[26:27]
	v_lshl_add_u64 v[8:9], v[136:137], 0, s[26:27]
	v_lshl_add_u64 v[10:11], v[138:139], 0, s[26:27]
	v_lshl_add_u64 v[12:13], v[140:141], 0, s[26:27]
	v_lshl_add_u64 v[14:15], v[142:143], 0, s[26:27]
	v_lshl_add_u64 v[16:17], v[144:145], 0, s[26:27]
	global_load_dwordx4 v[118:121], v[2:3], off nt
	global_load_dwordx4 v[110:113], v[4:5], off nt
	global_load_dwordx4 v[102:105], v[6:7], off nt
	global_load_dwordx4 v[98:101], v[8:9], off nt
	global_load_dwordx4 v[58:61], v[10:11], off nt
	global_load_dwordx4 v[50:53], v[12:13], off nt
	global_load_dwordx4 v[30:33], v[14:15], off nt
	global_load_dwordx4 v[22:25], v[16:17], off nt
	v_mov_b32_e32 v2, v198
	s_waitcnt vmcnt(23)
	s_waitcnt vmcnt(22)
	s_waitcnt vmcnt(21)
	s_waitcnt vmcnt(20)
	s_waitcnt vmcnt(19)
	s_waitcnt vmcnt(18)
	s_waitcnt vmcnt(17)
	s_waitcnt vmcnt(16)
	ds_read_b32 v2, v187 offset:192
	s_waitcnt lgkmcnt(0)
	v_pk_fma_f32 v[4:5], v[2:3], v[90:91], 0 op_sel_hi:[0,1,0] neg_lo:[1,0,0] neg_hi:[1,0,0]
	v_pk_fma_f32 v[2:3], v[2:3], v[92:93], 0 op_sel_hi:[0,1,0] neg_lo:[1,0,0] neg_hi:[1,0,0]
	v_cvt_pk_bf16_f32 v4, v4, v5
	v_cvt_pk_bf16_f32 v5, v2, v3
	ds_write_b64 v186, v[4:5]
	ds_read_b32 v2, v187 offset:200
	s_waitcnt lgkmcnt(0)
	v_pk_fma_f32 v[4:5], v[2:3], v[82:83], 0 op_sel_hi:[0,1,0] neg_lo:[1,0,0] neg_hi:[1,0,0]
	v_pk_fma_f32 v[2:3], v[2:3], v[84:85], 0 op_sel_hi:[0,1,0] neg_lo:[1,0,0] neg_hi:[1,0,0]
	v_cvt_pk_bf16_f32 v4, v4, v5
	v_cvt_pk_bf16_f32 v5, v2, v3
	ds_write_b64 v186, v[4:5] offset:544
	ds_read_b32 v2, v187 offset:208
	s_waitcnt lgkmcnt(0)
	v_pk_fma_f32 v[4:5], v[2:3], v[78:79], 0 op_sel_hi:[0,1,0] neg_lo:[1,0,0] neg_hi:[1,0,0]
	v_pk_fma_f32 v[2:3], v[2:3], v[80:81], 0 op_sel_hi:[0,1,0] neg_lo:[1,0,0] neg_hi:[1,0,0]
	v_cvt_pk_bf16_f32 v4, v4, v5
	v_cvt_pk_bf16_f32 v5, v2, v3
	ds_write_b64 v186, v[4:5] offset:1088
	ds_read_b32 v2, v187 offset:216
	s_waitcnt lgkmcnt(0)
	v_pk_fma_f32 v[4:5], v[2:3], v[70:71], 0 op_sel_hi:[0,1,0] neg_lo:[1,0,0] neg_hi:[1,0,0]
	v_pk_fma_f32 v[2:3], v[2:3], v[72:73], 0 op_sel_hi:[0,1,0] neg_lo:[1,0,0] neg_hi:[1,0,0]
	v_cvt_pk_bf16_f32 v4, v4, v5
	v_cvt_pk_bf16_f32 v5, v2, v3
	ds_write_b64 v186, v[4:5] offset:1632
	ds_read_b32 v2, v187 offset:224
	s_waitcnt lgkmcnt(0)
	v_pk_fma_f32 v[4:5], v[2:3], v[66:67], 0 op_sel_hi:[0,1,0] neg_lo:[1,0,0] neg_hi:[1,0,0]
	v_pk_fma_f32 v[2:3], v[2:3], v[68:69], 0 op_sel_hi:[0,1,0] neg_lo:[1,0,0] neg_hi:[1,0,0]
	v_cvt_pk_bf16_f32 v4, v4, v5
	v_cvt_pk_bf16_f32 v5, v2, v3
	ds_write_b64 v186, v[4:5] offset:2176
	ds_read_b32 v2, v187 offset:232
	s_waitcnt lgkmcnt(0)
	v_pk_fma_f32 v[4:5], v[2:3], v[62:63], 0 op_sel_hi:[0,1,0] neg_lo:[1,0,0] neg_hi:[1,0,0]
	v_pk_fma_f32 v[2:3], v[2:3], v[64:65], 0 op_sel_hi:[0,1,0] neg_lo:[1,0,0] neg_hi:[1,0,0]
	v_cvt_pk_bf16_f32 v4, v4, v5
	v_cvt_pk_bf16_f32 v5, v2, v3
	ds_write_b64 v186, v[4:5] offset:2720
	ds_read_b32 v2, v187 offset:240
	s_waitcnt lgkmcnt(0)
	v_pk_fma_f32 v[4:5], v[2:3], v[54:55], 0 op_sel_hi:[0,1,0] neg_lo:[1,0,0] neg_hi:[1,0,0]
	v_pk_fma_f32 v[2:3], v[2:3], v[56:57], 0 op_sel_hi:[0,1,0] neg_lo:[1,0,0] neg_hi:[1,0,0]
	v_cvt_pk_bf16_f32 v4, v4, v5
	v_cvt_pk_bf16_f32 v5, v2, v3
	ds_write_b64 v186, v[4:5] offset:3264
	ds_read_b32 v2, v187 offset:248
	s_waitcnt lgkmcnt(0)
	v_pk_fma_f32 v[4:5], v[2:3], v[46:47], 0 op_sel_hi:[0,1,0] neg_lo:[1,0,0] neg_hi:[1,0,0]
	v_pk_fma_f32 v[2:3], v[2:3], v[48:49], 0 op_sel_hi:[0,1,0] neg_lo:[1,0,0] neg_hi:[1,0,0]
	v_cvt_pk_bf16_f32 v4, v4, v5
	v_cvt_pk_bf16_f32 v5, v2, v3
	ds_write_b64 v186, v[4:5] offset:3808
	ds_read_b128 v[2:5], v1
	s_waitcnt lgkmcnt(0)
	ds_write_b128 v184, v[2:5] offset:12288
	ds_read_b128 v[2:5], v1 offset:64
	s_waitcnt lgkmcnt(0)
	ds_write_b128 v184, v[2:5] offset:13312
	ds_read_b128 v[2:5], v1 offset:128
	s_waitcnt lgkmcnt(0)
	ds_write_b128 v184, v[2:5] offset:14336
	ds_read_b128 v[2:5], v1 offset:192
	s_waitcnt lgkmcnt(0)
	ds_write_b128 v184, v[2:5] offset:15360
	s_lshl_b32 s24, s22, 2
	s_mov_b32 s25, s21
	v_lshl_add_u64 v[2:3], v[126:127], 0, s[24:25]
	v_lshl_add_u64 v[6:7], v[134:135], 0, s[24:25]
	v_lshl_add_u64 v[8:9], v[136:137], 0, s[24:25]
	v_lshl_add_u64 v[14:15], v[142:143], 0, s[24:25]
	v_lshl_add_u64 v[4:5], v[128:129], 0, s[24:25]
	v_lshl_add_u64 v[10:11], v[138:139], 0, s[24:25]
	v_lshl_add_u64 v[12:13], v[140:141], 0, s[24:25]
	v_lshl_add_u64 v[18:19], v[144:145], 0, s[24:25]
	global_load_dwordx4 v[94:97], v[2:3], off nt
	global_load_dwordx4 v[90:93], v[4:5], off nt
	global_load_dwordx4 v[82:85], v[6:7], off nt
	global_load_dwordx4 v[70:73], v[8:9], off nt
	global_load_dwordx4 v[54:57], v[10:11], off nt
	global_load_dwordx4 v[26:29], v[12:13], off nt
	s_nop 0
	global_load_dwordx4 v[14:17], v[14:15], off nt
	s_nop 0
	global_load_dwordx4 v[6:9], v[18:19], off nt
	v_mov_b32_e32 v2, v197
	s_waitcnt vmcnt(23)
	s_waitcnt vmcnt(22)
	s_waitcnt vmcnt(21)
	s_waitcnt vmcnt(20)
	s_waitcnt vmcnt(19)
	s_waitcnt vmcnt(18)
	s_waitcnt vmcnt(17)
	s_waitcnt vmcnt(16)
	ds_read_b32 v2, v187 offset:192
	s_waitcnt lgkmcnt(0)
	v_pk_fma_f32 v[4:5], v[2:3], v[122:123], 0 op_sel_hi:[0,1,0] neg_lo:[1,0,0] neg_hi:[1,0,0]
	v_pk_fma_f32 v[2:3], v[2:3], v[124:125], 0 op_sel_hi:[0,1,0] neg_lo:[1,0,0] neg_hi:[1,0,0]
	v_cvt_pk_bf16_f32 v4, v4, v5
	v_cvt_pk_bf16_f32 v5, v2, v3
	ds_write_b64 v186, v[4:5]
	ds_read_b32 v2, v187 offset:200
	s_waitcnt lgkmcnt(0)
	v_pk_fma_f32 v[4:5], v[2:3], v[114:115], 0 op_sel_hi:[0,1,0] neg_lo:[1,0,0] neg_hi:[1,0,0]
	v_pk_fma_f32 v[2:3], v[2:3], v[116:117], 0 op_sel_hi:[0,1,0] neg_lo:[1,0,0] neg_hi:[1,0,0]
	v_cvt_pk_bf16_f32 v4, v4, v5
	v_cvt_pk_bf16_f32 v5, v2, v3
	ds_write_b64 v186, v[4:5] offset:544
	ds_read_b32 v2, v187 offset:208
	s_waitcnt lgkmcnt(0)
	v_pk_fma_f32 v[4:5], v[2:3], v[106:107], 0 op_sel_hi:[0,1,0] neg_lo:[1,0,0] neg_hi:[1,0,0]
	v_pk_fma_f32 v[2:3], v[2:3], v[108:109], 0 op_sel_hi:[0,1,0] neg_lo:[1,0,0] neg_hi:[1,0,0]
	v_cvt_pk_bf16_f32 v4, v4, v5
	v_cvt_pk_bf16_f32 v5, v2, v3
	ds_write_b64 v186, v[4:5] offset:1088
	ds_read_b32 v2, v187 offset:216
	s_waitcnt lgkmcnt(0)
	v_pk_fma_f32 v[4:5], v[2:3], v[86:87], 0 op_sel_hi:[0,1,0] neg_lo:[1,0,0] neg_hi:[1,0,0]
	v_pk_fma_f32 v[2:3], v[2:3], v[88:89], 0 op_sel_hi:[0,1,0] neg_lo:[1,0,0] neg_hi:[1,0,0]
	v_cvt_pk_bf16_f32 v4, v4, v5
	v_cvt_pk_bf16_f32 v5, v2, v3
	ds_write_b64 v186, v[4:5] offset:1632
	ds_read_b32 v2, v187 offset:224
	s_waitcnt lgkmcnt(0)
	v_pk_fma_f32 v[4:5], v[2:3], v[74:75], 0 op_sel_hi:[0,1,0] neg_lo:[1,0,0] neg_hi:[1,0,0]
	v_pk_fma_f32 v[2:3], v[2:3], v[76:77], 0 op_sel_hi:[0,1,0] neg_lo:[1,0,0] neg_hi:[1,0,0]
	v_cvt_pk_bf16_f32 v4, v4, v5
	v_cvt_pk_bf16_f32 v5, v2, v3
	ds_write_b64 v186, v[4:5] offset:2176
	ds_read_b32 v2, v187 offset:232
	s_waitcnt lgkmcnt(0)
	v_pk_fma_f32 v[4:5], v[2:3], v[42:43], 0 op_sel_hi:[0,1,0] neg_lo:[1,0,0] neg_hi:[1,0,0]
	v_pk_fma_f32 v[2:3], v[2:3], v[44:45], 0 op_sel_hi:[0,1,0] neg_lo:[1,0,0] neg_hi:[1,0,0]
	v_cvt_pk_bf16_f32 v4, v4, v5
	v_cvt_pk_bf16_f32 v5, v2, v3
	ds_write_b64 v186, v[4:5] offset:2720
	ds_read_b32 v2, v187 offset:240
	s_waitcnt lgkmcnt(0)
	v_pk_fma_f32 v[4:5], v[2:3], v[38:39], 0 op_sel_hi:[0,1,0] neg_lo:[1,0,0] neg_hi:[1,0,0]
	v_pk_fma_f32 v[2:3], v[2:3], v[40:41], 0 op_sel_hi:[0,1,0] neg_lo:[1,0,0] neg_hi:[1,0,0]
	v_cvt_pk_bf16_f32 v4, v4, v5
	v_cvt_pk_bf16_f32 v5, v2, v3
	ds_write_b64 v186, v[4:5] offset:3264
	ds_read_b32 v2, v187 offset:248
	s_waitcnt lgkmcnt(0)
	v_pk_fma_f32 v[4:5], v[2:3], v[34:35], 0 op_sel_hi:[0,1,0] neg_lo:[1,0,0] neg_hi:[1,0,0]
	v_pk_fma_f32 v[2:3], v[2:3], v[36:37], 0 op_sel_hi:[0,1,0] neg_lo:[1,0,0] neg_hi:[1,0,0]
	v_cvt_pk_bf16_f32 v4, v4, v5
	v_cvt_pk_bf16_f32 v5, v2, v3
	ds_write_b64 v186, v[4:5] offset:3808
	ds_read_b128 v[2:5], v1
	s_waitcnt lgkmcnt(0)
	ds_write_b128 v184, v[2:5] offset:16384
	ds_read_b128 v[2:5], v1 offset:64
	s_waitcnt lgkmcnt(0)
	ds_write_b128 v184, v[2:5] offset:17408
	ds_read_b128 v[2:5], v1 offset:128
	s_waitcnt lgkmcnt(0)
	ds_write_b128 v184, v[2:5] offset:18432
	ds_read_b128 v[2:5], v1 offset:192
	s_waitcnt lgkmcnt(0)
	ds_write_b128 v184, v[2:5] offset:19456
	s_lshl_b32 s22, s7, 2
	s_mov_b32 s23, s21
	v_lshl_add_u64 v[2:3], v[126:127], 0, s[22:23]
	v_lshl_add_u64 v[4:5], v[128:129], 0, s[22:23]
	v_lshl_add_u64 v[10:11], v[134:135], 0, s[22:23]
	v_lshl_add_u64 v[12:13], v[136:137], 0, s[22:23]
	v_lshl_add_u64 v[34:35], v[138:139], 0, s[22:23]
	v_lshl_add_u64 v[36:37], v[140:141], 0, s[22:23]
	v_lshl_add_u64 v[46:47], v[142:143], 0, s[22:23]
	v_lshl_add_u64 v[48:49], v[144:145], 0, s[22:23]
	global_load_dwordx4 v[86:89], v[2:3], off nt
	global_load_dwordx4 v[78:81], v[4:5], off nt
	global_load_dwordx4 v[66:69], v[10:11], off nt
	global_load_dwordx4 v[42:45], v[12:13], off nt
	global_load_dwordx4 v[38:41], v[34:35], off nt
	global_load_dwordx4 v[18:21], v[36:37], off nt
	s_nop 0
	global_load_dwordx4 v[10:13], v[46:47], off nt
	global_load_dwordx4 v[2:5], v[48:49], off nt
	v_mov_b32_e32 v34, v196
	s_waitcnt vmcnt(23)
	s_waitcnt vmcnt(22)
	s_waitcnt vmcnt(21)
	s_waitcnt vmcnt(20)
	s_waitcnt vmcnt(19)
	s_waitcnt vmcnt(18)
	s_waitcnt vmcnt(17)
	s_waitcnt vmcnt(16)
	ds_read_b32 v34, v187 offset:192
	s_waitcnt lgkmcnt(0)
	v_pk_fma_f32 v[36:37], v[34:35], v[118:119], 0 op_sel_hi:[0,1,0] neg_lo:[1,0,0] neg_hi:[1,0,0]
	v_pk_fma_f32 v[34:35], v[34:35], v[120:121], 0 op_sel_hi:[0,1,0] neg_lo:[1,0,0] neg_hi:[1,0,0]
	v_cvt_pk_bf16_f32 v36, v36, v37
	v_cvt_pk_bf16_f32 v37, v34, v35
	ds_write_b64 v186, v[36:37]
	ds_read_b32 v34, v187 offset:200
	s_waitcnt lgkmcnt(0)
	v_pk_fma_f32 v[36:37], v[34:35], v[110:111], 0 op_sel_hi:[0,1,0] neg_lo:[1,0,0] neg_hi:[1,0,0]
	v_pk_fma_f32 v[34:35], v[34:35], v[112:113], 0 op_sel_hi:[0,1,0] neg_lo:[1,0,0] neg_hi:[1,0,0]
	v_cvt_pk_bf16_f32 v36, v36, v37
	v_cvt_pk_bf16_f32 v37, v34, v35
	ds_write_b64 v186, v[36:37] offset:544
	ds_read_b32 v34, v187 offset:208
	s_waitcnt lgkmcnt(0)
	v_pk_fma_f32 v[36:37], v[34:35], v[102:103], 0 op_sel_hi:[0,1,0] neg_lo:[1,0,0] neg_hi:[1,0,0]
	v_pk_fma_f32 v[34:35], v[34:35], v[104:105], 0 op_sel_hi:[0,1,0] neg_lo:[1,0,0] neg_hi:[1,0,0]
	v_cvt_pk_bf16_f32 v36, v36, v37
	v_cvt_pk_bf16_f32 v37, v34, v35
	ds_write_b64 v186, v[36:37] offset:1088
	ds_read_b32 v34, v187 offset:216
	s_waitcnt lgkmcnt(0)
	v_pk_fma_f32 v[36:37], v[34:35], v[98:99], 0 op_sel_hi:[0,1,0] neg_lo:[1,0,0] neg_hi:[1,0,0]
	v_pk_fma_f32 v[34:35], v[34:35], v[100:101], 0 op_sel_hi:[0,1,0] neg_lo:[1,0,0] neg_hi:[1,0,0]
	v_cvt_pk_bf16_f32 v36, v36, v37
	v_cvt_pk_bf16_f32 v37, v34, v35
	ds_write_b64 v186, v[36:37] offset:1632
	ds_read_b32 v34, v187 offset:224
	s_waitcnt lgkmcnt(0)
	v_pk_fma_f32 v[36:37], v[34:35], v[58:59], 0 op_sel_hi:[0,1,0] neg_lo:[1,0,0] neg_hi:[1,0,0]
	v_pk_fma_f32 v[34:35], v[34:35], v[60:61], 0 op_sel_hi:[0,1,0] neg_lo:[1,0,0] neg_hi:[1,0,0]
	v_cvt_pk_bf16_f32 v36, v36, v37
	v_cvt_pk_bf16_f32 v37, v34, v35
	ds_write_b64 v186, v[36:37] offset:2176
	ds_read_b32 v34, v187 offset:232
	s_waitcnt lgkmcnt(0)
	v_pk_fma_f32 v[36:37], v[34:35], v[50:51], 0 op_sel_hi:[0,1,0] neg_lo:[1,0,0] neg_hi:[1,0,0]
	v_pk_fma_f32 v[34:35], v[34:35], v[52:53], 0 op_sel_hi:[0,1,0] neg_lo:[1,0,0] neg_hi:[1,0,0]
	v_cvt_pk_bf16_f32 v36, v36, v37
	v_cvt_pk_bf16_f32 v37, v34, v35
	ds_write_b64 v186, v[36:37] offset:2720
	ds_read_b32 v34, v187 offset:240
	s_waitcnt lgkmcnt(0)
	v_pk_fma_f32 v[30:31], v[34:35], v[30:31], 0 op_sel_hi:[0,1,0] neg_lo:[1,0,0] neg_hi:[1,0,0]
	v_pk_fma_f32 v[32:33], v[34:35], v[32:33], 0 op_sel_hi:[0,1,0] neg_lo:[1,0,0] neg_hi:[1,0,0]
	v_cvt_pk_bf16_f32 v30, v30, v31
	v_cvt_pk_bf16_f32 v31, v32, v33
	ds_write_b64 v186, v[30:31] offset:3264
	ds_read_b32 v30, v187 offset:248
	s_waitcnt lgkmcnt(0)
	v_pk_fma_f32 v[22:23], v[30:31], v[22:23], 0 op_sel_hi:[0,1,0] neg_lo:[1,0,0] neg_hi:[1,0,0]
	v_pk_fma_f32 v[24:25], v[30:31], v[24:25], 0 op_sel_hi:[0,1,0] neg_lo:[1,0,0] neg_hi:[1,0,0]
	v_cvt_pk_bf16_f32 v22, v22, v23
	v_cvt_pk_bf16_f32 v23, v24, v25
	ds_write_b64 v186, v[22:23] offset:3808
	ds_read_b128 v[22:25], v1
	s_waitcnt lgkmcnt(0)
	ds_write_b128 v184, v[22:25] offset:20480
	ds_read_b128 v[22:25], v1 offset:64
	s_waitcnt lgkmcnt(0)
	ds_write_b128 v184, v[22:25] offset:21504
	ds_read_b128 v[22:25], v1 offset:128
	s_waitcnt lgkmcnt(0)
	ds_write_b128 v184, v[22:25] offset:22528
	ds_read_b128 v[22:25], v1 offset:192
	s_waitcnt lgkmcnt(0)
	ds_write_b128 v184, v[22:25] offset:23552
	v_lshl_add_u64 v[22:23], v[130:131], 0, s[30:31]
	s_movk_i32 s7, 0x2000
	v_add_co_u32_e32 v24, vcc, s7, v22
	s_movk_i32 s36, 0x4000
	s_nop 0
	v_addc_co_u32_e32 v25, vcc, 0, v23, vcc
	global_load_dwordx4 v[74:77], v[22:23], off nt
	global_load_dwordx4 v[62:65], v[24:25], off nt
	v_add_co_u32_e32 v24, vcc, s36, v22
	s_movk_i32 s37, 0x6000
	s_nop 0
	v_addc_co_u32_e32 v25, vcc, 0, v23, vcc
	v_add_co_u32_e32 v30, vcc, s37, v22
	s_mov_b32 s38, 0x8000
	s_nop 0
	v_addc_co_u32_e32 v31, vcc, 0, v23, vcc
	global_load_dwordx4 v[58:61], v[24:25], off nt
	global_load_dwordx4 v[46:49], v[30:31], off nt
	v_add_co_u32_e32 v24, vcc, s38, v22
	s_mov_b32 s39, 0xa000
	s_nop 0
	v_addc_co_u32_e32 v25, vcc, 0, v23, vcc
	v_add_co_u32_e32 v34, vcc, s39, v22
	s_mov_b32 s41, 0xc000
	s_nop 0
	v_addc_co_u32_e32 v35, vcc, 0, v23, vcc
	global_load_dwordx4 v[50:53], v[24:25], off nt
	global_load_dwordx4 v[30:33], v[34:35], off nt
	v_add_co_u32_e32 v24, vcc, s41, v22
	s_mov_b32 s42, 0xe000
	s_nop 0
	v_addc_co_u32_e32 v25, vcc, 0, v23, vcc
	v_add_co_u32_e32 v22, vcc, s42, v22
	s_nop 1
	v_addc_co_u32_e32 v23, vcc, 0, v23, vcc
	global_load_dwordx4 v[34:37], v[24:25], off nt
	s_nop 0
	global_load_dwordx4 v[22:25], v[22:23], off nt
	v_mov_b32_e32 v98, v195
	s_waitcnt vmcnt(23)
	s_waitcnt vmcnt(22)
	s_waitcnt vmcnt(21)
	s_waitcnt vmcnt(20)
	s_waitcnt vmcnt(19)
	s_waitcnt vmcnt(18)
	s_waitcnt vmcnt(17)
	s_waitcnt vmcnt(16)
	ds_read_b32 v98, v187 offset:192
	s_waitcnt lgkmcnt(0)
	v_pk_fma_f32 v[94:95], v[98:99], v[94:95], 0 op_sel_hi:[0,1,0] neg_lo:[1,0,0] neg_hi:[1,0,0]
	v_pk_fma_f32 v[96:97], v[98:99], v[96:97], 0 op_sel_hi:[0,1,0] neg_lo:[1,0,0] neg_hi:[1,0,0]
	v_cvt_pk_bf16_f32 v94, v94, v95
	v_cvt_pk_bf16_f32 v95, v96, v97
	ds_write_b64 v186, v[94:95]
	ds_read_b32 v94, v187 offset:200
	s_waitcnt lgkmcnt(0)
	v_pk_fma_f32 v[90:91], v[94:95], v[90:91], 0 op_sel_hi:[0,1,0] neg_lo:[1,0,0] neg_hi:[1,0,0]
	v_pk_fma_f32 v[92:93], v[94:95], v[92:93], 0 op_sel_hi:[0,1,0] neg_lo:[1,0,0] neg_hi:[1,0,0]
	v_cvt_pk_bf16_f32 v90, v90, v91
	v_cvt_pk_bf16_f32 v91, v92, v93
	ds_write_b64 v186, v[90:91] offset:544
	ds_read_b32 v90, v187 offset:208
	s_waitcnt lgkmcnt(0)
	v_pk_fma_f32 v[82:83], v[90:91], v[82:83], 0 op_sel_hi:[0,1,0] neg_lo:[1,0,0] neg_hi:[1,0,0]
	v_pk_fma_f32 v[84:85], v[90:91], v[84:85], 0 op_sel_hi:[0,1,0] neg_lo:[1,0,0] neg_hi:[1,0,0]
	v_cvt_pk_bf16_f32 v82, v82, v83
	v_cvt_pk_bf16_f32 v83, v84, v85
	ds_write_b64 v186, v[82:83] offset:1088
	ds_read_b32 v82, v187 offset:216
	s_waitcnt lgkmcnt(0)
	v_pk_fma_f32 v[70:71], v[82:83], v[70:71], 0 op_sel_hi:[0,1,0] neg_lo:[1,0,0] neg_hi:[1,0,0]
	v_pk_fma_f32 v[72:73], v[82:83], v[72:73], 0 op_sel_hi:[0,1,0] neg_lo:[1,0,0] neg_hi:[1,0,0]
	v_cvt_pk_bf16_f32 v70, v70, v71
	v_cvt_pk_bf16_f32 v71, v72, v73
	ds_write_b64 v186, v[70:71] offset:1632
	ds_read_b32 v70, v187 offset:224
	s_waitcnt lgkmcnt(0)
	v_pk_fma_f32 v[54:55], v[70:71], v[54:55], 0 op_sel_hi:[0,1,0] neg_lo:[1,0,0] neg_hi:[1,0,0]
	v_pk_fma_f32 v[56:57], v[70:71], v[56:57], 0 op_sel_hi:[0,1,0] neg_lo:[1,0,0] neg_hi:[1,0,0]
	v_cvt_pk_bf16_f32 v54, v54, v55
	v_cvt_pk_bf16_f32 v55, v56, v57
	ds_write_b64 v186, v[54:55] offset:2176
	ds_read_b32 v54, v187 offset:232
	s_waitcnt lgkmcnt(0)
	v_pk_fma_f32 v[26:27], v[54:55], v[26:27], 0 op_sel_hi:[0,1,0] neg_lo:[1,0,0] neg_hi:[1,0,0]
	v_pk_fma_f32 v[28:29], v[54:55], v[28:29], 0 op_sel_hi:[0,1,0] neg_lo:[1,0,0] neg_hi:[1,0,0]
	v_cvt_pk_bf16_f32 v26, v26, v27
	v_cvt_pk_bf16_f32 v27, v28, v29
	ds_write_b64 v186, v[26:27] offset:2720
	ds_read_b32 v26, v187 offset:240
	s_waitcnt lgkmcnt(0)
	v_pk_fma_f32 v[14:15], v[26:27], v[14:15], 0 op_sel_hi:[0,1,0] neg_lo:[1,0,0] neg_hi:[1,0,0]
	v_pk_fma_f32 v[16:17], v[26:27], v[16:17], 0 op_sel_hi:[0,1,0] neg_lo:[1,0,0] neg_hi:[1,0,0]
	v_cvt_pk_bf16_f32 v14, v14, v15
	v_cvt_pk_bf16_f32 v15, v16, v17
	ds_write_b64 v186, v[14:15] offset:3264
	ds_read_b32 v14, v187 offset:248
	s_waitcnt lgkmcnt(0)
	v_pk_fma_f32 v[6:7], v[14:15], v[6:7], 0 op_sel_hi:[0,1,0] neg_lo:[1,0,0] neg_hi:[1,0,0]
	v_pk_fma_f32 v[8:9], v[14:15], v[8:9], 0 op_sel_hi:[0,1,0] neg_lo:[1,0,0] neg_hi:[1,0,0]
	v_cvt_pk_bf16_f32 v6, v6, v7
	v_cvt_pk_bf16_f32 v7, v8, v9
	ds_write_b64 v186, v[6:7] offset:3808
	ds_read_b128 v[6:9], v1
	s_waitcnt lgkmcnt(0)
	ds_write_b128 v184, v[6:9] offset:24576
	ds_read_b128 v[6:9], v1 offset:64
	s_waitcnt lgkmcnt(0)
	ds_write_b128 v184, v[6:9] offset:25600
	ds_read_b128 v[6:9], v1 offset:128
	s_waitcnt lgkmcnt(0)
	ds_write_b128 v184, v[6:9] offset:26624
	ds_read_b128 v[6:9], v1 offset:192
	s_waitcnt lgkmcnt(0)
	ds_write_b128 v184, v[6:9] offset:27648
	s_mov_b64 s[44:45], 0x10000
	v_lshl_add_u64 v[150:151], v[130:131], 0, s[44:45]
	s_mov_b64 s[44:45], 0x12000
	v_lshl_add_u64 v[152:153], v[130:131], 0, s[44:45]
	s_mov_b64 s[44:45], 0x14000
	v_lshl_add_u64 v[156:157], v[130:131], 0, s[44:45]
	s_mov_b64 s[44:45], 0x16000
	v_lshl_add_u64 v[158:159], v[130:131], 0, s[44:45]
	s_mov_b64 s[44:45], 0x18000
	v_lshl_add_u64 v[160:161], v[130:131], 0, s[44:45]
	s_mov_b64 s[44:45], 0x1a000
	v_lshl_add_u64 v[162:163], v[130:131], 0, s[44:45]
	s_mov_b64 s[44:45], 0x1c000
	v_lshl_add_u64 v[164:165], v[130:131], 0, s[44:45]
	s_mov_b64 s[44:45], 0x1e000
	v_lshl_add_u64 v[6:7], v[150:151], 0, s[30:31]
	v_lshl_add_u64 v[8:9], v[152:153], 0, s[30:31]
	v_lshl_add_u64 v[14:15], v[156:157], 0, s[30:31]
	v_lshl_add_u64 v[16:17], v[158:159], 0, s[30:31]
	v_lshl_add_u64 v[26:27], v[160:161], 0, s[30:31]
	v_lshl_add_u64 v[28:29], v[162:163], 0, s[30:31]
	v_lshl_add_u64 v[166:167], v[130:131], 0, s[44:45]
	v_lshl_add_u64 v[98:99], v[164:165], 0, s[30:31]
	v_lshl_add_u64 v[100:101], v[166:167], 0, s[30:31]
	global_load_dwordx4 v[94:97], v[6:7], off nt
	global_load_dwordx4 v[90:93], v[8:9], off nt
	global_load_dwordx4 v[82:85], v[14:15], off nt
	global_load_dwordx4 v[70:73], v[16:17], off nt
	global_load_dwordx4 v[54:57], v[26:27], off nt
	s_nop 0
	global_load_dwordx4 v[26:29], v[28:29], off nt
	s_nop 0
	global_load_dwordx4 v[14:17], v[98:99], off nt
	global_load_dwordx4 v[6:9], v[100:101], off nt
	v_mov_b32_e32 v98, v194
	s_waitcnt vmcnt(23)
	s_waitcnt vmcnt(22)
	s_waitcnt vmcnt(21)
	s_waitcnt vmcnt(20)
	s_waitcnt vmcnt(19)
	s_waitcnt vmcnt(18)
	s_waitcnt vmcnt(17)
	s_waitcnt vmcnt(16)
	ds_read_b32 v98, v187 offset:192
	s_waitcnt lgkmcnt(0)
	v_pk_fma_f32 v[86:87], v[98:99], v[86:87], 0 op_sel_hi:[0,1,0] neg_lo:[1,0,0] neg_hi:[1,0,0]
	v_pk_fma_f32 v[88:89], v[98:99], v[88:89], 0 op_sel_hi:[0,1,0] neg_lo:[1,0,0] neg_hi:[1,0,0]
	v_cvt_pk_bf16_f32 v86, v86, v87
	v_cvt_pk_bf16_f32 v87, v88, v89
	ds_write_b64 v186, v[86:87]
	ds_read_b32 v86, v187 offset:200
	s_waitcnt lgkmcnt(0)
	v_pk_fma_f32 v[78:79], v[86:87], v[78:79], 0 op_sel_hi:[0,1,0] neg_lo:[1,0,0] neg_hi:[1,0,0]
	v_pk_fma_f32 v[80:81], v[86:87], v[80:81], 0 op_sel_hi:[0,1,0] neg_lo:[1,0,0] neg_hi:[1,0,0]
	v_cvt_pk_bf16_f32 v78, v78, v79
	v_cvt_pk_bf16_f32 v79, v80, v81
	ds_write_b64 v186, v[78:79] offset:544
	ds_read_b32 v78, v187 offset:208
	s_waitcnt lgkmcnt(0)
	v_pk_fma_f32 v[66:67], v[78:79], v[66:67], 0 op_sel_hi:[0,1,0] neg_lo:[1,0,0] neg_hi:[1,0,0]
	v_pk_fma_f32 v[68:69], v[78:79], v[68:69], 0 op_sel_hi:[0,1,0] neg_lo:[1,0,0] neg_hi:[1,0,0]
	v_cvt_pk_bf16_f32 v66, v66, v67
	v_cvt_pk_bf16_f32 v67, v68, v69
	ds_write_b64 v186, v[66:67] offset:1088
	ds_read_b32 v66, v187 offset:216
	s_waitcnt lgkmcnt(0)
	v_pk_fma_f32 v[42:43], v[66:67], v[42:43], 0 op_sel_hi:[0,1,0] neg_lo:[1,0,0] neg_hi:[1,0,0]
	v_pk_fma_f32 v[44:45], v[66:67], v[44:45], 0 op_sel_hi:[0,1,0] neg_lo:[1,0,0] neg_hi:[1,0,0]
	v_cvt_pk_bf16_f32 v42, v42, v43
	v_cvt_pk_bf16_f32 v43, v44, v45
	ds_write_b64 v186, v[42:43] offset:1632
	ds_read_b32 v42, v187 offset:224
	s_waitcnt lgkmcnt(0)
	v_pk_fma_f32 v[38:39], v[42:43], v[38:39], 0 op_sel_hi:[0,1,0] neg_lo:[1,0,0] neg_hi:[1,0,0]
	v_pk_fma_f32 v[40:41], v[42:43], v[40:41], 0 op_sel_hi:[0,1,0] neg_lo:[1,0,0] neg_hi:[1,0,0]
	v_cvt_pk_bf16_f32 v38, v38, v39
	v_cvt_pk_bf16_f32 v39, v40, v41
	ds_write_b64 v186, v[38:39] offset:2176
	ds_read_b32 v38, v187 offset:232
	s_waitcnt lgkmcnt(0)
	v_pk_fma_f32 v[18:19], v[38:39], v[18:19], 0 op_sel_hi:[0,1,0] neg_lo:[1,0,0] neg_hi:[1,0,0]
	v_pk_fma_f32 v[20:21], v[38:39], v[20:21], 0 op_sel_hi:[0,1,0] neg_lo:[1,0,0] neg_hi:[1,0,0]
	v_cvt_pk_bf16_f32 v18, v18, v19
	v_cvt_pk_bf16_f32 v19, v20, v21
	ds_write_b64 v186, v[18:19] offset:2720
	ds_read_b32 v18, v187 offset:240
	s_waitcnt lgkmcnt(0)
	v_pk_fma_f32 v[10:11], v[18:19], v[10:11], 0 op_sel_hi:[0,1,0] neg_lo:[1,0,0] neg_hi:[1,0,0]
	v_pk_fma_f32 v[12:13], v[18:19], v[12:13], 0 op_sel_hi:[0,1,0] neg_lo:[1,0,0] neg_hi:[1,0,0]
	v_cvt_pk_bf16_f32 v10, v10, v11
	v_cvt_pk_bf16_f32 v11, v12, v13
	ds_write_b64 v186, v[10:11] offset:3264
	ds_read_b32 v10, v187 offset:248
	s_waitcnt lgkmcnt(0)
	v_pk_fma_f32 v[2:3], v[10:11], v[2:3], 0 op_sel_hi:[0,1,0] neg_lo:[1,0,0] neg_hi:[1,0,0]
	v_pk_fma_f32 v[4:5], v[10:11], v[4:5], 0 op_sel_hi:[0,1,0] neg_lo:[1,0,0] neg_hi:[1,0,0]
	v_cvt_pk_bf16_f32 v2, v2, v3
	v_cvt_pk_bf16_f32 v3, v4, v5
	ds_write_b64 v186, v[2:3] offset:3808
	ds_read_b128 v[2:5], v1
	s_waitcnt lgkmcnt(0)
	ds_write_b128 v184, v[2:5] offset:28672
	ds_read_b128 v[2:5], v1 offset:64
	s_waitcnt lgkmcnt(0)
	ds_write_b128 v184, v[2:5] offset:29696
	ds_read_b128 v[2:5], v1 offset:128
	s_waitcnt lgkmcnt(0)
	ds_write_b128 v184, v[2:5] offset:30720
	ds_read_b128 v[2:5], v1 offset:192
	s_waitcnt lgkmcnt(0)
	ds_write_b128 v184, v[2:5] offset:31744
	s_mov_b64 s[44:45], 0x20000
	v_lshl_add_u64 v[168:169], v[130:131], 0, s[44:45]
	s_mov_b64 s[44:45], 0x22000
	v_lshl_add_u64 v[170:171], v[130:131], 0, s[44:45]
	s_mov_b64 s[44:45], 0x24000
	v_lshl_add_u64 v[172:173], v[130:131], 0, s[44:45]
	s_mov_b64 s[44:45], 0x26000
	v_lshl_add_u64 v[174:175], v[130:131], 0, s[44:45]
	s_mov_b64 s[44:45], 0x28000
	v_lshl_add_u64 v[176:177], v[130:131], 0, s[44:45]
	s_mov_b64 s[44:45], 0x2a000
	v_lshl_add_u64 v[178:179], v[130:131], 0, s[44:45]
	s_mov_b64 s[44:45], 0x2c000
	v_lshl_add_u64 v[180:181], v[130:131], 0, s[44:45]
	s_mov_b64 s[44:45], 0x2e000
	v_lshl_add_u64 v[2:3], v[168:169], 0, s[30:31]
	v_lshl_add_u64 v[4:5], v[170:171], 0, s[30:31]
	v_lshl_add_u64 v[10:11], v[172:173], 0, s[30:31]
	v_lshl_add_u64 v[12:13], v[174:175], 0, s[30:31]
	v_lshl_add_u64 v[18:19], v[176:177], 0, s[30:31]
	v_lshl_add_u64 v[20:21], v[178:179], 0, s[30:31]
	v_lshl_add_u64 v[182:183], v[130:131], 0, s[44:45]
	v_lshl_add_u64 v[42:43], v[180:181], 0, s[30:31]
	v_lshl_add_u64 v[44:45], v[182:183], 0, s[30:31]
	global_load_dwordx4 v[106:109], v[2:3], off nt
	global_load_dwordx4 v[98:101], v[4:5], off nt
	global_load_dwordx4 v[78:81], v[10:11], off nt
	global_load_dwordx4 v[66:69], v[12:13], off nt
	global_load_dwordx4 v[38:41], v[18:19], off nt
	s_nop 0
	global_load_dwordx4 v[18:21], v[20:21], off nt
	s_nop 0
	global_load_dwordx4 v[10:13], v[42:43], off nt
	global_load_dwordx4 v[2:5], v[44:45], off nt
	v_mov_b32_e32 v42, v198
	s_waitcnt vmcnt(23)
	s_waitcnt vmcnt(22)
	s_waitcnt vmcnt(21)
	s_waitcnt vmcnt(20)
	s_waitcnt vmcnt(19)
	s_waitcnt vmcnt(18)
	s_waitcnt vmcnt(17)
	s_waitcnt vmcnt(16)
	ds_read_b32 v42, v187
	s_waitcnt lgkmcnt(0)
	v_pk_fma_f32 v[44:45], v[42:43], v[74:75], 0 op_sel_hi:[0,1,0] neg_lo:[1,0,0] neg_hi:[1,0,0]
	v_pk_fma_f32 v[42:43], v[42:43], v[76:77], 0 op_sel_hi:[0,1,0] neg_lo:[1,0,0] neg_hi:[1,0,0]
	v_cvt_pk_bf16_f32 v44, v44, v45
	v_cvt_pk_bf16_f32 v45, v42, v43
	ds_write_b64 v186, v[44:45]
	ds_read_b32 v42, v187 offset:8
	s_waitcnt lgkmcnt(0)
	v_pk_fma_f32 v[44:45], v[42:43], v[62:63], 0 op_sel_hi:[0,1,0] neg_lo:[1,0,0] neg_hi:[1,0,0]
	v_pk_fma_f32 v[42:43], v[42:43], v[64:65], 0 op_sel_hi:[0,1,0] neg_lo:[1,0,0] neg_hi:[1,0,0]
	v_cvt_pk_bf16_f32 v44, v44, v45
	v_cvt_pk_bf16_f32 v45, v42, v43
	ds_write_b64 v186, v[44:45] offset:544
	ds_read_b32 v42, v187 offset:16
	s_waitcnt lgkmcnt(0)
	v_pk_fma_f32 v[44:45], v[42:43], v[58:59], 0 op_sel_hi:[0,1,0] neg_lo:[1,0,0] neg_hi:[1,0,0]
	v_pk_fma_f32 v[42:43], v[42:43], v[60:61], 0 op_sel_hi:[0,1,0] neg_lo:[1,0,0] neg_hi:[1,0,0]
	v_cvt_pk_bf16_f32 v44, v44, v45
	v_cvt_pk_bf16_f32 v45, v42, v43
	ds_write_b64 v186, v[44:45] offset:1088
	ds_read_b32 v42, v187 offset:24
	s_waitcnt lgkmcnt(0)
	v_pk_fma_f32 v[44:45], v[42:43], v[46:47], 0 op_sel_hi:[0,1,0] neg_lo:[1,0,0] neg_hi:[1,0,0]
	v_pk_fma_f32 v[42:43], v[42:43], v[48:49], 0 op_sel_hi:[0,1,0] neg_lo:[1,0,0] neg_hi:[1,0,0]
	v_cvt_pk_bf16_f32 v44, v44, v45
	v_cvt_pk_bf16_f32 v45, v42, v43
	ds_write_b64 v186, v[44:45] offset:1632
	ds_read_b32 v42, v187 offset:32
	s_waitcnt lgkmcnt(0)
	v_pk_fma_f32 v[44:45], v[42:43], v[50:51], 0 op_sel_hi:[0,1,0] neg_lo:[1,0,0] neg_hi:[1,0,0]
	v_pk_fma_f32 v[42:43], v[42:43], v[52:53], 0 op_sel_hi:[0,1,0] neg_lo:[1,0,0] neg_hi:[1,0,0]
	v_cvt_pk_bf16_f32 v44, v44, v45
	v_cvt_pk_bf16_f32 v45, v42, v43
	ds_write_b64 v186, v[44:45] offset:2176
	ds_read_b32 v42, v187 offset:40
	s_waitcnt lgkmcnt(0)
	v_pk_fma_f32 v[30:31], v[42:43], v[30:31], 0 op_sel_hi:[0,1,0] neg_lo:[1,0,0] neg_hi:[1,0,0]
	v_pk_fma_f32 v[32:33], v[42:43], v[32:33], 0 op_sel_hi:[0,1,0] neg_lo:[1,0,0] neg_hi:[1,0,0]
	v_cvt_pk_bf16_f32 v30, v30, v31
	v_cvt_pk_bf16_f32 v31, v32, v33
	ds_write_b64 v186, v[30:31] offset:2720
	ds_read_b32 v30, v187 offset:48
	s_waitcnt lgkmcnt(0)
	v_pk_fma_f32 v[32:33], v[30:31], v[34:35], 0 op_sel_hi:[0,1,0] neg_lo:[1,0,0] neg_hi:[1,0,0]
	v_pk_fma_f32 v[30:31], v[30:31], v[36:37], 0 op_sel_hi:[0,1,0] neg_lo:[1,0,0] neg_hi:[1,0,0]
	v_cvt_pk_bf16_f32 v32, v32, v33
	v_cvt_pk_bf16_f32 v33, v30, v31
	ds_write_b64 v186, v[32:33] offset:3264
	ds_read_b32 v30, v187 offset:56
	s_waitcnt lgkmcnt(0)
	v_pk_fma_f32 v[22:23], v[30:31], v[22:23], 0 op_sel_hi:[0,1,0] neg_lo:[1,0,0] neg_hi:[1,0,0]
	v_pk_fma_f32 v[24:25], v[30:31], v[24:25], 0 op_sel_hi:[0,1,0] neg_lo:[1,0,0] neg_hi:[1,0,0]
	v_cvt_pk_bf16_f32 v22, v22, v23
	v_cvt_pk_bf16_f32 v23, v24, v25
	ds_write_b64 v186, v[22:23] offset:3808
	ds_read_b128 a[0:3], v1
	ds_read_b128 a[4:7], v1 offset:64
	ds_read_b128 a[8:11], v1 offset:128
	ds_read_b128 a[12:15], v1 offset:192
	v_lshl_add_u64 v[22:23], v[130:131], 0, s[28:29]
	v_add_co_u32_e32 v24, vcc, s7, v22
	s_nop 1
	v_addc_co_u32_e32 v25, vcc, 0, v23, vcc
	global_load_dwordx4 v[102:105], v[22:23], off nt
	global_load_dwordx4 v[86:89], v[24:25], off nt
	v_add_co_u32_e32 v24, vcc, s36, v22
	s_nop 1
	v_addc_co_u32_e32 v25, vcc, 0, v23, vcc
	v_add_co_u32_e32 v30, vcc, s37, v22
	s_nop 1
	v_addc_co_u32_e32 v31, vcc, 0, v23, vcc
	global_load_dwordx4 v[74:77], v[24:25], off nt
	global_load_dwordx4 v[62:65], v[30:31], off nt
	v_add_co_u32_e32 v24, vcc, s38, v22
	s_nop 1
	v_addc_co_u32_e32 v25, vcc, 0, v23, vcc
	v_add_co_u32_e32 v30, vcc, s39, v22
	s_nop 1
	v_addc_co_u32_e32 v31, vcc, 0, v23, vcc
	global_load_dwordx4 v[58:61], v[24:25], off nt
	global_load_dwordx4 v[46:49], v[30:31], off nt
	v_add_co_u32_e32 v24, vcc, s41, v22
	s_nop 1
	v_addc_co_u32_e32 v25, vcc, 0, v23, vcc
	v_add_co_u32_e32 v22, vcc, s42, v22
	s_nop 1
	v_addc_co_u32_e32 v23, vcc, 0, v23, vcc
	global_load_dwordx4 v[42:45], v[24:25], off nt
	global_load_dwordx4 v[30:33], v[22:23], off nt
	v_mov_b32_e32 v22, v198
	s_waitcnt vmcnt(23)
	s_waitcnt vmcnt(22)
	s_waitcnt vmcnt(21)
	s_waitcnt vmcnt(20)
	s_waitcnt vmcnt(19)
	s_waitcnt vmcnt(18)
	s_waitcnt vmcnt(17)
	s_waitcnt vmcnt(16)
	ds_read_b32 v22, v187 offset:64
	s_waitcnt lgkmcnt(0)
	v_pk_fma_f32 v[24:25], v[22:23], v[94:95], 0 op_sel_hi:[0,1,0] neg_lo:[1,0,0] neg_hi:[1,0,0]
	v_pk_fma_f32 v[22:23], v[22:23], v[96:97], 0 op_sel_hi:[0,1,0] neg_lo:[1,0,0] neg_hi:[1,0,0]
	v_cvt_pk_bf16_f32 v24, v24, v25
	v_cvt_pk_bf16_f32 v25, v22, v23
	ds_write_b64 v186, v[24:25]
	ds_read_b32 v22, v187 offset:72
	s_waitcnt lgkmcnt(0)
	v_pk_fma_f32 v[24:25], v[22:23], v[90:91], 0 op_sel_hi:[0,1,0] neg_lo:[1,0,0] neg_hi:[1,0,0]
	v_pk_fma_f32 v[22:23], v[22:23], v[92:93], 0 op_sel_hi:[0,1,0] neg_lo:[1,0,0] neg_hi:[1,0,0]
	v_cvt_pk_bf16_f32 v24, v24, v25
	v_cvt_pk_bf16_f32 v25, v22, v23
	ds_write_b64 v186, v[24:25] offset:544
	ds_read_b32 v22, v187 offset:80
	s_waitcnt lgkmcnt(0)
	v_pk_fma_f32 v[24:25], v[22:23], v[82:83], 0 op_sel_hi:[0,1,0] neg_lo:[1,0,0] neg_hi:[1,0,0]
	v_pk_fma_f32 v[22:23], v[22:23], v[84:85], 0 op_sel_hi:[0,1,0] neg_lo:[1,0,0] neg_hi:[1,0,0]
	v_cvt_pk_bf16_f32 v24, v24, v25
	v_cvt_pk_bf16_f32 v25, v22, v23
	ds_write_b64 v186, v[24:25] offset:1088
	ds_read_b32 v22, v187 offset:88
	s_waitcnt lgkmcnt(0)
	v_pk_fma_f32 v[24:25], v[22:23], v[70:71], 0 op_sel_hi:[0,1,0] neg_lo:[1,0,0] neg_hi:[1,0,0]
	v_pk_fma_f32 v[22:23], v[22:23], v[72:73], 0 op_sel_hi:[0,1,0] neg_lo:[1,0,0] neg_hi:[1,0,0]
	v_cvt_pk_bf16_f32 v24, v24, v25
	v_cvt_pk_bf16_f32 v25, v22, v23
	ds_write_b64 v186, v[24:25] offset:1632
	ds_read_b32 v22, v187 offset:96
	s_waitcnt lgkmcnt(0)
	v_pk_fma_f32 v[24:25], v[22:23], v[54:55], 0 op_sel_hi:[0,1,0] neg_lo:[1,0,0] neg_hi:[1,0,0]
	v_pk_fma_f32 v[22:23], v[22:23], v[56:57], 0 op_sel_hi:[0,1,0] neg_lo:[1,0,0] neg_hi:[1,0,0]
	v_cvt_pk_bf16_f32 v24, v24, v25
	v_cvt_pk_bf16_f32 v25, v22, v23
	ds_write_b64 v186, v[24:25] offset:2176
	ds_read_b32 v22, v187 offset:104
	s_waitcnt lgkmcnt(0)
	v_pk_fma_f32 v[24:25], v[22:23], v[26:27], 0 op_sel_hi:[0,1,0] neg_lo:[1,0,0] neg_hi:[1,0,0]
	v_pk_fma_f32 v[22:23], v[22:23], v[28:29], 0 op_sel_hi:[0,1,0] neg_lo:[1,0,0] neg_hi:[1,0,0]
	v_cvt_pk_bf16_f32 v24, v24, v25
	v_cvt_pk_bf16_f32 v25, v22, v23
	ds_write_b64 v186, v[24:25] offset:2720
	ds_read_b32 v22, v187 offset:112
	s_waitcnt lgkmcnt(0)
	v_pk_fma_f32 v[14:15], v[22:23], v[14:15], 0 op_sel_hi:[0,1,0] neg_lo:[1,0,0] neg_hi:[1,0,0]
	v_pk_fma_f32 v[16:17], v[22:23], v[16:17], 0 op_sel_hi:[0,1,0] neg_lo:[1,0,0] neg_hi:[1,0,0]
	v_cvt_pk_bf16_f32 v14, v14, v15
	v_cvt_pk_bf16_f32 v15, v16, v17
	ds_write_b64 v186, v[14:15] offset:3264
	ds_read_b32 v14, v187 offset:120
	s_waitcnt lgkmcnt(0)
	v_pk_fma_f32 v[6:7], v[14:15], v[6:7], 0 op_sel_hi:[0,1,0] neg_lo:[1,0,0] neg_hi:[1,0,0]
	v_pk_fma_f32 v[8:9], v[14:15], v[8:9], 0 op_sel_hi:[0,1,0] neg_lo:[1,0,0] neg_hi:[1,0,0]
	v_cvt_pk_bf16_f32 v6, v6, v7
	v_cvt_pk_bf16_f32 v7, v8, v9
	ds_write_b64 v186, v[6:7] offset:3808
	ds_read_b128 a[16:19], v1
	ds_read_b128 a[20:23], v1 offset:64
	ds_read_b128 a[24:27], v1 offset:128
	ds_read_b128 a[28:31], v1 offset:192
	v_lshl_add_u64 v[6:7], v[150:151], 0, s[28:29]
	v_lshl_add_u64 v[8:9], v[152:153], 0, s[28:29]
	v_lshl_add_u64 v[14:15], v[156:157], 0, s[28:29]
	v_lshl_add_u64 v[16:17], v[158:159], 0, s[28:29]
	v_lshl_add_u64 v[22:23], v[160:161], 0, s[28:29]
	v_lshl_add_u64 v[24:25], v[162:163], 0, s[28:29]
	v_lshl_add_u64 v[26:27], v[164:165], 0, s[28:29]
	v_lshl_add_u64 v[28:29], v[166:167], 0, s[28:29]
	global_load_dwordx4 v[110:113], v[6:7], off nt
	global_load_dwordx4 v[90:93], v[8:9], off nt
	global_load_dwordx4 v[70:73], v[14:15], off nt
	global_load_dwordx4 v[50:53], v[16:17], off nt
	global_load_dwordx4 v[34:37], v[22:23], off nt
	s_nop 0
	global_load_dwordx4 v[22:25], v[24:25], off nt
	s_nop 0
	global_load_dwordx4 v[14:17], v[26:27], off nt
	global_load_dwordx4 v[6:9], v[28:29], off nt
	s_waitcnt vmcnt(23)
	s_waitcnt vmcnt(22)
	s_waitcnt vmcnt(21)
	s_waitcnt vmcnt(20)
	s_waitcnt vmcnt(19)
	s_waitcnt vmcnt(18)
	s_waitcnt vmcnt(17)
	s_waitcnt vmcnt(16)
	ds_read_b32 v26, v187 offset:128
	s_waitcnt lgkmcnt(0)
	v_pk_fma_f32 v[28:29], v[26:27], v[106:107], 0 op_sel_hi:[0,1,0] neg_lo:[1,0,0] neg_hi:[1,0,0]
	v_pk_fma_f32 v[26:27], v[26:27], v[108:109], 0 op_sel_hi:[0,1,0] neg_lo:[1,0,0] neg_hi:[1,0,0]
	v_cvt_pk_bf16_f32 v28, v28, v29
	v_cvt_pk_bf16_f32 v29, v26, v27
	ds_write_b64 v186, v[28:29]
	ds_read_b32 v26, v187 offset:136
	s_waitcnt lgkmcnt(0)
	v_pk_fma_f32 v[28:29], v[26:27], v[98:99], 0 op_sel_hi:[0,1,0] neg_lo:[1,0,0] neg_hi:[1,0,0]
	v_pk_fma_f32 v[26:27], v[26:27], v[100:101], 0 op_sel_hi:[0,1,0] neg_lo:[1,0,0] neg_hi:[1,0,0]
	v_cvt_pk_bf16_f32 v28, v28, v29
	v_cvt_pk_bf16_f32 v29, v26, v27
	ds_write_b64 v186, v[28:29] offset:544
	ds_read_b32 v26, v187 offset:144
	s_waitcnt lgkmcnt(0)
	v_pk_fma_f32 v[28:29], v[26:27], v[78:79], 0 op_sel_hi:[0,1,0] neg_lo:[1,0,0] neg_hi:[1,0,0]
	v_pk_fma_f32 v[26:27], v[26:27], v[80:81], 0 op_sel_hi:[0,1,0] neg_lo:[1,0,0] neg_hi:[1,0,0]
	v_cvt_pk_bf16_f32 v28, v28, v29
	v_cvt_pk_bf16_f32 v29, v26, v27
	ds_write_b64 v186, v[28:29] offset:1088
	ds_read_b32 v26, v187 offset:152
	s_waitcnt lgkmcnt(0)
	v_pk_fma_f32 v[28:29], v[26:27], v[66:67], 0 op_sel_hi:[0,1,0] neg_lo:[1,0,0] neg_hi:[1,0,0]
	v_pk_fma_f32 v[26:27], v[26:27], v[68:69], 0 op_sel_hi:[0,1,0] neg_lo:[1,0,0] neg_hi:[1,0,0]
	v_cvt_pk_bf16_f32 v28, v28, v29
	v_cvt_pk_bf16_f32 v29, v26, v27
	ds_write_b64 v186, v[28:29] offset:1632
	ds_read_b32 v26, v187 offset:160
	s_waitcnt lgkmcnt(0)
	v_pk_fma_f32 v[28:29], v[26:27], v[38:39], 0 op_sel_hi:[0,1,0] neg_lo:[1,0,0] neg_hi:[1,0,0]
	v_pk_fma_f32 v[26:27], v[26:27], v[40:41], 0 op_sel_hi:[0,1,0] neg_lo:[1,0,0] neg_hi:[1,0,0]
	v_cvt_pk_bf16_f32 v28, v28, v29
	v_cvt_pk_bf16_f32 v29, v26, v27
	ds_write_b64 v186, v[28:29] offset:2176
	ds_read_b32 v26, v187 offset:168
	s_waitcnt lgkmcnt(0)
	v_pk_fma_f32 v[18:19], v[26:27], v[18:19], 0 op_sel_hi:[0,1,0] neg_lo:[1,0,0] neg_hi:[1,0,0]
	v_pk_fma_f32 v[20:21], v[26:27], v[20:21], 0 op_sel_hi:[0,1,0] neg_lo:[1,0,0] neg_hi:[1,0,0]
	v_cvt_pk_bf16_f32 v18, v18, v19
	v_cvt_pk_bf16_f32 v19, v20, v21
	ds_write_b64 v186, v[18:19] offset:2720
	ds_read_b32 v18, v187 offset:176
	s_waitcnt lgkmcnt(0)
	v_pk_fma_f32 v[10:11], v[18:19], v[10:11], 0 op_sel_hi:[0,1,0] neg_lo:[1,0,0] neg_hi:[1,0,0]
	v_pk_fma_f32 v[12:13], v[18:19], v[12:13], 0 op_sel_hi:[0,1,0] neg_lo:[1,0,0] neg_hi:[1,0,0]
	v_cvt_pk_bf16_f32 v10, v10, v11
	v_cvt_pk_bf16_f32 v11, v12, v13
	ds_write_b64 v186, v[10:11] offset:3264
	ds_read_b32 v10, v187 offset:184
	s_waitcnt lgkmcnt(0)
	v_pk_fma_f32 v[2:3], v[10:11], v[2:3], 0 op_sel_hi:[0,1,0] neg_lo:[1,0,0] neg_hi:[1,0,0]
	v_pk_fma_f32 v[4:5], v[10:11], v[4:5], 0 op_sel_hi:[0,1,0] neg_lo:[1,0,0] neg_hi:[1,0,0]
	v_cvt_pk_bf16_f32 v2, v2, v3
	v_cvt_pk_bf16_f32 v3, v4, v5
	ds_write_b64 v186, v[2:3] offset:3808
	ds_read_b128 a[32:35], v1
	ds_read_b128 a[36:39], v1 offset:64
	ds_read_b128 a[40:43], v1 offset:128
	ds_read_b128 a[44:47], v1 offset:192
	v_lshl_add_u64 v[2:3], v[168:169], 0, s[28:29]
	v_lshl_add_u64 v[4:5], v[170:171], 0, s[28:29]
	v_lshl_add_u64 v[10:11], v[172:173], 0, s[28:29]
	v_lshl_add_u64 v[12:13], v[174:175], 0, s[28:29]
	v_lshl_add_u64 v[18:19], v[176:177], 0, s[28:29]
	v_lshl_add_u64 v[20:21], v[178:179], 0, s[28:29]
	v_lshl_add_u64 v[26:27], v[180:181], 0, s[28:29]
	v_lshl_add_u64 v[28:29], v[182:183], 0, s[28:29]
	global_load_dwordx4 v[106:109], v[2:3], off nt
	global_load_dwordx4 v[94:97], v[4:5], off nt
	global_load_dwordx4 v[66:69], v[10:11], off nt
	global_load_dwordx4 v[54:57], v[12:13], off nt
	global_load_dwordx4 v[38:41], v[18:19], off nt
	s_nop 0
	global_load_dwordx4 v[18:21], v[20:21], off nt
	s_nop 0
	global_load_dwordx4 v[10:13], v[26:27], off nt
	global_load_dwordx4 v[2:5], v[28:29], off nt
	v_mov_b32_e32 v26, v197
	s_waitcnt vmcnt(23)
	s_waitcnt vmcnt(22)
	s_waitcnt vmcnt(21)
	s_waitcnt vmcnt(20)
	s_waitcnt vmcnt(19)
	s_waitcnt vmcnt(18)
	s_waitcnt vmcnt(17)
	s_waitcnt vmcnt(16)
	ds_read_b32 v26, v187
	s_waitcnt lgkmcnt(0)
	v_pk_fma_f32 v[28:29], v[26:27], v[102:103], 0 op_sel_hi:[0,1,0] neg_lo:[1,0,0] neg_hi:[1,0,0]
	v_pk_fma_f32 v[26:27], v[26:27], v[104:105], 0 op_sel_hi:[0,1,0] neg_lo:[1,0,0] neg_hi:[1,0,0]
	v_cvt_pk_bf16_f32 v28, v28, v29
	v_cvt_pk_bf16_f32 v29, v26, v27
	ds_write_b64 v186, v[28:29]
	ds_read_b32 v26, v187 offset:8
	s_waitcnt lgkmcnt(0)
	v_pk_fma_f32 v[28:29], v[26:27], v[86:87], 0 op_sel_hi:[0,1,0] neg_lo:[1,0,0] neg_hi:[1,0,0]
	v_pk_fma_f32 v[26:27], v[26:27], v[88:89], 0 op_sel_hi:[0,1,0] neg_lo:[1,0,0] neg_hi:[1,0,0]
	v_cvt_pk_bf16_f32 v28, v28, v29
	v_cvt_pk_bf16_f32 v29, v26, v27
	ds_write_b64 v186, v[28:29] offset:544
	ds_read_b32 v26, v187 offset:16
	s_waitcnt lgkmcnt(0)
	v_pk_fma_f32 v[28:29], v[26:27], v[74:75], 0 op_sel_hi:[0,1,0] neg_lo:[1,0,0] neg_hi:[1,0,0]
	v_pk_fma_f32 v[26:27], v[26:27], v[76:77], 0 op_sel_hi:[0,1,0] neg_lo:[1,0,0] neg_hi:[1,0,0]
	v_cvt_pk_bf16_f32 v28, v28, v29
	v_cvt_pk_bf16_f32 v29, v26, v27
	ds_write_b64 v186, v[28:29] offset:1088
	ds_read_b32 v26, v187 offset:24
	s_waitcnt lgkmcnt(0)
	v_pk_fma_f32 v[28:29], v[26:27], v[62:63], 0 op_sel_hi:[0,1,0] neg_lo:[1,0,0] neg_hi:[1,0,0]
	v_pk_fma_f32 v[26:27], v[26:27], v[64:65], 0 op_sel_hi:[0,1,0] neg_lo:[1,0,0] neg_hi:[1,0,0]
	v_cvt_pk_bf16_f32 v28, v28, v29
	v_cvt_pk_bf16_f32 v29, v26, v27
	ds_write_b64 v186, v[28:29] offset:1632
	ds_read_b32 v26, v187 offset:32
	s_waitcnt lgkmcnt(0)
	v_pk_fma_f32 v[28:29], v[26:27], v[58:59], 0 op_sel_hi:[0,1,0] neg_lo:[1,0,0] neg_hi:[1,0,0]
	v_pk_fma_f32 v[26:27], v[26:27], v[60:61], 0 op_sel_hi:[0,1,0] neg_lo:[1,0,0] neg_hi:[1,0,0]
	v_cvt_pk_bf16_f32 v28, v28, v29
	v_cvt_pk_bf16_f32 v29, v26, v27
	ds_write_b64 v186, v[28:29] offset:2176
	ds_read_b32 v26, v187 offset:40
	s_waitcnt lgkmcnt(0)
	v_pk_fma_f32 v[28:29], v[26:27], v[46:47], 0 op_sel_hi:[0,1,0] neg_lo:[1,0,0] neg_hi:[1,0,0]
	v_pk_fma_f32 v[26:27], v[26:27], v[48:49], 0 op_sel_hi:[0,1,0] neg_lo:[1,0,0] neg_hi:[1,0,0]
	v_cvt_pk_bf16_f32 v28, v28, v29
	v_cvt_pk_bf16_f32 v29, v26, v27
	ds_write_b64 v186, v[28:29] offset:2720
	ds_read_b32 v26, v187 offset:48
	s_waitcnt lgkmcnt(0)
	v_pk_fma_f32 v[28:29], v[26:27], v[42:43], 0 op_sel_hi:[0,1,0] neg_lo:[1,0,0] neg_hi:[1,0,0]
	v_pk_fma_f32 v[26:27], v[26:27], v[44:45], 0 op_sel_hi:[0,1,0] neg_lo:[1,0,0] neg_hi:[1,0,0]
	v_cvt_pk_bf16_f32 v28, v28, v29
	v_cvt_pk_bf16_f32 v29, v26, v27
	ds_write_b64 v186, v[28:29] offset:3264
	ds_read_b32 v26, v187 offset:56
	s_waitcnt lgkmcnt(0)
	v_pk_fma_f32 v[28:29], v[26:27], v[30:31], 0 op_sel_hi:[0,1,0] neg_lo:[1,0,0] neg_hi:[1,0,0]
	v_pk_fma_f32 v[26:27], v[26:27], v[32:33], 0 op_sel_hi:[0,1,0] neg_lo:[1,0,0] neg_hi:[1,0,0]
	v_cvt_pk_bf16_f32 v28, v28, v29
	v_cvt_pk_bf16_f32 v29, v26, v27
	ds_write_b64 v186, v[28:29] offset:3808
	ds_read_b128 a[48:51], v1
	ds_read_b128 a[52:55], v1 offset:64
	ds_read_b128 a[56:59], v1 offset:128
	ds_read_b128 a[60:63], v1 offset:192
	v_lshl_add_u64 v[26:27], v[130:131], 0, s[26:27]
	v_add_co_u32_e32 v28, vcc, s7, v26
	s_nop 1
	v_addc_co_u32_e32 v29, vcc, 0, v27, vcc
	global_load_dwordx4 v[86:89], v[26:27], off nt
	global_load_dwordx4 v[82:85], v[28:29], off nt
	v_add_co_u32_e32 v28, vcc, s36, v26
	s_nop 1
	v_addc_co_u32_e32 v29, vcc, 0, v27, vcc
	v_add_co_u32_e32 v30, vcc, s37, v26
	s_nop 1
	v_addc_co_u32_e32 v31, vcc, 0, v27, vcc
	global_load_dwordx4 v[78:81], v[28:29], off nt
	global_load_dwordx4 v[58:61], v[30:31], off nt
	v_add_co_u32_e32 v28, vcc, s38, v26
	s_nop 1
	v_addc_co_u32_e32 v29, vcc, 0, v27, vcc
	v_add_co_u32_e32 v30, vcc, s39, v26
	s_nop 1
	v_addc_co_u32_e32 v31, vcc, 0, v27, vcc
	global_load_dwordx4 v[46:49], v[28:29], off nt
	global_load_dwordx4 v[42:45], v[30:31], off nt
	v_add_co_u32_e32 v28, vcc, s41, v26
	s_nop 1
	v_addc_co_u32_e32 v29, vcc, 0, v27, vcc
	v_add_co_u32_e32 v26, vcc, s42, v26
	s_nop 1
	v_addc_co_u32_e32 v27, vcc, 0, v27, vcc
	global_load_dwordx4 v[30:33], v[28:29], off nt
	s_nop 0
	global_load_dwordx4 v[26:29], v[26:27], off nt
	v_mov_b32_e32 v62, v197
	s_waitcnt vmcnt(23)
	s_waitcnt vmcnt(22)
	s_waitcnt vmcnt(21)
	s_waitcnt vmcnt(20)
	s_waitcnt vmcnt(19)
	s_waitcnt vmcnt(18)
	s_waitcnt vmcnt(17)
	s_waitcnt vmcnt(16)
	ds_read_b32 v62, v187 offset:64
	s_waitcnt lgkmcnt(0)
	v_pk_fma_f32 v[64:65], v[62:63], v[110:111], 0 op_sel_hi:[0,1,0] neg_lo:[1,0,0] neg_hi:[1,0,0]
	v_pk_fma_f32 v[62:63], v[62:63], v[112:113], 0 op_sel_hi:[0,1,0] neg_lo:[1,0,0] neg_hi:[1,0,0]
	v_cvt_pk_bf16_f32 v64, v64, v65
	v_cvt_pk_bf16_f32 v65, v62, v63
	ds_write_b64 v186, v[64:65]
	ds_read_b32 v62, v187 offset:72
	s_waitcnt lgkmcnt(0)
	v_pk_fma_f32 v[64:65], v[62:63], v[90:91], 0 op_sel_hi:[0,1,0] neg_lo:[1,0,0] neg_hi:[1,0,0]
	v_pk_fma_f32 v[62:63], v[62:63], v[92:93], 0 op_sel_hi:[0,1,0] neg_lo:[1,0,0] neg_hi:[1,0,0]
	v_cvt_pk_bf16_f32 v64, v64, v65
	v_cvt_pk_bf16_f32 v65, v62, v63
	ds_write_b64 v186, v[64:65] offset:544
	ds_read_b32 v62, v187 offset:80
	s_waitcnt lgkmcnt(0)
	v_pk_fma_f32 v[64:65], v[62:63], v[70:71], 0 op_sel_hi:[0,1,0] neg_lo:[1,0,0] neg_hi:[1,0,0]
	v_pk_fma_f32 v[62:63], v[62:63], v[72:73], 0 op_sel_hi:[0,1,0] neg_lo:[1,0,0] neg_hi:[1,0,0]
	v_cvt_pk_bf16_f32 v64, v64, v65
	v_cvt_pk_bf16_f32 v65, v62, v63
	ds_write_b64 v186, v[64:65] offset:1088
	ds_read_b32 v62, v187 offset:88
	s_waitcnt lgkmcnt(0)
	v_pk_fma_f32 v[50:51], v[62:63], v[50:51], 0 op_sel_hi:[0,1,0] neg_lo:[1,0,0] neg_hi:[1,0,0]
	v_pk_fma_f32 v[52:53], v[62:63], v[52:53], 0 op_sel_hi:[0,1,0] neg_lo:[1,0,0] neg_hi:[1,0,0]
	v_cvt_pk_bf16_f32 v50, v50, v51
	v_cvt_pk_bf16_f32 v51, v52, v53
	ds_write_b64 v186, v[50:51] offset:1632
	ds_read_b32 v50, v187 offset:96
	s_waitcnt lgkmcnt(0)
	v_pk_fma_f32 v[34:35], v[50:51], v[34:35], 0 op_sel_hi:[0,1,0] neg_lo:[1,0,0] neg_hi:[1,0,0]
	v_pk_fma_f32 v[36:37], v[50:51], v[36:37], 0 op_sel_hi:[0,1,0] neg_lo:[1,0,0] neg_hi:[1,0,0]
	v_cvt_pk_bf16_f32 v34, v34, v35
	v_cvt_pk_bf16_f32 v35, v36, v37
	ds_write_b64 v186, v[34:35] offset:2176
	ds_read_b32 v34, v187 offset:104
	s_waitcnt lgkmcnt(0)
	v_pk_fma_f32 v[22:23], v[34:35], v[22:23], 0 op_sel_hi:[0,1,0] neg_lo:[1,0,0] neg_hi:[1,0,0]
	v_pk_fma_f32 v[24:25], v[34:35], v[24:25], 0 op_sel_hi:[0,1,0] neg_lo:[1,0,0] neg_hi:[1,0,0]
	v_cvt_pk_bf16_f32 v22, v22, v23
	v_cvt_pk_bf16_f32 v23, v24, v25
	ds_write_b64 v186, v[22:23] offset:2720
	ds_read_b32 v22, v187 offset:112
	s_waitcnt lgkmcnt(0)
	v_pk_fma_f32 v[14:15], v[22:23], v[14:15], 0 op_sel_hi:[0,1,0] neg_lo:[1,0,0] neg_hi:[1,0,0]
	v_pk_fma_f32 v[16:17], v[22:23], v[16:17], 0 op_sel_hi:[0,1,0] neg_lo:[1,0,0] neg_hi:[1,0,0]
	v_cvt_pk_bf16_f32 v14, v14, v15
	v_cvt_pk_bf16_f32 v15, v16, v17
	ds_write_b64 v186, v[14:15] offset:3264
	ds_read_b32 v14, v187 offset:120
	s_waitcnt lgkmcnt(0)
	v_pk_fma_f32 v[6:7], v[14:15], v[6:7], 0 op_sel_hi:[0,1,0] neg_lo:[1,0,0] neg_hi:[1,0,0]
	v_pk_fma_f32 v[8:9], v[14:15], v[8:9], 0 op_sel_hi:[0,1,0] neg_lo:[1,0,0] neg_hi:[1,0,0]
	v_cvt_pk_bf16_f32 v6, v6, v7
	v_cvt_pk_bf16_f32 v7, v8, v9
	ds_write_b64 v186, v[6:7] offset:3808
	ds_read_b128 a[64:67], v1
	ds_read_b128 a[68:71], v1 offset:64
	ds_read_b128 a[72:75], v1 offset:128
	ds_read_b128 a[76:79], v1 offset:192
	v_lshl_add_u64 v[6:7], v[150:151], 0, s[26:27]
	v_lshl_add_u64 v[8:9], v[152:153], 0, s[26:27]
	v_lshl_add_u64 v[14:15], v[156:157], 0, s[26:27]
	v_lshl_add_u64 v[16:17], v[158:159], 0, s[26:27]
	v_lshl_add_u64 v[22:23], v[160:161], 0, s[26:27]
	v_lshl_add_u64 v[24:25], v[162:163], 0, s[26:27]
	v_lshl_add_u64 v[70:71], v[164:165], 0, s[26:27]
	v_lshl_add_u64 v[72:73], v[166:167], 0, s[26:27]
	global_load_dwordx4 v[110:113], v[6:7], off nt
	global_load_dwordx4 v[98:101], v[8:9], off nt
	global_load_dwordx4 v[62:65], v[14:15], off nt
	global_load_dwordx4 v[50:53], v[16:17], off nt
	global_load_dwordx4 v[34:37], v[22:23], off nt
	s_nop 0
	global_load_dwordx4 v[22:25], v[24:25], off nt
	s_nop 0
	global_load_dwordx4 v[14:17], v[70:71], off nt
	global_load_dwordx4 v[6:9], v[72:73], off nt
	s_waitcnt vmcnt(23)
	s_waitcnt vmcnt(22)
	s_waitcnt vmcnt(21)
	s_waitcnt vmcnt(20)
	s_waitcnt vmcnt(19)
	s_waitcnt vmcnt(18)
	s_waitcnt vmcnt(17)
	s_waitcnt vmcnt(16)
	ds_read_b32 v70, v187 offset:128
	s_waitcnt lgkmcnt(0)
	v_pk_fma_f32 v[72:73], v[70:71], v[106:107], 0 op_sel_hi:[0,1,0] neg_lo:[1,0,0] neg_hi:[1,0,0]
	v_pk_fma_f32 v[70:71], v[70:71], v[108:109], 0 op_sel_hi:[0,1,0] neg_lo:[1,0,0] neg_hi:[1,0,0]
	v_cvt_pk_bf16_f32 v72, v72, v73
	v_cvt_pk_bf16_f32 v73, v70, v71
	ds_write_b64 v186, v[72:73]
	ds_read_b32 v70, v187 offset:136
	s_waitcnt lgkmcnt(0)
	v_pk_fma_f32 v[72:73], v[70:71], v[94:95], 0 op_sel_hi:[0,1,0] neg_lo:[1,0,0] neg_hi:[1,0,0]
	v_pk_fma_f32 v[70:71], v[70:71], v[96:97], 0 op_sel_hi:[0,1,0] neg_lo:[1,0,0] neg_hi:[1,0,0]
	v_cvt_pk_bf16_f32 v72, v72, v73
	v_cvt_pk_bf16_f32 v73, v70, v71
	ds_write_b64 v186, v[72:73] offset:544
	ds_read_b32 v70, v187 offset:144
	s_waitcnt lgkmcnt(0)
	v_pk_fma_f32 v[66:67], v[70:71], v[66:67], 0 op_sel_hi:[0,1,0] neg_lo:[1,0,0] neg_hi:[1,0,0]
	v_pk_fma_f32 v[68:69], v[70:71], v[68:69], 0 op_sel_hi:[0,1,0] neg_lo:[1,0,0] neg_hi:[1,0,0]
	v_cvt_pk_bf16_f32 v66, v66, v67
	v_cvt_pk_bf16_f32 v67, v68, v69
	ds_write_b64 v186, v[66:67] offset:1088
	ds_read_b32 v66, v187 offset:152
	s_waitcnt lgkmcnt(0)
	v_pk_fma_f32 v[54:55], v[66:67], v[54:55], 0 op_sel_hi:[0,1,0] neg_lo:[1,0,0] neg_hi:[1,0,0]
	v_pk_fma_f32 v[56:57], v[66:67], v[56:57], 0 op_sel_hi:[0,1,0] neg_lo:[1,0,0] neg_hi:[1,0,0]
	v_cvt_pk_bf16_f32 v54, v54, v55
	v_cvt_pk_bf16_f32 v55, v56, v57
	ds_write_b64 v186, v[54:55] offset:1632
	ds_read_b32 v54, v187 offset:160
	s_waitcnt lgkmcnt(0)
	v_pk_fma_f32 v[38:39], v[54:55], v[38:39], 0 op_sel_hi:[0,1,0] neg_lo:[1,0,0] neg_hi:[1,0,0]
	v_pk_fma_f32 v[40:41], v[54:55], v[40:41], 0 op_sel_hi:[0,1,0] neg_lo:[1,0,0] neg_hi:[1,0,0]
	v_cvt_pk_bf16_f32 v38, v38, v39
	v_cvt_pk_bf16_f32 v39, v40, v41
	ds_write_b64 v186, v[38:39] offset:2176
	ds_read_b32 v38, v187 offset:168
	s_waitcnt lgkmcnt(0)
	v_pk_fma_f32 v[18:19], v[38:39], v[18:19], 0 op_sel_hi:[0,1,0] neg_lo:[1,0,0] neg_hi:[1,0,0]
	v_pk_fma_f32 v[20:21], v[38:39], v[20:21], 0 op_sel_hi:[0,1,0] neg_lo:[1,0,0] neg_hi:[1,0,0]
	v_cvt_pk_bf16_f32 v18, v18, v19
	v_cvt_pk_bf16_f32 v19, v20, v21
	ds_write_b64 v186, v[18:19] offset:2720
	ds_read_b32 v18, v187 offset:176
	s_waitcnt lgkmcnt(0)
	v_pk_fma_f32 v[10:11], v[18:19], v[10:11], 0 op_sel_hi:[0,1,0] neg_lo:[1,0,0] neg_hi:[1,0,0]
	v_pk_fma_f32 v[12:13], v[18:19], v[12:13], 0 op_sel_hi:[0,1,0] neg_lo:[1,0,0] neg_hi:[1,0,0]
	v_cvt_pk_bf16_f32 v10, v10, v11
	v_cvt_pk_bf16_f32 v11, v12, v13
	ds_write_b64 v186, v[10:11] offset:3264
	ds_read_b32 v10, v187 offset:184
	s_waitcnt lgkmcnt(0)
	v_pk_fma_f32 v[2:3], v[10:11], v[2:3], 0 op_sel_hi:[0,1,0] neg_lo:[1,0,0] neg_hi:[1,0,0]
	v_pk_fma_f32 v[4:5], v[10:11], v[4:5], 0 op_sel_hi:[0,1,0] neg_lo:[1,0,0] neg_hi:[1,0,0]
	v_cvt_pk_bf16_f32 v2, v2, v3
	v_cvt_pk_bf16_f32 v3, v4, v5
	ds_write_b64 v186, v[2:3] offset:3808
	ds_read_b128 a[80:83], v1
	ds_read_b128 a[84:87], v1 offset:64
	ds_read_b128 a[88:91], v1 offset:128
	ds_read_b128 a[92:95], v1 offset:192
	v_lshl_add_u64 v[2:3], v[168:169], 0, s[26:27]
	v_lshl_add_u64 v[4:5], v[170:171], 0, s[26:27]
	v_lshl_add_u64 v[10:11], v[172:173], 0, s[26:27]
	v_lshl_add_u64 v[12:13], v[174:175], 0, s[26:27]
	v_lshl_add_u64 v[18:19], v[176:177], 0, s[26:27]
	v_lshl_add_u64 v[20:21], v[178:179], 0, s[26:27]
	v_lshl_add_u64 v[66:67], v[180:181], 0, s[26:27]
	v_lshl_add_u64 v[68:69], v[182:183], 0, s[26:27]
	global_load_dwordx4 v[106:109], v[2:3], off nt
	global_load_dwordx4 v[94:97], v[4:5], off nt
	global_load_dwordx4 v[74:77], v[10:11], off nt
	global_load_dwordx4 v[54:57], v[12:13], off nt
	global_load_dwordx4 v[38:41], v[18:19], off nt
	s_nop 0
	global_load_dwordx4 v[18:21], v[20:21], off nt
	s_nop 0
	global_load_dwordx4 v[10:13], v[66:67], off nt
	global_load_dwordx4 v[2:5], v[68:69], off nt
	v_mov_b32_e32 v66, v196
	s_waitcnt vmcnt(23)
	s_waitcnt vmcnt(22)
	s_waitcnt vmcnt(21)
	s_waitcnt vmcnt(20)
	s_waitcnt vmcnt(19)
	s_waitcnt vmcnt(18)
	s_waitcnt vmcnt(17)
	s_waitcnt vmcnt(16)
	ds_read_b32 v66, v187
	s_waitcnt lgkmcnt(0)
	v_pk_fma_f32 v[68:69], v[66:67], v[86:87], 0 op_sel_hi:[0,1,0] neg_lo:[1,0,0] neg_hi:[1,0,0]
	v_pk_fma_f32 v[66:67], v[66:67], v[88:89], 0 op_sel_hi:[0,1,0] neg_lo:[1,0,0] neg_hi:[1,0,0]
	v_cvt_pk_bf16_f32 v68, v68, v69
	v_cvt_pk_bf16_f32 v69, v66, v67
	ds_write_b64 v186, v[68:69]
	ds_read_b32 v66, v187 offset:8
	s_waitcnt lgkmcnt(0)
	v_pk_fma_f32 v[68:69], v[66:67], v[82:83], 0 op_sel_hi:[0,1,0] neg_lo:[1,0,0] neg_hi:[1,0,0]
	v_pk_fma_f32 v[66:67], v[66:67], v[84:85], 0 op_sel_hi:[0,1,0] neg_lo:[1,0,0] neg_hi:[1,0,0]
	v_cvt_pk_bf16_f32 v68, v68, v69
	v_cvt_pk_bf16_f32 v69, v66, v67
	ds_write_b64 v186, v[68:69] offset:544
	ds_read_b32 v66, v187 offset:16
	s_waitcnt lgkmcnt(0)
	v_pk_fma_f32 v[68:69], v[66:67], v[78:79], 0 op_sel_hi:[0,1,0] neg_lo:[1,0,0] neg_hi:[1,0,0]
	v_pk_fma_f32 v[66:67], v[66:67], v[80:81], 0 op_sel_hi:[0,1,0] neg_lo:[1,0,0] neg_hi:[1,0,0]
	v_cvt_pk_bf16_f32 v68, v68, v69
	v_cvt_pk_bf16_f32 v69, v66, v67
	ds_write_b64 v186, v[68:69] offset:1088
	ds_read_b32 v66, v187 offset:24
	s_waitcnt lgkmcnt(0)
	v_pk_fma_f32 v[58:59], v[66:67], v[58:59], 0 op_sel_hi:[0,1,0] neg_lo:[1,0,0] neg_hi:[1,0,0]
	v_pk_fma_f32 v[60:61], v[66:67], v[60:61], 0 op_sel_hi:[0,1,0] neg_lo:[1,0,0] neg_hi:[1,0,0]
	v_cvt_pk_bf16_f32 v58, v58, v59
	v_cvt_pk_bf16_f32 v59, v60, v61
	ds_write_b64 v186, v[58:59] offset:1632
	ds_read_b32 v58, v187 offset:32
	s_waitcnt lgkmcnt(0)
	v_pk_fma_f32 v[46:47], v[58:59], v[46:47], 0 op_sel_hi:[0,1,0] neg_lo:[1,0,0] neg_hi:[1,0,0]
	v_pk_fma_f32 v[48:49], v[58:59], v[48:49], 0 op_sel_hi:[0,1,0] neg_lo:[1,0,0] neg_hi:[1,0,0]
	v_cvt_pk_bf16_f32 v46, v46, v47
	v_cvt_pk_bf16_f32 v47, v48, v49
	ds_write_b64 v186, v[46:47] offset:2176
	ds_read_b32 v46, v187 offset:40
	s_waitcnt lgkmcnt(0)
	v_pk_fma_f32 v[42:43], v[46:47], v[42:43], 0 op_sel_hi:[0,1,0] neg_lo:[1,0,0] neg_hi:[1,0,0]
	v_pk_fma_f32 v[44:45], v[46:47], v[44:45], 0 op_sel_hi:[0,1,0] neg_lo:[1,0,0] neg_hi:[1,0,0]
	v_cvt_pk_bf16_f32 v42, v42, v43
	v_cvt_pk_bf16_f32 v43, v44, v45
	ds_write_b64 v186, v[42:43] offset:2720
	ds_read_b32 v42, v187 offset:48
	s_waitcnt lgkmcnt(0)
	v_pk_fma_f32 v[30:31], v[42:43], v[30:31], 0 op_sel_hi:[0,1,0] neg_lo:[1,0,0] neg_hi:[1,0,0]
	v_pk_fma_f32 v[32:33], v[42:43], v[32:33], 0 op_sel_hi:[0,1,0] neg_lo:[1,0,0] neg_hi:[1,0,0]
	v_cvt_pk_bf16_f32 v30, v30, v31
	v_cvt_pk_bf16_f32 v31, v32, v33
	ds_write_b64 v186, v[30:31] offset:3264
	ds_read_b32 v30, v187 offset:56
	s_waitcnt lgkmcnt(0)
	v_pk_fma_f32 v[26:27], v[30:31], v[26:27], 0 op_sel_hi:[0,1,0] neg_lo:[1,0,0] neg_hi:[1,0,0]
	v_pk_fma_f32 v[28:29], v[30:31], v[28:29], 0 op_sel_hi:[0,1,0] neg_lo:[1,0,0] neg_hi:[1,0,0]
	v_cvt_pk_bf16_f32 v26, v26, v27
	v_cvt_pk_bf16_f32 v27, v28, v29
	ds_write_b64 v186, v[26:27] offset:3808
	ds_read_b128 a[96:99], v1
	ds_read_b128 a[100:103], v1 offset:64
	ds_read_b128 a[104:107], v1 offset:128
	ds_read_b128 a[108:111], v1 offset:192
	v_lshl_add_u64 v[26:27], v[130:131], 0, s[24:25]
	v_add_co_u32_e32 v28, vcc, s7, v26
	s_nop 1
	v_addc_co_u32_e32 v29, vcc, 0, v27, vcc
	global_load_dwordx4 v[102:105], v[26:27], off nt
	global_load_dwordx4 v[90:93], v[28:29], off nt
	v_add_co_u32_e32 v28, vcc, s36, v26
	s_nop 1
	v_addc_co_u32_e32 v29, vcc, 0, v27, vcc
	v_add_co_u32_e32 v30, vcc, s37, v26
	s_nop 1
	v_addc_co_u32_e32 v31, vcc, 0, v27, vcc
	global_load_dwordx4 v[86:89], v[28:29], off nt
	global_load_dwordx4 v[70:73], v[30:31], off nt
	v_add_co_u32_e32 v28, vcc, s38, v26
	s_nop 1
	v_addc_co_u32_e32 v29, vcc, 0, v27, vcc
	v_add_co_u32_e32 v30, vcc, s39, v26
	s_nop 1
	v_addc_co_u32_e32 v31, vcc, 0, v27, vcc
	global_load_dwordx4 v[66:69], v[28:29], off nt
	global_load_dwordx4 v[46:49], v[30:31], off nt
	v_add_co_u32_e32 v28, vcc, s41, v26
	s_nop 1
	v_addc_co_u32_e32 v29, vcc, 0, v27, vcc
	v_add_co_u32_e32 v26, vcc, s42, v26
	s_nop 1
	v_addc_co_u32_e32 v27, vcc, 0, v27, vcc
	global_load_dwordx4 v[42:45], v[28:29], off nt
	global_load_dwordx4 v[30:33], v[26:27], off nt
	v_mov_b32_e32 v26, v196
	s_waitcnt vmcnt(23)
	s_waitcnt vmcnt(22)
	s_waitcnt vmcnt(21)
	s_waitcnt vmcnt(20)
	s_waitcnt vmcnt(19)
	s_waitcnt vmcnt(18)
	s_waitcnt vmcnt(17)
	s_waitcnt vmcnt(16)
	ds_read_b32 v26, v187 offset:64
	s_waitcnt lgkmcnt(0)
	v_pk_fma_f32 v[28:29], v[26:27], v[110:111], 0 op_sel_hi:[0,1,0] neg_lo:[1,0,0] neg_hi:[1,0,0]
	v_pk_fma_f32 v[26:27], v[26:27], v[112:113], 0 op_sel_hi:[0,1,0] neg_lo:[1,0,0] neg_hi:[1,0,0]
	v_cvt_pk_bf16_f32 v28, v28, v29
	v_cvt_pk_bf16_f32 v29, v26, v27
	ds_write_b64 v186, v[28:29]
	ds_read_b32 v26, v187 offset:72
	s_waitcnt lgkmcnt(0)
	v_pk_fma_f32 v[28:29], v[26:27], v[98:99], 0 op_sel_hi:[0,1,0] neg_lo:[1,0,0] neg_hi:[1,0,0]
	v_pk_fma_f32 v[26:27], v[26:27], v[100:101], 0 op_sel_hi:[0,1,0] neg_lo:[1,0,0] neg_hi:[1,0,0]
	v_cvt_pk_bf16_f32 v28, v28, v29
	v_cvt_pk_bf16_f32 v29, v26, v27
	ds_write_b64 v186, v[28:29] offset:544
	ds_read_b32 v26, v187 offset:80
	s_waitcnt lgkmcnt(0)
	v_pk_fma_f32 v[28:29], v[26:27], v[62:63], 0 op_sel_hi:[0,1,0] neg_lo:[1,0,0] neg_hi:[1,0,0]
	v_pk_fma_f32 v[26:27], v[26:27], v[64:65], 0 op_sel_hi:[0,1,0] neg_lo:[1,0,0] neg_hi:[1,0,0]
	v_cvt_pk_bf16_f32 v28, v28, v29
	v_cvt_pk_bf16_f32 v29, v26, v27
	ds_write_b64 v186, v[28:29] offset:1088
	ds_read_b32 v26, v187 offset:88
	s_waitcnt lgkmcnt(0)
	v_pk_fma_f32 v[28:29], v[26:27], v[50:51], 0 op_sel_hi:[0,1,0] neg_lo:[1,0,0] neg_hi:[1,0,0]
	v_pk_fma_f32 v[26:27], v[26:27], v[52:53], 0 op_sel_hi:[0,1,0] neg_lo:[1,0,0] neg_hi:[1,0,0]
	v_cvt_pk_bf16_f32 v28, v28, v29
	v_cvt_pk_bf16_f32 v29, v26, v27
	ds_write_b64 v186, v[28:29] offset:1632
	ds_read_b32 v26, v187 offset:96
	s_waitcnt lgkmcnt(0)
	v_pk_fma_f32 v[28:29], v[26:27], v[34:35], 0 op_sel_hi:[0,1,0] neg_lo:[1,0,0] neg_hi:[1,0,0]
	v_pk_fma_f32 v[26:27], v[26:27], v[36:37], 0 op_sel_hi:[0,1,0] neg_lo:[1,0,0] neg_hi:[1,0,0]
	v_cvt_pk_bf16_f32 v28, v28, v29
	v_cvt_pk_bf16_f32 v29, v26, v27
	ds_write_b64 v186, v[28:29] offset:2176
	ds_read_b32 v26, v187 offset:104
	s_waitcnt lgkmcnt(0)
	v_pk_fma_f32 v[22:23], v[26:27], v[22:23], 0 op_sel_hi:[0,1,0] neg_lo:[1,0,0] neg_hi:[1,0,0]
	v_pk_fma_f32 v[24:25], v[26:27], v[24:25], 0 op_sel_hi:[0,1,0] neg_lo:[1,0,0] neg_hi:[1,0,0]
	v_cvt_pk_bf16_f32 v22, v22, v23
	v_cvt_pk_bf16_f32 v23, v24, v25
	ds_write_b64 v186, v[22:23] offset:2720
	ds_read_b32 v22, v187 offset:112
	s_waitcnt lgkmcnt(0)
	v_pk_fma_f32 v[14:15], v[22:23], v[14:15], 0 op_sel_hi:[0,1,0] neg_lo:[1,0,0] neg_hi:[1,0,0]
	v_pk_fma_f32 v[16:17], v[22:23], v[16:17], 0 op_sel_hi:[0,1,0] neg_lo:[1,0,0] neg_hi:[1,0,0]
	v_cvt_pk_bf16_f32 v14, v14, v15
	v_cvt_pk_bf16_f32 v15, v16, v17
	ds_write_b64 v186, v[14:15] offset:3264
	ds_read_b32 v14, v187 offset:120
	s_waitcnt lgkmcnt(0)
	v_pk_fma_f32 v[6:7], v[14:15], v[6:7], 0 op_sel_hi:[0,1,0] neg_lo:[1,0,0] neg_hi:[1,0,0]
	v_pk_fma_f32 v[8:9], v[14:15], v[8:9], 0 op_sel_hi:[0,1,0] neg_lo:[1,0,0] neg_hi:[1,0,0]
	v_cvt_pk_bf16_f32 v6, v6, v7
	v_cvt_pk_bf16_f32 v7, v8, v9
	ds_write_b64 v186, v[6:7] offset:3808
	ds_read_b128 a[112:115], v1
	ds_read_b128 a[116:119], v1 offset:64
	ds_read_b128 a[120:123], v1 offset:128
	ds_read_b128 a[124:127], v1 offset:192
	v_lshl_add_u64 v[6:7], v[150:151], 0, s[24:25]
	v_lshl_add_u64 v[8:9], v[152:153], 0, s[24:25]
	v_lshl_add_u64 v[14:15], v[156:157], 0, s[24:25]
	v_lshl_add_u64 v[16:17], v[158:159], 0, s[24:25]
	v_lshl_add_u64 v[22:23], v[160:161], 0, s[24:25]
	v_lshl_add_u64 v[24:25], v[162:163], 0, s[24:25]
	v_lshl_add_u64 v[26:27], v[164:165], 0, s[24:25]
	v_lshl_add_u64 v[28:29], v[166:167], 0, s[24:25]
	global_load_dwordx4 v[110:113], v[6:7], off nt
	global_load_dwordx4 v[98:101], v[8:9], off nt
	global_load_dwordx4 v[78:81], v[14:15], off nt
	global_load_dwordx4 v[58:61], v[16:17], off nt
	global_load_dwordx4 v[34:37], v[22:23], off nt
	s_nop 0
	global_load_dwordx4 v[22:25], v[24:25], off nt
	s_nop 0
	global_load_dwordx4 v[14:17], v[26:27], off nt
	global_load_dwordx4 v[6:9], v[28:29], off nt
	s_waitcnt vmcnt(23)
	s_waitcnt vmcnt(22)
	s_waitcnt vmcnt(21)
	s_waitcnt vmcnt(20)
	s_waitcnt vmcnt(19)
	s_waitcnt vmcnt(18)
	s_waitcnt vmcnt(17)
	s_waitcnt vmcnt(16)
	ds_read_b32 v26, v187 offset:128
	s_waitcnt lgkmcnt(0)
	v_pk_fma_f32 v[28:29], v[26:27], v[106:107], 0 op_sel_hi:[0,1,0] neg_lo:[1,0,0] neg_hi:[1,0,0]
	v_pk_fma_f32 v[26:27], v[26:27], v[108:109], 0 op_sel_hi:[0,1,0] neg_lo:[1,0,0] neg_hi:[1,0,0]
	v_cvt_pk_bf16_f32 v28, v28, v29
	v_cvt_pk_bf16_f32 v29, v26, v27
	ds_write_b64 v186, v[28:29]
	ds_read_b32 v26, v187 offset:136
	s_waitcnt lgkmcnt(0)
	v_pk_fma_f32 v[28:29], v[26:27], v[94:95], 0 op_sel_hi:[0,1,0] neg_lo:[1,0,0] neg_hi:[1,0,0]
	v_pk_fma_f32 v[26:27], v[26:27], v[96:97], 0 op_sel_hi:[0,1,0] neg_lo:[1,0,0] neg_hi:[1,0,0]
	v_cvt_pk_bf16_f32 v28, v28, v29
	v_cvt_pk_bf16_f32 v29, v26, v27
	ds_write_b64 v186, v[28:29] offset:544
	ds_read_b32 v26, v187 offset:144
	s_waitcnt lgkmcnt(0)
	v_pk_fma_f32 v[28:29], v[26:27], v[74:75], 0 op_sel_hi:[0,1,0] neg_lo:[1,0,0] neg_hi:[1,0,0]
	v_pk_fma_f32 v[26:27], v[26:27], v[76:77], 0 op_sel_hi:[0,1,0] neg_lo:[1,0,0] neg_hi:[1,0,0]
	v_cvt_pk_bf16_f32 v28, v28, v29
	v_cvt_pk_bf16_f32 v29, v26, v27
	ds_write_b64 v186, v[28:29] offset:1088
	ds_read_b32 v26, v187 offset:152
	s_waitcnt lgkmcnt(0)
	v_pk_fma_f32 v[28:29], v[26:27], v[54:55], 0 op_sel_hi:[0,1,0] neg_lo:[1,0,0] neg_hi:[1,0,0]
	v_pk_fma_f32 v[26:27], v[26:27], v[56:57], 0 op_sel_hi:[0,1,0] neg_lo:[1,0,0] neg_hi:[1,0,0]
	v_cvt_pk_bf16_f32 v28, v28, v29
	v_cvt_pk_bf16_f32 v29, v26, v27
	ds_write_b64 v186, v[28:29] offset:1632
	ds_read_b32 v26, v187 offset:160
	s_waitcnt lgkmcnt(0)
	v_pk_fma_f32 v[28:29], v[26:27], v[38:39], 0 op_sel_hi:[0,1,0] neg_lo:[1,0,0] neg_hi:[1,0,0]
	v_pk_fma_f32 v[26:27], v[26:27], v[40:41], 0 op_sel_hi:[0,1,0] neg_lo:[1,0,0] neg_hi:[1,0,0]
	v_cvt_pk_bf16_f32 v28, v28, v29
	v_cvt_pk_bf16_f32 v29, v26, v27
	ds_write_b64 v186, v[28:29] offset:2176
	ds_read_b32 v26, v187 offset:168
	s_waitcnt lgkmcnt(0)
	v_pk_fma_f32 v[18:19], v[26:27], v[18:19], 0 op_sel_hi:[0,1,0] neg_lo:[1,0,0] neg_hi:[1,0,0]
	v_pk_fma_f32 v[20:21], v[26:27], v[20:21], 0 op_sel_hi:[0,1,0] neg_lo:[1,0,0] neg_hi:[1,0,0]
	v_cvt_pk_bf16_f32 v18, v18, v19
	v_cvt_pk_bf16_f32 v19, v20, v21
	ds_write_b64 v186, v[18:19] offset:2720
	ds_read_b32 v18, v187 offset:176
	s_waitcnt lgkmcnt(0)
	v_pk_fma_f32 v[10:11], v[18:19], v[10:11], 0 op_sel_hi:[0,1,0] neg_lo:[1,0,0] neg_hi:[1,0,0]
	v_pk_fma_f32 v[12:13], v[18:19], v[12:13], 0 op_sel_hi:[0,1,0] neg_lo:[1,0,0] neg_hi:[1,0,0]
	v_cvt_pk_bf16_f32 v10, v10, v11
	v_cvt_pk_bf16_f32 v11, v12, v13
	ds_write_b64 v186, v[10:11] offset:3264
	ds_read_b32 v10, v187 offset:184
	s_waitcnt lgkmcnt(0)
	v_pk_fma_f32 v[2:3], v[10:11], v[2:3], 0 op_sel_hi:[0,1,0] neg_lo:[1,0,0] neg_hi:[1,0,0]
	v_pk_fma_f32 v[4:5], v[10:11], v[4:5], 0 op_sel_hi:[0,1,0] neg_lo:[1,0,0] neg_hi:[1,0,0]
	v_cvt_pk_bf16_f32 v2, v2, v3
	v_cvt_pk_bf16_f32 v3, v4, v5
	ds_write_b64 v186, v[2:3] offset:3808
	ds_read_b128 a[128:131], v1
	ds_read_b128 a[132:135], v1 offset:64
	ds_read_b128 a[136:139], v1 offset:128
	ds_read_b128 a[140:143], v1 offset:192
	v_lshl_add_u64 v[2:3], v[168:169], 0, s[24:25]
	v_lshl_add_u64 v[4:5], v[170:171], 0, s[24:25]
	v_lshl_add_u64 v[10:11], v[172:173], 0, s[24:25]
	v_lshl_add_u64 v[12:13], v[174:175], 0, s[24:25]
	v_lshl_add_u64 v[18:19], v[176:177], 0, s[24:25]
	v_lshl_add_u64 v[20:21], v[178:179], 0, s[24:25]
	v_lshl_add_u64 v[50:51], v[180:181], 0, s[24:25]
	v_lshl_add_u64 v[52:53], v[182:183], 0, s[24:25]
	global_load_dwordx4 v[114:117], v[2:3], off nt
	global_load_dwordx4 v[94:97], v[4:5], off nt
	global_load_dwordx4 v[82:85], v[10:11], off nt
	global_load_dwordx4 v[62:65], v[12:13], off nt
	global_load_dwordx4 v[38:41], v[18:19], off nt
	global_load_dwordx4 v[26:29], v[20:21], off nt
	s_nop 0
	global_load_dwordx4 v[10:13], v[50:51], off nt
	global_load_dwordx4 v[2:5], v[52:53], off nt
	v_mov_b32_e32 v18, v195
	s_waitcnt vmcnt(23)
	s_waitcnt vmcnt(22)
	s_waitcnt vmcnt(21)
	s_waitcnt vmcnt(20)
	s_waitcnt vmcnt(19)
	s_waitcnt vmcnt(18)
	s_waitcnt vmcnt(17)
	s_waitcnt vmcnt(16)
	ds_read_b32 v18, v187
	s_waitcnt lgkmcnt(0)
	v_pk_fma_f32 v[20:21], v[18:19], v[102:103], 0 op_sel_hi:[0,1,0] neg_lo:[1,0,0] neg_hi:[1,0,0]
	v_pk_fma_f32 v[18:19], v[18:19], v[104:105], 0 op_sel_hi:[0,1,0] neg_lo:[1,0,0] neg_hi:[1,0,0]
	v_cvt_pk_bf16_f32 v20, v20, v21
	v_cvt_pk_bf16_f32 v21, v18, v19
	ds_write_b64 v186, v[20:21]
	ds_read_b32 v18, v187 offset:8
	s_waitcnt lgkmcnt(0)
	v_pk_fma_f32 v[20:21], v[18:19], v[90:91], 0 op_sel_hi:[0,1,0] neg_lo:[1,0,0] neg_hi:[1,0,0]
	v_pk_fma_f32 v[18:19], v[18:19], v[92:93], 0 op_sel_hi:[0,1,0] neg_lo:[1,0,0] neg_hi:[1,0,0]
	v_cvt_pk_bf16_f32 v20, v20, v21
	v_cvt_pk_bf16_f32 v21, v18, v19
	ds_write_b64 v186, v[20:21] offset:544
	ds_read_b32 v18, v187 offset:16
	s_waitcnt lgkmcnt(0)
	v_pk_fma_f32 v[20:21], v[18:19], v[86:87], 0 op_sel_hi:[0,1,0] neg_lo:[1,0,0] neg_hi:[1,0,0]
	v_pk_fma_f32 v[18:19], v[18:19], v[88:89], 0 op_sel_hi:[0,1,0] neg_lo:[1,0,0] neg_hi:[1,0,0]
	v_cvt_pk_bf16_f32 v20, v20, v21
	v_cvt_pk_bf16_f32 v21, v18, v19
	ds_write_b64 v186, v[20:21] offset:1088
	ds_read_b32 v18, v187 offset:24
	s_waitcnt lgkmcnt(0)
	v_pk_fma_f32 v[20:21], v[18:19], v[70:71], 0 op_sel_hi:[0,1,0] neg_lo:[1,0,0] neg_hi:[1,0,0]
	v_pk_fma_f32 v[18:19], v[18:19], v[72:73], 0 op_sel_hi:[0,1,0] neg_lo:[1,0,0] neg_hi:[1,0,0]
	v_cvt_pk_bf16_f32 v20, v20, v21
	v_cvt_pk_bf16_f32 v21, v18, v19
	ds_write_b64 v186, v[20:21] offset:1632
	ds_read_b32 v18, v187 offset:32
	s_waitcnt lgkmcnt(0)
	v_pk_fma_f32 v[20:21], v[18:19], v[66:67], 0 op_sel_hi:[0,1,0] neg_lo:[1,0,0] neg_hi:[1,0,0]
	v_pk_fma_f32 v[18:19], v[18:19], v[68:69], 0 op_sel_hi:[0,1,0] neg_lo:[1,0,0] neg_hi:[1,0,0]
	v_cvt_pk_bf16_f32 v20, v20, v21
	v_cvt_pk_bf16_f32 v21, v18, v19
	ds_write_b64 v186, v[20:21] offset:2176
	ds_read_b32 v18, v187 offset:40
	s_waitcnt lgkmcnt(0)
	v_pk_fma_f32 v[20:21], v[18:19], v[46:47], 0 op_sel_hi:[0,1,0] neg_lo:[1,0,0] neg_hi:[1,0,0]
	v_pk_fma_f32 v[18:19], v[18:19], v[48:49], 0 op_sel_hi:[0,1,0] neg_lo:[1,0,0] neg_hi:[1,0,0]
	v_cvt_pk_bf16_f32 v20, v20, v21
	v_cvt_pk_bf16_f32 v21, v18, v19
	ds_write_b64 v186, v[20:21] offset:2720
	ds_read_b32 v18, v187 offset:48
	s_waitcnt lgkmcnt(0)
	v_pk_fma_f32 v[20:21], v[18:19], v[42:43], 0 op_sel_hi:[0,1,0] neg_lo:[1,0,0] neg_hi:[1,0,0]
	v_pk_fma_f32 v[18:19], v[18:19], v[44:45], 0 op_sel_hi:[0,1,0] neg_lo:[1,0,0] neg_hi:[1,0,0]
	v_cvt_pk_bf16_f32 v20, v20, v21
	v_cvt_pk_bf16_f32 v21, v18, v19
	ds_write_b64 v186, v[20:21] offset:3264
	ds_read_b32 v18, v187 offset:56
	s_waitcnt lgkmcnt(0)
	v_pk_fma_f32 v[20:21], v[18:19], v[30:31], 0 op_sel_hi:[0,1,0] neg_lo:[1,0,0] neg_hi:[1,0,0]
	v_pk_fma_f32 v[18:19], v[18:19], v[32:33], 0 op_sel_hi:[0,1,0] neg_lo:[1,0,0] neg_hi:[1,0,0]
	v_cvt_pk_bf16_f32 v20, v20, v21
	v_cvt_pk_bf16_f32 v21, v18, v19
	ds_write_b64 v186, v[20:21] offset:3808
	ds_read_b128 a[144:147], v1
	ds_read_b128 a[148:151], v1 offset:64
	ds_read_b128 a[152:155], v1 offset:128
	ds_read_b128 a[156:159], v1 offset:192
	v_lshl_add_u64 v[18:19], v[130:131], 0, s[22:23]
	v_add_co_u32_e32 v20, vcc, s7, v18
	s_nop 1
	v_addc_co_u32_e32 v21, vcc, 0, v19, vcc
	global_load_dwordx4 v[106:109], v[18:19], off nt
	global_load_dwordx4 v[90:93], v[20:21], off nt
	v_add_co_u32_e32 v20, vcc, s36, v18
	s_nop 1
	v_addc_co_u32_e32 v21, vcc, 0, v19, vcc
	v_add_co_u32_e32 v30, vcc, s37, v18
	s_nop 1
	v_addc_co_u32_e32 v31, vcc, 0, v19, vcc
	global_load_dwordx4 v[86:89], v[20:21], off nt
	global_load_dwordx4 v[74:77], v[30:31], off nt
	v_add_co_u32_e32 v20, vcc, s38, v18
	s_nop 1
	v_addc_co_u32_e32 v21, vcc, 0, v19, vcc
	v_add_co_u32_e32 v30, vcc, s39, v18
	s_nop 1
	v_addc_co_u32_e32 v31, vcc, 0, v19, vcc
	global_load_dwordx4 v[70:73], v[20:21], off nt
	global_load_dwordx4 v[54:57], v[30:31], off nt
	v_add_co_u32_e32 v20, vcc, s41, v18
	s_nop 1
	v_addc_co_u32_e32 v21, vcc, 0, v19, vcc
	v_add_co_u32_e32 v18, vcc, s42, v18
	s_nop 1
	v_addc_co_u32_e32 v19, vcc, 0, v19, vcc
	global_load_dwordx4 v[50:53], v[20:21], off nt
	global_load_dwordx4 v[46:49], v[18:19], off nt
	v_mov_b32_e32 v18, v195
	s_waitcnt vmcnt(23)
	s_waitcnt vmcnt(22)
	s_waitcnt vmcnt(21)
	s_waitcnt vmcnt(20)
	s_waitcnt vmcnt(19)
	s_waitcnt vmcnt(18)
	s_waitcnt vmcnt(17)
	s_waitcnt vmcnt(16)
	ds_read_b32 v18, v187 offset:64
	s_waitcnt lgkmcnt(0)
	v_pk_fma_f32 v[20:21], v[18:19], v[110:111], 0 op_sel_hi:[0,1,0] neg_lo:[1,0,0] neg_hi:[1,0,0]
	v_pk_fma_f32 v[18:19], v[18:19], v[112:113], 0 op_sel_hi:[0,1,0] neg_lo:[1,0,0] neg_hi:[1,0,0]
	v_cvt_pk_bf16_f32 v20, v20, v21
	v_cvt_pk_bf16_f32 v21, v18, v19
	ds_write_b64 v186, v[20:21]
	ds_read_b32 v18, v187 offset:72
	s_waitcnt lgkmcnt(0)
	v_pk_fma_f32 v[20:21], v[18:19], v[98:99], 0 op_sel_hi:[0,1,0] neg_lo:[1,0,0] neg_hi:[1,0,0]
	v_pk_fma_f32 v[18:19], v[18:19], v[100:101], 0 op_sel_hi:[0,1,0] neg_lo:[1,0,0] neg_hi:[1,0,0]
	v_cvt_pk_bf16_f32 v20, v20, v21
	v_cvt_pk_bf16_f32 v21, v18, v19
	ds_write_b64 v186, v[20:21] offset:544
	ds_read_b32 v18, v187 offset:80
	s_waitcnt lgkmcnt(0)
	v_pk_fma_f32 v[20:21], v[18:19], v[78:79], 0 op_sel_hi:[0,1,0] neg_lo:[1,0,0] neg_hi:[1,0,0]
	v_pk_fma_f32 v[18:19], v[18:19], v[80:81], 0 op_sel_hi:[0,1,0] neg_lo:[1,0,0] neg_hi:[1,0,0]
	v_cvt_pk_bf16_f32 v20, v20, v21
	v_cvt_pk_bf16_f32 v21, v18, v19
	ds_write_b64 v186, v[20:21] offset:1088
	ds_read_b32 v18, v187 offset:88
	s_waitcnt lgkmcnt(0)
	v_pk_fma_f32 v[20:21], v[18:19], v[58:59], 0 op_sel_hi:[0,1,0] neg_lo:[1,0,0] neg_hi:[1,0,0]
	v_pk_fma_f32 v[18:19], v[18:19], v[60:61], 0 op_sel_hi:[0,1,0] neg_lo:[1,0,0] neg_hi:[1,0,0]
	v_cvt_pk_bf16_f32 v20, v20, v21
	v_cvt_pk_bf16_f32 v21, v18, v19
	ds_write_b64 v186, v[20:21] offset:1632
	ds_read_b32 v18, v187 offset:96
	s_waitcnt lgkmcnt(0)
	v_pk_fma_f32 v[20:21], v[18:19], v[34:35], 0 op_sel_hi:[0,1,0] neg_lo:[1,0,0] neg_hi:[1,0,0]
	v_pk_fma_f32 v[18:19], v[18:19], v[36:37], 0 op_sel_hi:[0,1,0] neg_lo:[1,0,0] neg_hi:[1,0,0]
	v_cvt_pk_bf16_f32 v20, v20, v21
	v_cvt_pk_bf16_f32 v21, v18, v19
	ds_write_b64 v186, v[20:21] offset:2176
	ds_read_b32 v18, v187 offset:104
	s_waitcnt lgkmcnt(0)
	v_pk_fma_f32 v[20:21], v[18:19], v[22:23], 0 op_sel_hi:[0,1,0] neg_lo:[1,0,0] neg_hi:[1,0,0]
	v_pk_fma_f32 v[18:19], v[18:19], v[24:25], 0 op_sel_hi:[0,1,0] neg_lo:[1,0,0] neg_hi:[1,0,0]
	v_cvt_pk_bf16_f32 v20, v20, v21
	v_cvt_pk_bf16_f32 v21, v18, v19
	ds_write_b64 v186, v[20:21] offset:2720
	ds_read_b32 v18, v187 offset:112
	s_waitcnt lgkmcnt(0)
	v_pk_fma_f32 v[14:15], v[18:19], v[14:15], 0 op_sel_hi:[0,1,0] neg_lo:[1,0,0] neg_hi:[1,0,0]
	v_pk_fma_f32 v[16:17], v[18:19], v[16:17], 0 op_sel_hi:[0,1,0] neg_lo:[1,0,0] neg_hi:[1,0,0]
	v_cvt_pk_bf16_f32 v14, v14, v15
	v_cvt_pk_bf16_f32 v15, v16, v17
	ds_write_b64 v186, v[14:15] offset:3264
	ds_read_b32 v14, v187 offset:120
	s_waitcnt lgkmcnt(0)
	v_pk_fma_f32 v[6:7], v[14:15], v[6:7], 0 op_sel_hi:[0,1,0] neg_lo:[1,0,0] neg_hi:[1,0,0]
	v_pk_fma_f32 v[8:9], v[14:15], v[8:9], 0 op_sel_hi:[0,1,0] neg_lo:[1,0,0] neg_hi:[1,0,0]
	v_cvt_pk_bf16_f32 v6, v6, v7
	v_cvt_pk_bf16_f32 v7, v8, v9
	ds_write_b64 v186, v[6:7] offset:3808
	ds_read_b128 a[160:163], v1
	ds_read_b128 a[164:167], v1 offset:64
	ds_read_b128 a[168:171], v1 offset:128
	ds_read_b128 a[172:175], v1 offset:192
	v_lshl_add_u64 v[6:7], v[150:151], 0, s[22:23]
	v_lshl_add_u64 v[18:19], v[160:161], 0, s[22:23]
	v_lshl_add_u64 v[20:21], v[162:163], 0, s[22:23]
	v_lshl_add_u64 v[22:23], v[164:165], 0, s[22:23]
	v_lshl_add_u64 v[8:9], v[152:153], 0, s[22:23]
	v_lshl_add_u64 v[14:15], v[156:157], 0, s[22:23]
	v_lshl_add_u64 v[16:17], v[158:159], 0, s[22:23]
	v_lshl_add_u64 v[34:35], v[166:167], 0, s[22:23]
	global_load_dwordx4 v[110:113], v[6:7], off nt
	global_load_dwordx4 v[98:101], v[8:9], off nt
	global_load_dwordx4 v[78:81], v[14:15], off nt
	global_load_dwordx4 v[66:69], v[16:17], off nt
	global_load_dwordx4 v[58:61], v[18:19], off nt
	global_load_dwordx4 v[30:33], v[20:21], off nt
	s_nop 0
	global_load_dwordx4 v[22:25], v[22:23], off nt
	s_nop 0
	global_load_dwordx4 v[18:21], v[34:35], off nt
	s_waitcnt vmcnt(23)
	s_waitcnt vmcnt(22)
	s_waitcnt vmcnt(21)
	s_waitcnt vmcnt(20)
	s_waitcnt vmcnt(19)
	s_waitcnt vmcnt(18)
	s_waitcnt vmcnt(17)
	s_waitcnt vmcnt(16)
	ds_read_b32 v6, v187 offset:128
	s_waitcnt lgkmcnt(0)
	v_pk_fma_f32 v[8:9], v[6:7], v[114:115], 0 op_sel_hi:[0,1,0] neg_lo:[1,0,0] neg_hi:[1,0,0]
	v_pk_fma_f32 v[6:7], v[6:7], v[116:117], 0 op_sel_hi:[0,1,0] neg_lo:[1,0,0] neg_hi:[1,0,0]
	v_cvt_pk_bf16_f32 v8, v8, v9
	v_cvt_pk_bf16_f32 v9, v6, v7
	ds_write_b64 v186, v[8:9]
	ds_read_b32 v6, v187 offset:136
	s_waitcnt lgkmcnt(0)
	v_pk_fma_f32 v[8:9], v[6:7], v[94:95], 0 op_sel_hi:[0,1,0] neg_lo:[1,0,0] neg_hi:[1,0,0]
	v_pk_fma_f32 v[6:7], v[6:7], v[96:97], 0 op_sel_hi:[0,1,0] neg_lo:[1,0,0] neg_hi:[1,0,0]
	v_cvt_pk_bf16_f32 v8, v8, v9
	v_cvt_pk_bf16_f32 v9, v6, v7
	ds_write_b64 v186, v[8:9] offset:544
	ds_read_b32 v6, v187 offset:144
	s_waitcnt lgkmcnt(0)
	v_pk_fma_f32 v[8:9], v[6:7], v[82:83], 0 op_sel_hi:[0,1,0] neg_lo:[1,0,0] neg_hi:[1,0,0]
	v_pk_fma_f32 v[6:7], v[6:7], v[84:85], 0 op_sel_hi:[0,1,0] neg_lo:[1,0,0] neg_hi:[1,0,0]
	v_cvt_pk_bf16_f32 v8, v8, v9
	v_cvt_pk_bf16_f32 v9, v6, v7
	ds_write_b64 v186, v[8:9] offset:1088
	ds_read_b32 v6, v187 offset:152
	s_waitcnt lgkmcnt(0)
	v_pk_fma_f32 v[8:9], v[6:7], v[62:63], 0 op_sel_hi:[0,1,0] neg_lo:[1,0,0] neg_hi:[1,0,0]
	v_pk_fma_f32 v[6:7], v[6:7], v[64:65], 0 op_sel_hi:[0,1,0] neg_lo:[1,0,0] neg_hi:[1,0,0]
	v_cvt_pk_bf16_f32 v8, v8, v9
	v_cvt_pk_bf16_f32 v9, v6, v7
	ds_write_b64 v186, v[8:9] offset:1632
	ds_read_b32 v6, v187 offset:160
	s_waitcnt lgkmcnt(0)
	v_pk_fma_f32 v[8:9], v[6:7], v[38:39], 0 op_sel_hi:[0,1,0] neg_lo:[1,0,0] neg_hi:[1,0,0]
	v_pk_fma_f32 v[6:7], v[6:7], v[40:41], 0 op_sel_hi:[0,1,0] neg_lo:[1,0,0] neg_hi:[1,0,0]
	v_cvt_pk_bf16_f32 v8, v8, v9
	v_cvt_pk_bf16_f32 v9, v6, v7
	ds_write_b64 v186, v[8:9] offset:2176
	ds_read_b32 v6, v187 offset:168
	s_waitcnt lgkmcnt(0)
	v_pk_fma_f32 v[8:9], v[6:7], v[26:27], 0 op_sel_hi:[0,1,0] neg_lo:[1,0,0] neg_hi:[1,0,0]
	v_pk_fma_f32 v[6:7], v[6:7], v[28:29], 0 op_sel_hi:[0,1,0] neg_lo:[1,0,0] neg_hi:[1,0,0]
	v_cvt_pk_bf16_f32 v8, v8, v9
	v_cvt_pk_bf16_f32 v9, v6, v7
	ds_write_b64 v186, v[8:9] offset:2720
	ds_read_b32 v6, v187 offset:176
	s_waitcnt lgkmcnt(0)
	v_pk_fma_f32 v[8:9], v[6:7], v[10:11], 0 op_sel_hi:[0,1,0] neg_lo:[1,0,0] neg_hi:[1,0,0]
	v_pk_fma_f32 v[6:7], v[6:7], v[12:13], 0 op_sel_hi:[0,1,0] neg_lo:[1,0,0] neg_hi:[1,0,0]
	v_cvt_pk_bf16_f32 v8, v8, v9
	v_cvt_pk_bf16_f32 v9, v6, v7
	ds_write_b64 v186, v[8:9] offset:3264
	ds_read_b32 v6, v187 offset:184
	s_waitcnt lgkmcnt(0)
	v_pk_fma_f32 v[2:3], v[6:7], v[2:3], 0 op_sel_hi:[0,1,0] neg_lo:[1,0,0] neg_hi:[1,0,0]
	v_pk_fma_f32 v[4:5], v[6:7], v[4:5], 0 op_sel_hi:[0,1,0] neg_lo:[1,0,0] neg_hi:[1,0,0]
	v_cvt_pk_bf16_f32 v2, v2, v3
	v_cvt_pk_bf16_f32 v3, v4, v5
	ds_write_b64 v186, v[2:3] offset:3808
	ds_read_b128 a[176:179], v1
	ds_read_b128 a[180:183], v1 offset:64
	ds_read_b128 a[184:187], v1 offset:128
	ds_read_b128 a[188:191], v1 offset:192
	v_lshl_add_u64 v[2:3], v[168:169], 0, s[22:23]
	v_lshl_add_u64 v[4:5], v[170:171], 0, s[22:23]
	v_lshl_add_u64 v[6:7], v[172:173], 0, s[22:23]
	v_lshl_add_u64 v[8:9], v[174:175], 0, s[22:23]
	v_lshl_add_u64 v[10:11], v[176:177], 0, s[22:23]
	v_lshl_add_u64 v[12:13], v[178:179], 0, s[22:23]
	v_lshl_add_u64 v[14:15], v[180:181], 0, s[22:23]
	v_lshl_add_u64 v[16:17], v[182:183], 0, s[22:23]
	global_load_dwordx4 v[114:117], v[2:3], off nt
	global_load_dwordx4 v[102:105], v[4:5], off nt
	global_load_dwordx4 v[94:97], v[6:7], off nt
	global_load_dwordx4 v[82:85], v[8:9], off nt
	global_load_dwordx4 v[62:65], v[10:11], off nt
	global_load_dwordx4 v[42:45], v[12:13], off nt
	global_load_dwordx4 v[38:41], v[14:15], off nt
	global_load_dwordx4 v[34:37], v[16:17], off nt
	v_mov_b32_e32 v2, v194
	s_waitcnt vmcnt(23)
	s_waitcnt vmcnt(22)
	s_waitcnt vmcnt(21)
	s_waitcnt vmcnt(20)
	s_waitcnt vmcnt(19)
	s_waitcnt vmcnt(18)
	s_waitcnt vmcnt(17)
	s_waitcnt vmcnt(16)
	ds_read_b32 v2, v187
	s_waitcnt lgkmcnt(0)
	v_pk_fma_f32 v[4:5], v[2:3], v[106:107], 0 op_sel_hi:[0,1,0] neg_lo:[1,0,0] neg_hi:[1,0,0]
	v_pk_fma_f32 v[2:3], v[2:3], v[108:109], 0 op_sel_hi:[0,1,0] neg_lo:[1,0,0] neg_hi:[1,0,0]
	v_cvt_pk_bf16_f32 v4, v4, v5
	v_cvt_pk_bf16_f32 v5, v2, v3
	ds_write_b64 v186, v[4:5]
	ds_read_b32 v2, v187 offset:8
	s_waitcnt lgkmcnt(0)
	v_pk_fma_f32 v[4:5], v[2:3], v[90:91], 0 op_sel_hi:[0,1,0] neg_lo:[1,0,0] neg_hi:[1,0,0]
	v_pk_fma_f32 v[2:3], v[2:3], v[92:93], 0 op_sel_hi:[0,1,0] neg_lo:[1,0,0] neg_hi:[1,0,0]
	v_cvt_pk_bf16_f32 v4, v4, v5
	v_cvt_pk_bf16_f32 v5, v2, v3
	ds_write_b64 v186, v[4:5] offset:544
	ds_read_b32 v2, v187 offset:16
	s_waitcnt lgkmcnt(0)
	v_pk_fma_f32 v[4:5], v[2:3], v[86:87], 0 op_sel_hi:[0,1,0] neg_lo:[1,0,0] neg_hi:[1,0,0]
	v_pk_fma_f32 v[2:3], v[2:3], v[88:89], 0 op_sel_hi:[0,1,0] neg_lo:[1,0,0] neg_hi:[1,0,0]
	v_cvt_pk_bf16_f32 v4, v4, v5
	v_cvt_pk_bf16_f32 v5, v2, v3
	ds_write_b64 v186, v[4:5] offset:1088
	ds_read_b32 v2, v187 offset:24
	s_waitcnt lgkmcnt(0)
	v_pk_fma_f32 v[4:5], v[2:3], v[74:75], 0 op_sel_hi:[0,1,0] neg_lo:[1,0,0] neg_hi:[1,0,0]
	v_pk_fma_f32 v[2:3], v[2:3], v[76:77], 0 op_sel_hi:[0,1,0] neg_lo:[1,0,0] neg_hi:[1,0,0]
	v_cvt_pk_bf16_f32 v4, v4, v5
	v_cvt_pk_bf16_f32 v5, v2, v3
	ds_write_b64 v186, v[4:5] offset:1632
	ds_read_b32 v2, v187 offset:32
	s_waitcnt lgkmcnt(0)
	v_pk_fma_f32 v[4:5], v[2:3], v[70:71], 0 op_sel_hi:[0,1,0] neg_lo:[1,0,0] neg_hi:[1,0,0]
	v_pk_fma_f32 v[2:3], v[2:3], v[72:73], 0 op_sel_hi:[0,1,0] neg_lo:[1,0,0] neg_hi:[1,0,0]
	v_cvt_pk_bf16_f32 v4, v4, v5
	v_cvt_pk_bf16_f32 v5, v2, v3
	ds_write_b64 v186, v[4:5] offset:2176
	ds_read_b32 v2, v187 offset:40
	s_waitcnt lgkmcnt(0)
	v_pk_fma_f32 v[4:5], v[2:3], v[54:55], 0 op_sel_hi:[0,1,0] neg_lo:[1,0,0] neg_hi:[1,0,0]
	v_pk_fma_f32 v[2:3], v[2:3], v[56:57], 0 op_sel_hi:[0,1,0] neg_lo:[1,0,0] neg_hi:[1,0,0]
	v_cvt_pk_bf16_f32 v4, v4, v5
	v_cvt_pk_bf16_f32 v5, v2, v3
	ds_write_b64 v186, v[4:5] offset:2720
	ds_read_b32 v2, v187 offset:48
	s_waitcnt lgkmcnt(0)
	v_pk_fma_f32 v[4:5], v[2:3], v[50:51], 0 op_sel_hi:[0,1,0] neg_lo:[1,0,0] neg_hi:[1,0,0]
	v_pk_fma_f32 v[2:3], v[2:3], v[52:53], 0 op_sel_hi:[0,1,0] neg_lo:[1,0,0] neg_hi:[1,0,0]
	v_cvt_pk_bf16_f32 v4, v4, v5
	v_cvt_pk_bf16_f32 v5, v2, v3
	ds_write_b64 v186, v[4:5] offset:3264
	ds_read_b32 v2, v187 offset:56
	s_waitcnt lgkmcnt(0)
	v_pk_fma_f32 v[4:5], v[2:3], v[46:47], 0 op_sel_hi:[0,1,0] neg_lo:[1,0,0] neg_hi:[1,0,0]
	v_pk_fma_f32 v[2:3], v[2:3], v[48:49], 0 op_sel_hi:[0,1,0] neg_lo:[1,0,0] neg_hi:[1,0,0]
	v_cvt_pk_bf16_f32 v4, v4, v5
	v_cvt_pk_bf16_f32 v5, v2, v3
	ds_write_b64 v186, v[4:5] offset:3808
	ds_read_b128 a[192:195], v1
	ds_read_b128 a[196:199], v1 offset:64
	ds_read_b128 a[200:203], v1 offset:128
	ds_read_b128 a[204:207], v1 offset:192
	v_lshl_add_u64 v[118:119], v[130:131], 0, s[20:21]
	v_add_co_u32_e32 v126, vcc, s7, v118
	s_nop 1
	v_addc_co_u32_e32 v127, vcc, 0, v119, vcc
	v_add_co_u32_e32 v128, vcc, s36, v118
	global_load_dwordx4 v[90:93], v[118:119], off nt
	global_load_dwordx4 v[86:89], v[126:127], off nt
	v_addc_co_u32_e32 v129, vcc, 0, v119, vcc
	v_add_co_u32_e32 v134, vcc, s37, v118
	s_nop 1
	v_addc_co_u32_e32 v135, vcc, 0, v119, vcc
	v_add_co_u32_e32 v136, vcc, s38, v118
	global_load_dwordx4 v[54:57], v[128:129], off nt
	global_load_dwordx4 v[50:53], v[134:135], off nt
	v_addc_co_u32_e32 v137, vcc, 0, v119, vcc
	v_add_co_u32_e32 v138, vcc, s39, v118
	s_nop 1
	v_addc_co_u32_e32 v139, vcc, 0, v119, vcc
	v_add_co_u32_e32 v140, vcc, s41, v118
	global_load_dwordx4 v[14:17], v[136:137], off nt
	global_load_dwordx4 v[10:13], v[138:139], off nt
	v_addc_co_u32_e32 v141, vcc, 0, v119, vcc
	v_add_co_u32_e32 v142, vcc, s42, v118
	s_nop 1
	v_addc_co_u32_e32 v143, vcc, 0, v119, vcc
	global_load_dwordx4 v[6:9], v[140:141], off nt
	global_load_dwordx4 v[2:5], v[142:143], off nt
	v_mov_b32_e32 v26, v194
	s_waitcnt vmcnt(23)
	s_waitcnt vmcnt(22)
	s_waitcnt vmcnt(21)
	s_waitcnt vmcnt(20)
	s_waitcnt vmcnt(19)
	s_waitcnt vmcnt(18)
	s_waitcnt vmcnt(17)
	s_waitcnt vmcnt(16)
	ds_read_b32 v26, v187 offset:64
	s_waitcnt lgkmcnt(0)
	v_pk_fma_f32 v[28:29], v[26:27], v[110:111], 0 op_sel_hi:[0,1,0] neg_lo:[1,0,0] neg_hi:[1,0,0]
	v_pk_fma_f32 v[26:27], v[26:27], v[112:113], 0 op_sel_hi:[0,1,0] neg_lo:[1,0,0] neg_hi:[1,0,0]
	v_cvt_pk_bf16_f32 v28, v28, v29
	v_cvt_pk_bf16_f32 v29, v26, v27
	ds_write_b64 v186, v[28:29]
	ds_read_b32 v26, v187 offset:72
	s_waitcnt lgkmcnt(0)
	v_pk_fma_f32 v[28:29], v[26:27], v[98:99], 0 op_sel_hi:[0,1,0] neg_lo:[1,0,0] neg_hi:[1,0,0]
	v_pk_fma_f32 v[26:27], v[26:27], v[100:101], 0 op_sel_hi:[0,1,0] neg_lo:[1,0,0] neg_hi:[1,0,0]
	v_cvt_pk_bf16_f32 v28, v28, v29
	v_cvt_pk_bf16_f32 v29, v26, v27
	ds_write_b64 v186, v[28:29] offset:544
	ds_read_b32 v26, v187 offset:80
	s_waitcnt lgkmcnt(0)
	v_pk_fma_f32 v[28:29], v[26:27], v[78:79], 0 op_sel_hi:[0,1,0] neg_lo:[1,0,0] neg_hi:[1,0,0]
	v_pk_fma_f32 v[26:27], v[26:27], v[80:81], 0 op_sel_hi:[0,1,0] neg_lo:[1,0,0] neg_hi:[1,0,0]
	v_cvt_pk_bf16_f32 v28, v28, v29
	v_cvt_pk_bf16_f32 v29, v26, v27
	ds_write_b64 v186, v[28:29] offset:1088
	ds_read_b32 v26, v187 offset:88
	s_waitcnt lgkmcnt(0)
	v_pk_fma_f32 v[28:29], v[26:27], v[66:67], 0 op_sel_hi:[0,1,0] neg_lo:[1,0,0] neg_hi:[1,0,0]
	v_pk_fma_f32 v[26:27], v[26:27], v[68:69], 0 op_sel_hi:[0,1,0] neg_lo:[1,0,0] neg_hi:[1,0,0]
	v_cvt_pk_bf16_f32 v28, v28, v29
	v_cvt_pk_bf16_f32 v29, v26, v27
	ds_write_b64 v186, v[28:29] offset:1632
	ds_read_b32 v26, v187 offset:96
	s_waitcnt lgkmcnt(0)
	v_pk_fma_f32 v[28:29], v[26:27], v[58:59], 0 op_sel_hi:[0,1,0] neg_lo:[1,0,0] neg_hi:[1,0,0]
	v_pk_fma_f32 v[26:27], v[26:27], v[60:61], 0 op_sel_hi:[0,1,0] neg_lo:[1,0,0] neg_hi:[1,0,0]
	v_cvt_pk_bf16_f32 v28, v28, v29
	v_cvt_pk_bf16_f32 v29, v26, v27
	ds_write_b64 v186, v[28:29] offset:2176
	ds_read_b32 v26, v187 offset:104
	s_waitcnt lgkmcnt(0)
	v_pk_fma_f32 v[28:29], v[26:27], v[30:31], 0 op_sel_hi:[0,1,0] neg_lo:[1,0,0] neg_hi:[1,0,0]
	v_pk_fma_f32 v[26:27], v[26:27], v[32:33], 0 op_sel_hi:[0,1,0] neg_lo:[1,0,0] neg_hi:[1,0,0]
	v_cvt_pk_bf16_f32 v28, v28, v29
	v_cvt_pk_bf16_f32 v29, v26, v27
	ds_write_b64 v186, v[28:29] offset:2720
	ds_read_b32 v26, v187 offset:112
	s_waitcnt lgkmcnt(0)
	v_pk_fma_f32 v[22:23], v[26:27], v[22:23], 0 op_sel_hi:[0,1,0] neg_lo:[1,0,0] neg_hi:[1,0,0]
	v_pk_fma_f32 v[24:25], v[26:27], v[24:25], 0 op_sel_hi:[0,1,0] neg_lo:[1,0,0] neg_hi:[1,0,0]
	v_cvt_pk_bf16_f32 v22, v22, v23
	v_cvt_pk_bf16_f32 v23, v24, v25
	ds_write_b64 v186, v[22:23] offset:3264
	ds_read_b32 v22, v187 offset:120
	s_waitcnt lgkmcnt(0)
	v_pk_fma_f32 v[18:19], v[22:23], v[18:19], 0 op_sel_hi:[0,1,0] neg_lo:[1,0,0] neg_hi:[1,0,0]
	v_pk_fma_f32 v[20:21], v[22:23], v[20:21], 0 op_sel_hi:[0,1,0] neg_lo:[1,0,0] neg_hi:[1,0,0]
	v_cvt_pk_bf16_f32 v18, v18, v19
	v_cvt_pk_bf16_f32 v19, v20, v21
	ds_write_b64 v186, v[18:19] offset:3808
	ds_read_b128 a[208:211], v1
	ds_read_b128 a[212:215], v1 offset:64
	ds_read_b128 a[216:219], v1 offset:128
	ds_read_b128 a[220:223], v1 offset:192
	v_lshl_add_u64 v[18:19], v[150:151], 0, s[20:21]
	v_lshl_add_u64 v[20:21], v[152:153], 0, s[20:21]
	v_lshl_add_u64 v[22:23], v[156:157], 0, s[20:21]
	v_lshl_add_u64 v[24:25], v[158:159], 0, s[20:21]
	v_lshl_add_u64 v[26:27], v[160:161], 0, s[20:21]
	v_lshl_add_u64 v[28:29], v[162:163], 0, s[20:21]
	v_lshl_add_u64 v[46:47], v[164:165], 0, s[20:21]
	v_lshl_add_u64 v[48:49], v[166:167], 0, s[20:21]
	global_load_dwordx4 v[78:81], v[18:19], off nt
	global_load_dwordx4 v[74:77], v[20:21], off nt
	global_load_dwordx4 v[70:73], v[22:23], off nt
	global_load_dwordx4 v[66:69], v[24:25], off nt
	global_load_dwordx4 v[30:33], v[26:27], off nt
	s_nop 0
	global_load_dwordx4 v[26:29], v[28:29], off nt
	s_nop 0
	global_load_dwordx4 v[22:25], v[46:47], off nt
	global_load_dwordx4 v[18:21], v[48:49], off nt
	s_waitcnt vmcnt(23)
	s_waitcnt vmcnt(22)
	s_waitcnt vmcnt(21)
	s_waitcnt vmcnt(20)
	s_waitcnt vmcnt(19)
	s_waitcnt vmcnt(18)
	s_waitcnt vmcnt(17)
	s_waitcnt vmcnt(16)
	ds_read_b32 v46, v187 offset:128
	s_waitcnt lgkmcnt(0)
	v_pk_fma_f32 v[48:49], v[46:47], v[114:115], 0 op_sel_hi:[0,1,0] neg_lo:[1,0,0] neg_hi:[1,0,0]
	v_pk_fma_f32 v[46:47], v[46:47], v[116:117], 0 op_sel_hi:[0,1,0] neg_lo:[1,0,0] neg_hi:[1,0,0]
	v_cvt_pk_bf16_f32 v48, v48, v49
	v_cvt_pk_bf16_f32 v49, v46, v47
	ds_write_b64 v186, v[48:49]
	ds_read_b32 v46, v187 offset:136
	s_waitcnt lgkmcnt(0)
	v_pk_fma_f32 v[48:49], v[46:47], v[102:103], 0 op_sel_hi:[0,1,0] neg_lo:[1,0,0] neg_hi:[1,0,0]
	v_pk_fma_f32 v[46:47], v[46:47], v[104:105], 0 op_sel_hi:[0,1,0] neg_lo:[1,0,0] neg_hi:[1,0,0]
	v_cvt_pk_bf16_f32 v48, v48, v49
	v_cvt_pk_bf16_f32 v49, v46, v47
	ds_write_b64 v186, v[48:49] offset:544
	ds_read_b32 v46, v187 offset:144
	s_waitcnt lgkmcnt(0)
	v_pk_fma_f32 v[48:49], v[46:47], v[94:95], 0 op_sel_hi:[0,1,0] neg_lo:[1,0,0] neg_hi:[1,0,0]
	v_pk_fma_f32 v[46:47], v[46:47], v[96:97], 0 op_sel_hi:[0,1,0] neg_lo:[1,0,0] neg_hi:[1,0,0]
	v_cvt_pk_bf16_f32 v48, v48, v49
	v_cvt_pk_bf16_f32 v49, v46, v47
	ds_write_b64 v186, v[48:49] offset:1088
	ds_read_b32 v46, v187 offset:152
	s_waitcnt lgkmcnt(0)
	v_pk_fma_f32 v[48:49], v[46:47], v[82:83], 0 op_sel_hi:[0,1,0] neg_lo:[1,0,0] neg_hi:[1,0,0]
	v_pk_fma_f32 v[46:47], v[46:47], v[84:85], 0 op_sel_hi:[0,1,0] neg_lo:[1,0,0] neg_hi:[1,0,0]
	v_cvt_pk_bf16_f32 v48, v48, v49
	v_cvt_pk_bf16_f32 v49, v46, v47
	ds_write_b64 v186, v[48:49] offset:1632
	ds_read_b32 v46, v187 offset:160
	s_waitcnt lgkmcnt(0)
	v_pk_fma_f32 v[48:49], v[46:47], v[62:63], 0 op_sel_hi:[0,1,0] neg_lo:[1,0,0] neg_hi:[1,0,0]
	v_pk_fma_f32 v[46:47], v[46:47], v[64:65], 0 op_sel_hi:[0,1,0] neg_lo:[1,0,0] neg_hi:[1,0,0]
	v_cvt_pk_bf16_f32 v48, v48, v49
	v_cvt_pk_bf16_f32 v49, v46, v47
	ds_write_b64 v186, v[48:49] offset:2176
	ds_read_b32 v46, v187 offset:168
	s_waitcnt lgkmcnt(0)
	v_pk_fma_f32 v[42:43], v[46:47], v[42:43], 0 op_sel_hi:[0,1,0] neg_lo:[1,0,0] neg_hi:[1,0,0]
	v_pk_fma_f32 v[44:45], v[46:47], v[44:45], 0 op_sel_hi:[0,1,0] neg_lo:[1,0,0] neg_hi:[1,0,0]
	v_cvt_pk_bf16_f32 v42, v42, v43
	v_cvt_pk_bf16_f32 v43, v44, v45
	ds_write_b64 v186, v[42:43] offset:2720
	ds_read_b32 v42, v187 offset:176
	s_waitcnt lgkmcnt(0)
	v_pk_fma_f32 v[38:39], v[42:43], v[38:39], 0 op_sel_hi:[0,1,0] neg_lo:[1,0,0] neg_hi:[1,0,0]
	v_pk_fma_f32 v[40:41], v[42:43], v[40:41], 0 op_sel_hi:[0,1,0] neg_lo:[1,0,0] neg_hi:[1,0,0]
	v_cvt_pk_bf16_f32 v38, v38, v39
	v_cvt_pk_bf16_f32 v39, v40, v41
	ds_write_b64 v186, v[38:39] offset:3264
	ds_read_b32 v38, v187 offset:184
	s_waitcnt lgkmcnt(0)
	v_pk_fma_f32 v[34:35], v[38:39], v[34:35], 0 op_sel_hi:[0,1,0] neg_lo:[1,0,0] neg_hi:[1,0,0]
	v_pk_fma_f32 v[36:37], v[38:39], v[36:37], 0 op_sel_hi:[0,1,0] neg_lo:[1,0,0] neg_hi:[1,0,0]
	v_cvt_pk_bf16_f32 v34, v34, v35
	v_cvt_pk_bf16_f32 v35, v36, v37
	ds_write_b64 v186, v[34:35] offset:3808
	ds_read_b128 a[224:227], v1
	ds_read_b128 a[228:231], v1 offset:64
	ds_read_b128 a[232:235], v1 offset:128
	ds_read_b128 a[236:239], v1 offset:192
	v_lshl_add_u64 v[34:35], v[168:169], 0, s[20:21]
	v_lshl_add_u64 v[36:37], v[170:171], 0, s[20:21]
	v_lshl_add_u64 v[38:39], v[172:173], 0, s[20:21]
	v_lshl_add_u64 v[40:41], v[174:175], 0, s[20:21]
	v_lshl_add_u64 v[42:43], v[176:177], 0, s[20:21]
	v_lshl_add_u64 v[44:45], v[178:179], 0, s[20:21]
	v_lshl_add_u64 v[58:59], v[180:181], 0, s[20:21]
	v_lshl_add_u64 v[60:61], v[182:183], 0, s[20:21]
	global_load_dwordx4 v[122:125], v[34:35], off nt
	global_load_dwordx4 v[106:109], v[36:37], off nt
	global_load_dwordx4 v[94:97], v[38:39], off nt
	global_load_dwordx4 v[82:85], v[40:41], off nt
	global_load_dwordx4 v[46:49], v[42:43], off nt
	s_nop 0
	global_load_dwordx4 v[42:45], v[44:45], off nt
	s_nop 0
	global_load_dwordx4 v[38:41], v[58:59], off nt
	global_load_dwordx4 v[34:37], v[60:61], off nt
	v_mov_b32_e32 v98, v133
	s_waitcnt vmcnt(23)
	s_waitcnt vmcnt(22)
	s_waitcnt vmcnt(21)
	s_waitcnt vmcnt(20)
	s_waitcnt vmcnt(19)
	s_waitcnt vmcnt(18)
	s_waitcnt vmcnt(17)
	s_waitcnt vmcnt(16)
	ds_read_b32 v58, v187
	v_add_u32_e32 v99, 1, v98
	v_cmp_eq_u32_e32 vcc, v98, v132
	s_nop 1
	v_cndmask_b32_e64 v60, 0, 1.0, vcc
	v_cmp_eq_u32_e32 vcc, v99, v132
	s_nop 1
	v_cndmask_b32_e64 v61, 0, 1.0, vcc
	s_waitcnt lgkmcnt(0)
	v_pk_fma_f32 v[62:63], v[58:59], v[90:91], v[60:61] op_sel_hi:[0,1,1] neg_lo:[1,0,0] neg_hi:[1,0,0]
	v_add_u32_e32 v90, 3, v98
	v_add_u32_e32 v91, 2, v98
	v_cmp_eq_u32_e32 vcc, v90, v132
	v_cvt_pk_bf16_f32 v62, v62, v63
	s_nop 0
	v_cndmask_b32_e64 v65, 0, 1.0, vcc
	v_cmp_eq_u32_e32 vcc, v91, v132
	s_nop 1
	v_cndmask_b32_e64 v64, 0, 1.0, vcc
	v_pk_fma_f32 v[58:59], v[58:59], v[92:93], v[64:65] op_sel_hi:[0,1,1] neg_lo:[1,0,0] neg_hi:[1,0,0]
	v_cvt_pk_bf16_f32 v63, v58, v59
	ds_write_b64 v186, v[62:63]
	ds_read_b32 v58, v187 offset:8
	v_cmp_eq_u32_e32 vcc, v98, v193
	s_nop 1
	v_cndmask_b32_e64 v62, 0, 1.0, vcc
	v_cmp_eq_u32_e32 vcc, v99, v193
	s_nop 1
	v_cndmask_b32_e64 v63, 0, 1.0, vcc
	v_cmp_eq_u32_e32 vcc, v90, v193
	s_waitcnt lgkmcnt(0)
	v_pk_fma_f32 v[62:63], v[58:59], v[86:87], v[62:63] op_sel_hi:[0,1,1] neg_lo:[1,0,0] neg_hi:[1,0,0]
	v_cvt_pk_bf16_f32 v62, v62, v63
	v_cndmask_b32_e64 v61, 0, 1.0, vcc
	v_pk_fma_f32 v[58:59], v[58:59], v[88:89], v[60:61] op_sel_hi:[0,1,1] neg_lo:[1,0,0] neg_hi:[1,0,0]
	v_cvt_pk_bf16_f32 v63, v58, v59
	ds_write_b64 v186, v[62:63] offset:544
	ds_read_b32 v58, v187 offset:16
	v_cmp_eq_u32_e32 vcc, v98, v192
	s_nop 1
	v_cndmask_b32_e64 v60, 0, 1.0, vcc
	v_cmp_eq_u32_e32 vcc, v99, v192
	s_nop 1
	v_cndmask_b32_e64 v61, 0, 1.0, vcc
	v_cmp_eq_u32_e32 vcc, v90, v192
	s_waitcnt lgkmcnt(0)
	v_pk_fma_f32 v[54:55], v[58:59], v[54:55], v[60:61] op_sel_hi:[0,1,1] neg_lo:[1,0,0] neg_hi:[1,0,0]
	v_cvt_pk_bf16_f32 v54, v54, v55
	v_cndmask_b32_e64 v61, 0, 1.0, vcc
	v_cmp_eq_u32_e32 vcc, v91, v192
	s_nop 1
	v_cndmask_b32_e64 v60, 0, 1.0, vcc
	v_pk_fma_f32 v[56:57], v[58:59], v[56:57], v[60:61] op_sel_hi:[0,1,1] neg_lo:[1,0,0] neg_hi:[1,0,0]
	v_cvt_pk_bf16_f32 v55, v56, v57
	ds_write_b64 v186, v[54:55] offset:1088
	ds_read_b32 v54, v187 offset:24
	v_cmp_eq_u32_e32 vcc, v98, v190
	s_nop 1
	v_cndmask_b32_e64 v56, 0, 1.0, vcc
	v_cmp_eq_u32_e32 vcc, v99, v190
	s_nop 1
	v_cndmask_b32_e64 v57, 0, 1.0, vcc
	v_cmp_eq_u32_e32 vcc, v90, v190
	s_waitcnt lgkmcnt(0)
	v_pk_fma_f32 v[50:51], v[54:55], v[50:51], v[56:57] op_sel_hi:[0,1,1] neg_lo:[1,0,0] neg_hi:[1,0,0]
	v_cvt_pk_bf16_f32 v50, v50, v51
	v_cndmask_b32_e64 v57, 0, 1.0, vcc
	v_cmp_eq_u32_e32 vcc, v91, v190
	s_nop 1
	v_cndmask_b32_e64 v56, 0, 1.0, vcc
	v_pk_fma_f32 v[52:53], v[54:55], v[52:53], v[56:57] op_sel_hi:[0,1,1] neg_lo:[1,0,0] neg_hi:[1,0,0]
	v_cvt_pk_bf16_f32 v51, v52, v53
	ds_write_b64 v186, v[50:51] offset:1632
	ds_read_b32 v50, v187 offset:32
	v_cmp_eq_u32_e32 vcc, v98, v149
	s_nop 1
	v_cndmask_b32_e64 v52, 0, 1.0, vcc
	v_cmp_eq_u32_e32 vcc, v99, v149
	s_nop 1
	v_cndmask_b32_e64 v53, 0, 1.0, vcc
	v_cmp_eq_u32_e32 vcc, v90, v149
	s_waitcnt lgkmcnt(0)
	v_pk_fma_f32 v[14:15], v[50:51], v[14:15], v[52:53] op_sel_hi:[0,1,1] neg_lo:[1,0,0] neg_hi:[1,0,0]
	v_cvt_pk_bf16_f32 v14, v14, v15
	v_cndmask_b32_e64 v53, 0, 1.0, vcc
	v_cmp_eq_u32_e32 vcc, v91, v149
	s_nop 1
	v_cndmask_b32_e64 v52, 0, 1.0, vcc
	v_pk_fma_f32 v[16:17], v[50:51], v[16:17], v[52:53] op_sel_hi:[0,1,1] neg_lo:[1,0,0] neg_hi:[1,0,0]
	v_cvt_pk_bf16_f32 v15, v16, v17
	ds_write_b64 v186, v[14:15] offset:2176
	ds_read_b32 v14, v187 offset:40
	v_cmp_eq_u32_e32 vcc, v98, v148
	s_nop 1
	v_cndmask_b32_e64 v16, 0, 1.0, vcc
	v_cmp_eq_u32_e32 vcc, v99, v148
	s_nop 1
	v_cndmask_b32_e64 v17, 0, 1.0, vcc
	v_cmp_eq_u32_e32 vcc, v90, v148
	s_waitcnt lgkmcnt(0)
	v_pk_fma_f32 v[10:11], v[14:15], v[10:11], v[16:17] op_sel_hi:[0,1,1] neg_lo:[1,0,0] neg_hi:[1,0,0]
	v_cvt_pk_bf16_f32 v10, v10, v11
	v_cndmask_b32_e64 v17, 0, 1.0, vcc
	v_cmp_eq_u32_e32 vcc, v91, v148
	s_nop 1
	v_cndmask_b32_e64 v16, 0, 1.0, vcc
	v_pk_fma_f32 v[12:13], v[14:15], v[12:13], v[16:17] op_sel_hi:[0,1,1] neg_lo:[1,0,0] neg_hi:[1,0,0]
	v_cvt_pk_bf16_f32 v11, v12, v13
	ds_write_b64 v186, v[10:11] offset:2720
	ds_read_b32 v10, v187 offset:48
	v_cmp_eq_u32_e32 vcc, v98, v147
	s_nop 1
	v_cndmask_b32_e64 v12, 0, 1.0, vcc
	v_cmp_eq_u32_e32 vcc, v99, v147
	s_nop 1
	v_cndmask_b32_e64 v13, 0, 1.0, vcc
	v_cmp_eq_u32_e32 vcc, v90, v147
	s_waitcnt lgkmcnt(0)
	v_pk_fma_f32 v[6:7], v[10:11], v[6:7], v[12:13] op_sel_hi:[0,1,1] neg_lo:[1,0,0] neg_hi:[1,0,0]
	v_cvt_pk_bf16_f32 v6, v6, v7
	v_cndmask_b32_e64 v13, 0, 1.0, vcc
	v_cmp_eq_u32_e32 vcc, v91, v147
	s_nop 1
	v_cndmask_b32_e64 v12, 0, 1.0, vcc
	v_pk_fma_f32 v[8:9], v[10:11], v[8:9], v[12:13] op_sel_hi:[0,1,1] neg_lo:[1,0,0] neg_hi:[1,0,0]
	v_cvt_pk_bf16_f32 v7, v8, v9
	ds_write_b64 v186, v[6:7] offset:3264
	ds_read_b32 v6, v187 offset:56
	v_cmp_eq_u32_e32 vcc, v98, v146
	s_nop 1
	v_cndmask_b32_e64 v8, 0, 1.0, vcc
	v_cmp_eq_u32_e32 vcc, v99, v146
	s_nop 1
	v_cndmask_b32_e64 v9, 0, 1.0, vcc
	v_cmp_eq_u32_e32 vcc, v90, v146
	s_waitcnt lgkmcnt(0)
	v_pk_fma_f32 v[2:3], v[6:7], v[2:3], v[8:9] op_sel_hi:[0,1,1] neg_lo:[1,0,0] neg_hi:[1,0,0]
	v_cvt_pk_bf16_f32 v2, v2, v3
	v_cndmask_b32_e64 v9, 0, 1.0, vcc
	v_cmp_eq_u32_e32 vcc, v91, v146
	s_nop 1
	v_cndmask_b32_e64 v8, 0, 1.0, vcc
	v_pk_fma_f32 v[4:5], v[6:7], v[4:5], v[8:9] op_sel_hi:[0,1,1] neg_lo:[1,0,0] neg_hi:[1,0,0]
	v_cvt_pk_bf16_f32 v3, v4, v5
	ds_write_b64 v186, v[2:3] offset:3808
	ds_read_b128 v[2:5], v1
	ds_read_b128 v[6:9], v1 offset:64
	ds_read_b128 v[10:13], v1 offset:128
	ds_read_b128 v[14:17], v1 offset:192
	global_load_dwordx4 v[118:121], v[118:119], off offset:512 nt
	s_nop 0
	global_load_dwordx4 v[110:113], v[126:127], off offset:512 nt
	global_load_dwordx4 v[98:101], v[128:129], off offset:512 nt
	global_load_dwordx4 v[86:89], v[134:135], off offset:512 nt
	global_load_dwordx4 v[62:65], v[136:137], off offset:512 nt
	global_load_dwordx4 v[58:61], v[138:139], off offset:512 nt
	global_load_dwordx4 v[54:57], v[140:141], off offset:512 nt
	global_load_dwordx4 v[50:53], v[142:143], off offset:512 nt
	v_mov_b32_e32 v91, v133
	s_waitcnt vmcnt(23)
	s_waitcnt vmcnt(22)
	s_waitcnt vmcnt(21)
	s_waitcnt vmcnt(20)
	s_waitcnt vmcnt(19)
	s_waitcnt vmcnt(18)
	s_waitcnt vmcnt(17)
	s_waitcnt vmcnt(16)
	ds_read_b32 v90, v187 offset:64
	v_or_b32_e32 v138, 16, v132
	v_add_u32_e32 v102, 1, v91
	v_cmp_eq_u32_e32 vcc, v91, v138
	v_add_u32_e32 v103, 3, v91
	v_add_u32_e32 v104, 2, v91
	v_cndmask_b32_e64 v92, 0, 1.0, vcc
	v_cmp_eq_u32_e32 vcc, v102, v138
	v_or_b32_e32 v139, 18, v132
	v_or_b32_e32 v140, 20, v132
	v_cndmask_b32_e64 v93, 0, 1.0, vcc
	v_cmp_eq_u32_e32 vcc, v103, v138
	s_waitcnt lgkmcnt(0)
	v_pk_fma_f32 v[78:79], v[90:91], v[78:79], v[92:93] op_sel_hi:[0,1,1] neg_lo:[1,0,0] neg_hi:[1,0,0]
	v_cvt_pk_bf16_f32 v78, v78, v79
	v_cndmask_b32_e64 v93, 0, 1.0, vcc
	v_cmp_eq_u32_e32 vcc, v104, v138
	v_or_b32_e32 v141, 22, v132
	v_or_b32_e32 v142, 24, v132
	v_cndmask_b32_e64 v92, 0, 1.0, vcc
	v_pk_fma_f32 v[80:81], v[90:91], v[80:81], v[92:93] op_sel_hi:[0,1,1] neg_lo:[1,0,0] neg_hi:[1,0,0]
	v_cvt_pk_bf16_f32 v79, v80, v81
	ds_write_b64 v186, v[78:79]
	ds_read_b32 v78, v187 offset:72
	v_cmp_eq_u32_e32 vcc, v91, v139
	v_or_b32_e32 v143, 26, v132
	v_or_b32_e32 v144, 28, v132
	v_cndmask_b32_e64 v80, 0, 1.0, vcc
	v_cmp_eq_u32_e32 vcc, v102, v139
	v_or_b32_e32 v145, 30, v132
	s_nop 0
	v_cndmask_b32_e64 v81, 0, 1.0, vcc
	v_cmp_eq_u32_e32 vcc, v103, v139
	s_waitcnt lgkmcnt(0)
	v_pk_fma_f32 v[74:75], v[78:79], v[74:75], v[80:81] op_sel_hi:[0,1,1] neg_lo:[1,0,0] neg_hi:[1,0,0]
	v_cvt_pk_bf16_f32 v74, v74, v75
	v_cndmask_b32_e64 v81, 0, 1.0, vcc
	v_cmp_eq_u32_e32 vcc, v104, v139
	s_nop 1
	v_cndmask_b32_e64 v80, 0, 1.0, vcc
	v_pk_fma_f32 v[76:77], v[78:79], v[76:77], v[80:81] op_sel_hi:[0,1,1] neg_lo:[1,0,0] neg_hi:[1,0,0]
	v_cvt_pk_bf16_f32 v75, v76, v77
	ds_write_b64 v186, v[74:75] offset:544
	ds_read_b32 v74, v187 offset:80
	v_cmp_eq_u32_e32 vcc, v91, v140
	s_nop 1
	v_cndmask_b32_e64 v76, 0, 1.0, vcc
	v_cmp_eq_u32_e32 vcc, v102, v140
	s_nop 1
	v_cndmask_b32_e64 v77, 0, 1.0, vcc
	v_cmp_eq_u32_e32 vcc, v103, v140
	s_waitcnt lgkmcnt(0)
	v_pk_fma_f32 v[70:71], v[74:75], v[70:71], v[76:77] op_sel_hi:[0,1,1] neg_lo:[1,0,0] neg_hi:[1,0,0]
	v_cvt_pk_bf16_f32 v70, v70, v71
	v_cndmask_b32_e64 v77, 0, 1.0, vcc
	v_cmp_eq_u32_e32 vcc, v104, v140
	s_nop 1
	v_cndmask_b32_e64 v76, 0, 1.0, vcc
	v_pk_fma_f32 v[72:73], v[74:75], v[72:73], v[76:77] op_sel_hi:[0,1,1] neg_lo:[1,0,0] neg_hi:[1,0,0]
	v_cvt_pk_bf16_f32 v71, v72, v73
	ds_write_b64 v186, v[70:71] offset:1088
	ds_read_b32 v70, v187 offset:88
	v_cmp_eq_u32_e32 vcc, v91, v141
	s_nop 1
	v_cndmask_b32_e64 v72, 0, 1.0, vcc
	v_cmp_eq_u32_e32 vcc, v102, v141
	s_nop 1
	v_cndmask_b32_e64 v73, 0, 1.0, vcc
	v_cmp_eq_u32_e32 vcc, v103, v141
	s_waitcnt lgkmcnt(0)
	v_pk_fma_f32 v[66:67], v[70:71], v[66:67], v[72:73] op_sel_hi:[0,1,1] neg_lo:[1,0,0] neg_hi:[1,0,0]
	v_cvt_pk_bf16_f32 v66, v66, v67
	v_cndmask_b32_e64 v73, 0, 1.0, vcc
	v_cmp_eq_u32_e32 vcc, v104, v141
	s_nop 1
	v_cndmask_b32_e64 v72, 0, 1.0, vcc
	v_pk_fma_f32 v[68:69], v[70:71], v[68:69], v[72:73] op_sel_hi:[0,1,1] neg_lo:[1,0,0] neg_hi:[1,0,0]
	v_cvt_pk_bf16_f32 v67, v68, v69
	ds_write_b64 v186, v[66:67] offset:1632
	ds_read_b32 v66, v187 offset:96
	v_cmp_eq_u32_e32 vcc, v91, v142
	s_nop 1
	v_cndmask_b32_e64 v68, 0, 1.0, vcc
	v_cmp_eq_u32_e32 vcc, v102, v142
	s_nop 1
	v_cndmask_b32_e64 v69, 0, 1.0, vcc
	v_cmp_eq_u32_e32 vcc, v103, v142
	s_waitcnt lgkmcnt(0)
	v_pk_fma_f32 v[30:31], v[66:67], v[30:31], v[68:69] op_sel_hi:[0,1,1] neg_lo:[1,0,0] neg_hi:[1,0,0]
	v_cvt_pk_bf16_f32 v30, v30, v31
	v_cndmask_b32_e64 v69, 0, 1.0, vcc
	v_cmp_eq_u32_e32 vcc, v104, v142
	s_nop 1
	v_cndmask_b32_e64 v68, 0, 1.0, vcc
	v_pk_fma_f32 v[32:33], v[66:67], v[32:33], v[68:69] op_sel_hi:[0,1,1] neg_lo:[1,0,0] neg_hi:[1,0,0]
	v_cvt_pk_bf16_f32 v31, v32, v33
	ds_write_b64 v186, v[30:31] offset:2176
	ds_read_b32 v30, v187 offset:104
	v_cmp_eq_u32_e32 vcc, v91, v143
	s_nop 1
	v_cndmask_b32_e64 v32, 0, 1.0, vcc
	v_cmp_eq_u32_e32 vcc, v102, v143
	s_nop 1
	v_cndmask_b32_e64 v33, 0, 1.0, vcc
	v_cmp_eq_u32_e32 vcc, v103, v143
	s_waitcnt lgkmcnt(0)
	v_pk_fma_f32 v[26:27], v[30:31], v[26:27], v[32:33] op_sel_hi:[0,1,1] neg_lo:[1,0,0] neg_hi:[1,0,0]
	v_cvt_pk_bf16_f32 v26, v26, v27
	v_cndmask_b32_e64 v33, 0, 1.0, vcc
	v_cmp_eq_u32_e32 vcc, v104, v143
	s_nop 1
	v_cndmask_b32_e64 v32, 0, 1.0, vcc
	v_pk_fma_f32 v[28:29], v[30:31], v[28:29], v[32:33] op_sel_hi:[0,1,1] neg_lo:[1,0,0] neg_hi:[1,0,0]
	v_cvt_pk_bf16_f32 v27, v28, v29
	ds_write_b64 v186, v[26:27] offset:2720
	ds_read_b32 v26, v187 offset:112
	v_cmp_eq_u32_e32 vcc, v91, v144
	s_nop 1
	v_cndmask_b32_e64 v28, 0, 1.0, vcc
	v_cmp_eq_u32_e32 vcc, v102, v144
	s_nop 1
	v_cndmask_b32_e64 v29, 0, 1.0, vcc
	v_cmp_eq_u32_e32 vcc, v103, v144
	s_waitcnt lgkmcnt(0)
	v_pk_fma_f32 v[22:23], v[26:27], v[22:23], v[28:29] op_sel_hi:[0,1,1] neg_lo:[1,0,0] neg_hi:[1,0,0]
	v_cvt_pk_bf16_f32 v22, v22, v23
	v_cndmask_b32_e64 v29, 0, 1.0, vcc
	v_cmp_eq_u32_e32 vcc, v104, v144
	s_nop 1
	v_cndmask_b32_e64 v28, 0, 1.0, vcc
	v_pk_fma_f32 v[24:25], v[26:27], v[24:25], v[28:29] op_sel_hi:[0,1,1] neg_lo:[1,0,0] neg_hi:[1,0,0]
	v_cvt_pk_bf16_f32 v23, v24, v25
	ds_write_b64 v186, v[22:23] offset:3264
	ds_read_b32 v22, v187 offset:120
	v_cmp_eq_u32_e32 vcc, v91, v145
	s_nop 1
	v_cndmask_b32_e64 v24, 0, 1.0, vcc
	v_cmp_eq_u32_e32 vcc, v102, v145
	s_nop 1
	v_cndmask_b32_e64 v25, 0, 1.0, vcc
	v_cmp_eq_u32_e32 vcc, v103, v145
	s_waitcnt lgkmcnt(0)
	v_pk_fma_f32 v[18:19], v[22:23], v[18:19], v[24:25] op_sel_hi:[0,1,1] neg_lo:[1,0,0] neg_hi:[1,0,0]
	v_cvt_pk_bf16_f32 v18, v18, v19
	v_cndmask_b32_e64 v25, 0, 1.0, vcc
	v_cmp_eq_u32_e32 vcc, v104, v145
	s_nop 1
	v_cndmask_b32_e64 v24, 0, 1.0, vcc
	v_pk_fma_f32 v[20:21], v[22:23], v[20:21], v[24:25] op_sel_hi:[0,1,1] neg_lo:[1,0,0] neg_hi:[1,0,0]
	v_cvt_pk_bf16_f32 v19, v20, v21
	ds_write_b64 v186, v[18:19] offset:3808
	ds_read_b128 v[18:21], v1
	ds_read_b128 v[22:25], v1 offset:64
	ds_read_b128 v[26:29], v1 offset:128
	ds_read_b128 v[30:33], v1 offset:192
	v_lshl_add_u64 v[66:67], v[150:151], 0, s[8:9]
	v_lshl_add_u64 v[68:69], v[152:153], 0, s[8:9]
	v_lshl_add_u64 v[70:71], v[156:157], 0, s[8:9]
	v_lshl_add_u64 v[72:73], v[158:159], 0, s[8:9]
	v_lshl_add_u64 v[74:75], v[160:161], 0, s[8:9]
	v_lshl_add_u64 v[76:77], v[162:163], 0, s[8:9]
	v_lshl_add_u64 v[134:135], v[164:165], 0, s[8:9]
	v_lshl_add_u64 v[136:137], v[166:167], 0, s[8:9]
	global_load_dwordx4 v[126:129], v[66:67], off nt
	global_load_dwordx4 v[114:117], v[68:69], off nt
	global_load_dwordx4 v[102:105], v[70:71], off nt
	global_load_dwordx4 v[90:93], v[72:73], off nt
	global_load_dwordx4 v[78:81], v[74:75], off nt
	s_nop 0
	global_load_dwordx4 v[74:77], v[76:77], off nt
	s_nop 0
	global_load_dwordx4 v[70:73], v[134:135], off nt
	global_load_dwordx4 v[66:69], v[136:137], off nt
	s_waitcnt vmcnt(23)
	s_waitcnt vmcnt(22)
	s_waitcnt vmcnt(21)
	s_waitcnt vmcnt(20)
	s_waitcnt vmcnt(19)
	s_waitcnt vmcnt(18)
	s_waitcnt vmcnt(17)
	s_waitcnt vmcnt(16)
	ds_read_b32 v134, v187 offset:128
	v_or_b32_e32 v194, 32, v132
	v_add_u32_e32 v135, 1, v133
	v_cmp_eq_u32_e32 vcc, v133, v194
	v_add_u32_e32 v202, 3, v133
	v_add_u32_e32 v203, 2, v133
	v_cndmask_b32_e64 v136, 0, 1.0, vcc
	v_cmp_eq_u32_e32 vcc, v135, v194
	v_or_b32_e32 v195, 34, v132
	v_or_b32_e32 v196, 36, v132
	v_cndmask_b32_e64 v137, 0, 1.0, vcc
	v_cmp_eq_u32_e32 vcc, v202, v194
	s_waitcnt lgkmcnt(0)
	v_pk_fma_f32 v[122:123], v[134:135], v[122:123], v[136:137] op_sel_hi:[0,1,1] neg_lo:[1,0,0] neg_hi:[1,0,0]
	v_cvt_pk_bf16_f32 v122, v122, v123
	v_cndmask_b32_e64 v137, 0, 1.0, vcc
	v_cmp_eq_u32_e32 vcc, v203, v194
	v_or_b32_e32 v197, 38, v132
	v_or_b32_e32 v198, 40, v132
	v_cndmask_b32_e64 v136, 0, 1.0, vcc
	v_pk_fma_f32 v[124:125], v[134:135], v[124:125], v[136:137] op_sel_hi:[0,1,1] neg_lo:[1,0,0] neg_hi:[1,0,0]
	v_cvt_pk_bf16_f32 v123, v124, v125
	ds_write_b64 v186, v[122:123]
	ds_read_b32 v122, v187 offset:136
	v_cmp_eq_u32_e32 vcc, v133, v195
	v_or_b32_e32 v199, 42, v132
	v_or_b32_e32 v200, 44, v132
	v_cndmask_b32_e64 v124, 0, 1.0, vcc
	v_cmp_eq_u32_e32 vcc, v135, v195
	v_or_b32_e32 v201, 46, v132
	s_nop 0
	v_cndmask_b32_e64 v125, 0, 1.0, vcc
	v_cmp_eq_u32_e32 vcc, v202, v195
	s_waitcnt lgkmcnt(0)
	v_pk_fma_f32 v[106:107], v[122:123], v[106:107], v[124:125] op_sel_hi:[0,1,1] neg_lo:[1,0,0] neg_hi:[1,0,0]
	v_cvt_pk_bf16_f32 v106, v106, v107
	v_cndmask_b32_e64 v125, 0, 1.0, vcc
	v_cmp_eq_u32_e32 vcc, v203, v195
	s_nop 1
	v_cndmask_b32_e64 v124, 0, 1.0, vcc
	v_pk_fma_f32 v[108:109], v[122:123], v[108:109], v[124:125] op_sel_hi:[0,1,1] neg_lo:[1,0,0] neg_hi:[1,0,0]
	v_cvt_pk_bf16_f32 v107, v108, v109
	ds_write_b64 v186, v[106:107] offset:544
	ds_read_b32 v106, v187 offset:144
	v_cmp_eq_u32_e32 vcc, v133, v196
	s_nop 1
	v_cndmask_b32_e64 v108, 0, 1.0, vcc
	v_cmp_eq_u32_e32 vcc, v135, v196
	s_nop 1
	v_cndmask_b32_e64 v109, 0, 1.0, vcc
	v_cmp_eq_u32_e32 vcc, v202, v196
	s_waitcnt lgkmcnt(0)
	v_pk_fma_f32 v[94:95], v[106:107], v[94:95], v[108:109] op_sel_hi:[0,1,1] neg_lo:[1,0,0] neg_hi:[1,0,0]
	v_cvt_pk_bf16_f32 v94, v94, v95
	v_cndmask_b32_e64 v109, 0, 1.0, vcc
	v_cmp_eq_u32_e32 vcc, v203, v196
	s_nop 1
	v_cndmask_b32_e64 v108, 0, 1.0, vcc
	v_pk_fma_f32 v[96:97], v[106:107], v[96:97], v[108:109] op_sel_hi:[0,1,1] neg_lo:[1,0,0] neg_hi:[1,0,0]
	v_cvt_pk_bf16_f32 v95, v96, v97
	ds_write_b64 v186, v[94:95] offset:1088
	ds_read_b32 v94, v187 offset:152
	v_cmp_eq_u32_e32 vcc, v133, v197
	s_nop 1
	v_cndmask_b32_e64 v96, 0, 1.0, vcc
	v_cmp_eq_u32_e32 vcc, v135, v197
	s_nop 1
	v_cndmask_b32_e64 v97, 0, 1.0, vcc
	v_cmp_eq_u32_e32 vcc, v202, v197
	s_waitcnt lgkmcnt(0)
	v_pk_fma_f32 v[82:83], v[94:95], v[82:83], v[96:97] op_sel_hi:[0,1,1] neg_lo:[1,0,0] neg_hi:[1,0,0]
	v_cvt_pk_bf16_f32 v82, v82, v83
	v_cndmask_b32_e64 v97, 0, 1.0, vcc
	v_cmp_eq_u32_e32 vcc, v203, v197
	s_nop 1
	v_cndmask_b32_e64 v96, 0, 1.0, vcc
	v_pk_fma_f32 v[84:85], v[94:95], v[84:85], v[96:97] op_sel_hi:[0,1,1] neg_lo:[1,0,0] neg_hi:[1,0,0]
	v_cvt_pk_bf16_f32 v83, v84, v85
	ds_write_b64 v186, v[82:83] offset:1632
	ds_read_b32 v82, v187 offset:160
	v_cmp_eq_u32_e32 vcc, v133, v198
	s_nop 1
	v_cndmask_b32_e64 v84, 0, 1.0, vcc
	v_cmp_eq_u32_e32 vcc, v135, v198
	s_nop 1
	v_cndmask_b32_e64 v85, 0, 1.0, vcc
	v_cmp_eq_u32_e32 vcc, v202, v198
	s_waitcnt lgkmcnt(0)
	v_pk_fma_f32 v[46:47], v[82:83], v[46:47], v[84:85] op_sel_hi:[0,1,1] neg_lo:[1,0,0] neg_hi:[1,0,0]
	v_cvt_pk_bf16_f32 v46, v46, v47
	v_cndmask_b32_e64 v85, 0, 1.0, vcc
	v_cmp_eq_u32_e32 vcc, v203, v198
	s_nop 1
	v_cndmask_b32_e64 v84, 0, 1.0, vcc
	v_pk_fma_f32 v[48:49], v[82:83], v[48:49], v[84:85] op_sel_hi:[0,1,1] neg_lo:[1,0,0] neg_hi:[1,0,0]
	v_cvt_pk_bf16_f32 v47, v48, v49
	ds_write_b64 v186, v[46:47] offset:2176
	ds_read_b32 v46, v187 offset:168
	v_cmp_eq_u32_e32 vcc, v133, v199
	s_nop 1
	v_cndmask_b32_e64 v48, 0, 1.0, vcc
	v_cmp_eq_u32_e32 vcc, v135, v199
	s_nop 1
	v_cndmask_b32_e64 v49, 0, 1.0, vcc
	v_cmp_eq_u32_e32 vcc, v202, v199
	s_waitcnt lgkmcnt(0)
	v_pk_fma_f32 v[42:43], v[46:47], v[42:43], v[48:49] op_sel_hi:[0,1,1] neg_lo:[1,0,0] neg_hi:[1,0,0]
	v_cvt_pk_bf16_f32 v42, v42, v43
	v_cndmask_b32_e64 v49, 0, 1.0, vcc
	v_cmp_eq_u32_e32 vcc, v203, v199
	s_nop 1
	v_cndmask_b32_e64 v48, 0, 1.0, vcc
	v_pk_fma_f32 v[44:45], v[46:47], v[44:45], v[48:49] op_sel_hi:[0,1,1] neg_lo:[1,0,0] neg_hi:[1,0,0]
	v_cvt_pk_bf16_f32 v43, v44, v45
	ds_write_b64 v186, v[42:43] offset:2720
	ds_read_b32 v42, v187 offset:176
	v_cmp_eq_u32_e32 vcc, v133, v200
	s_nop 1
	v_cndmask_b32_e64 v44, 0, 1.0, vcc
	v_cmp_eq_u32_e32 vcc, v135, v200
	s_nop 1
	v_cndmask_b32_e64 v45, 0, 1.0, vcc
	v_cmp_eq_u32_e32 vcc, v202, v200
	s_waitcnt lgkmcnt(0)
	v_pk_fma_f32 v[38:39], v[42:43], v[38:39], v[44:45] op_sel_hi:[0,1,1] neg_lo:[1,0,0] neg_hi:[1,0,0]
	v_cvt_pk_bf16_f32 v38, v38, v39
	v_cndmask_b32_e64 v45, 0, 1.0, vcc
	v_cmp_eq_u32_e32 vcc, v203, v200
	s_nop 1
	v_cndmask_b32_e64 v44, 0, 1.0, vcc
	v_pk_fma_f32 v[40:41], v[42:43], v[40:41], v[44:45] op_sel_hi:[0,1,1] neg_lo:[1,0,0] neg_hi:[1,0,0]
	v_cvt_pk_bf16_f32 v39, v40, v41
	ds_write_b64 v186, v[38:39] offset:3264
	ds_read_b32 v38, v187 offset:184
	v_cmp_eq_u32_e32 vcc, v133, v201
	s_nop 1
	v_cndmask_b32_e64 v40, 0, 1.0, vcc
	v_cmp_eq_u32_e32 vcc, v135, v201
	s_nop 1
	v_cndmask_b32_e64 v41, 0, 1.0, vcc
	v_cmp_eq_u32_e32 vcc, v202, v201
	s_waitcnt lgkmcnt(0)
	v_pk_fma_f32 v[34:35], v[38:39], v[34:35], v[40:41] op_sel_hi:[0,1,1] neg_lo:[1,0,0] neg_hi:[1,0,0]
	v_cvt_pk_bf16_f32 v34, v34, v35
	v_cndmask_b32_e64 v41, 0, 1.0, vcc
	v_cmp_eq_u32_e32 vcc, v203, v201
	s_nop 1
	v_cndmask_b32_e64 v40, 0, 1.0, vcc
	v_pk_fma_f32 v[36:37], v[38:39], v[36:37], v[40:41] op_sel_hi:[0,1,1] neg_lo:[1,0,0] neg_hi:[1,0,0]
	v_cvt_pk_bf16_f32 v35, v36, v37
	ds_write_b64 v186, v[34:35] offset:3808
	ds_read_b128 v[34:37], v1
	ds_read_b128 v[38:41], v1 offset:64
	ds_read_b128 v[42:45], v1 offset:128
	ds_read_b128 v[46:49], v1 offset:192
	v_mov_b32_e32 v106, v189
	s_waitcnt vmcnt(15)
	s_waitcnt vmcnt(14)
	s_waitcnt vmcnt(13)
	s_waitcnt vmcnt(12)
	s_waitcnt vmcnt(11)
	s_waitcnt vmcnt(10)
	s_waitcnt vmcnt(9)
	s_waitcnt vmcnt(8)
	ds_read_b32 v82, v187
	v_add_u32_e32 v107, 1, v106
	v_cmp_eq_u32_e32 vcc, v106, v132
	v_add_u32_e32 v108, 3, v106
	v_add_u32_e32 v109, 2, v106
	v_cndmask_b32_e64 v84, 0, 1.0, vcc
	v_cmp_eq_u32_e32 vcc, v107, v132
	s_nop 1
	v_cndmask_b32_e64 v85, 0, 1.0, vcc
	v_cmp_eq_u32_e32 vcc, v108, v132
	s_waitcnt lgkmcnt(0)
	v_pk_fma_f32 v[94:95], v[82:83], v[118:119], v[84:85] op_sel_hi:[0,1,1] neg_lo:[1,0,0] neg_hi:[1,0,0]
	v_cvt_pk_bf16_f32 v94, v94, v95
	v_cndmask_b32_e64 v97, 0, 1.0, vcc
	v_cmp_eq_u32_e32 vcc, v109, v132
	s_nop 1
	v_cndmask_b32_e64 v96, 0, 1.0, vcc
	v_pk_fma_f32 v[82:83], v[82:83], v[120:121], v[96:97] op_sel_hi:[0,1,1] neg_lo:[1,0,0] neg_hi:[1,0,0]
	v_cvt_pk_bf16_f32 v95, v82, v83
	ds_write_b64 v186, v[94:95]
	ds_read_b32 v82, v187 offset:8
	v_cmp_eq_u32_e32 vcc, v106, v193
	s_nop 1
	v_cndmask_b32_e64 v94, 0, 1.0, vcc
	v_cmp_eq_u32_e32 vcc, v107, v193
	s_nop 1
	v_cndmask_b32_e64 v95, 0, 1.0, vcc
	v_cmp_eq_u32_e32 vcc, v108, v193
	s_waitcnt lgkmcnt(0)
	v_pk_fma_f32 v[94:95], v[82:83], v[110:111], v[94:95] op_sel_hi:[0,1,1] neg_lo:[1,0,0] neg_hi:[1,0,0]
	v_cvt_pk_bf16_f32 v94, v94, v95
	v_cndmask_b32_e64 v85, 0, 1.0, vcc
	v_pk_fma_f32 v[82:83], v[82:83], v[112:113], v[84:85] op_sel_hi:[0,1,1] neg_lo:[1,0,0] neg_hi:[1,0,0]
	v_cvt_pk_bf16_f32 v95, v82, v83
	ds_write_b64 v186, v[94:95] offset:544
	ds_read_b32 v82, v187 offset:16
	v_cmp_eq_u32_e32 vcc, v106, v192
	s_nop 1
	v_cndmask_b32_e64 v84, 0, 1.0, vcc
	v_cmp_eq_u32_e32 vcc, v107, v192
	s_nop 1
	v_cndmask_b32_e64 v85, 0, 1.0, vcc
	v_cmp_eq_u32_e32 vcc, v108, v192
	s_waitcnt lgkmcnt(0)
	v_pk_fma_f32 v[84:85], v[82:83], v[98:99], v[84:85] op_sel_hi:[0,1,1] neg_lo:[1,0,0] neg_hi:[1,0,0]
	v_cvt_pk_bf16_f32 v84, v84, v85
	v_cndmask_b32_e64 v95, 0, 1.0, vcc
	v_cmp_eq_u32_e32 vcc, v109, v192
	s_nop 1
	v_cndmask_b32_e64 v94, 0, 1.0, vcc
	v_pk_fma_f32 v[82:83], v[82:83], v[100:101], v[94:95] op_sel_hi:[0,1,1] neg_lo:[1,0,0] neg_hi:[1,0,0]
	v_cvt_pk_bf16_f32 v85, v82, v83
	ds_write_b64 v186, v[84:85] offset:1088
	ds_read_b32 v82, v187 offset:24
	v_cmp_eq_u32_e32 vcc, v106, v190
	s_nop 1
	v_cndmask_b32_e64 v84, 0, 1.0, vcc
	v_cmp_eq_u32_e32 vcc, v107, v190
	s_nop 1
	v_cndmask_b32_e64 v85, 0, 1.0, vcc
	v_cmp_eq_u32_e32 vcc, v108, v190
	s_waitcnt lgkmcnt(0)
	v_pk_fma_f32 v[84:85], v[82:83], v[86:87], v[84:85] op_sel_hi:[0,1,1] neg_lo:[1,0,0] neg_hi:[1,0,0]
	v_cvt_pk_bf16_f32 v84, v84, v85
	v_cndmask_b32_e64 v87, 0, 1.0, vcc
	v_cmp_eq_u32_e32 vcc, v109, v190
	s_nop 1
	v_cndmask_b32_e64 v86, 0, 1.0, vcc
	v_pk_fma_f32 v[82:83], v[82:83], v[88:89], v[86:87] op_sel_hi:[0,1,1] neg_lo:[1,0,0] neg_hi:[1,0,0]
	v_cvt_pk_bf16_f32 v85, v82, v83
	ds_write_b64 v186, v[84:85] offset:1632
	ds_read_b32 v82, v187 offset:32
	v_cmp_eq_u32_e32 vcc, v106, v149
	s_nop 1
	v_cndmask_b32_e64 v84, 0, 1.0, vcc
	v_cmp_eq_u32_e32 vcc, v107, v149
	s_nop 1
	v_cndmask_b32_e64 v85, 0, 1.0, vcc
	v_cmp_eq_u32_e32 vcc, v108, v149
	s_waitcnt lgkmcnt(0)
	v_pk_fma_f32 v[62:63], v[82:83], v[62:63], v[84:85] op_sel_hi:[0,1,1] neg_lo:[1,0,0] neg_hi:[1,0,0]
	v_cvt_pk_bf16_f32 v62, v62, v63
	v_cndmask_b32_e64 v85, 0, 1.0, vcc
	v_cmp_eq_u32_e32 vcc, v109, v149
	s_nop 1
	v_cndmask_b32_e64 v84, 0, 1.0, vcc
	v_pk_fma_f32 v[64:65], v[82:83], v[64:65], v[84:85] op_sel_hi:[0,1,1] neg_lo:[1,0,0] neg_hi:[1,0,0]
	v_cvt_pk_bf16_f32 v63, v64, v65
	ds_write_b64 v186, v[62:63] offset:2176
	ds_read_b32 v62, v187 offset:40
	v_cmp_eq_u32_e32 vcc, v106, v148
	s_nop 1
	v_cndmask_b32_e64 v64, 0, 1.0, vcc
	v_cmp_eq_u32_e32 vcc, v107, v148
	s_nop 1
	v_cndmask_b32_e64 v65, 0, 1.0, vcc
	v_cmp_eq_u32_e32 vcc, v108, v148
	s_waitcnt lgkmcnt(0)
	v_pk_fma_f32 v[58:59], v[62:63], v[58:59], v[64:65] op_sel_hi:[0,1,1] neg_lo:[1,0,0] neg_hi:[1,0,0]
	v_cvt_pk_bf16_f32 v58, v58, v59
	v_cndmask_b32_e64 v65, 0, 1.0, vcc
	v_cmp_eq_u32_e32 vcc, v109, v148
	s_nop 1
	v_cndmask_b32_e64 v64, 0, 1.0, vcc
	v_pk_fma_f32 v[60:61], v[62:63], v[60:61], v[64:65] op_sel_hi:[0,1,1] neg_lo:[1,0,0] neg_hi:[1,0,0]
	v_cvt_pk_bf16_f32 v59, v60, v61
	ds_write_b64 v186, v[58:59] offset:2720
	ds_read_b32 v58, v187 offset:48
	v_cmp_eq_u32_e32 vcc, v106, v147
	s_nop 1
	v_cndmask_b32_e64 v60, 0, 1.0, vcc
	v_cmp_eq_u32_e32 vcc, v107, v147
	s_nop 1
	v_cndmask_b32_e64 v61, 0, 1.0, vcc
	v_cmp_eq_u32_e32 vcc, v108, v147
	s_waitcnt lgkmcnt(0)
	v_pk_fma_f32 v[54:55], v[58:59], v[54:55], v[60:61] op_sel_hi:[0,1,1] neg_lo:[1,0,0] neg_hi:[1,0,0]
	v_cvt_pk_bf16_f32 v54, v54, v55
	v_cndmask_b32_e64 v61, 0, 1.0, vcc
	v_cmp_eq_u32_e32 vcc, v109, v147
	s_nop 1
	v_cndmask_b32_e64 v60, 0, 1.0, vcc
	v_pk_fma_f32 v[56:57], v[58:59], v[56:57], v[60:61] op_sel_hi:[0,1,1] neg_lo:[1,0,0] neg_hi:[1,0,0]
	v_cvt_pk_bf16_f32 v55, v56, v57
	ds_write_b64 v186, v[54:55] offset:3264
	ds_read_b32 v54, v187 offset:56
	v_cmp_eq_u32_e32 vcc, v106, v146
	s_nop 1
	v_cndmask_b32_e64 v56, 0, 1.0, vcc
	v_cmp_eq_u32_e32 vcc, v107, v146
	s_nop 1
	v_cndmask_b32_e64 v57, 0, 1.0, vcc
	v_cmp_eq_u32_e32 vcc, v108, v146
	s_waitcnt lgkmcnt(0)
	v_pk_fma_f32 v[50:51], v[54:55], v[50:51], v[56:57] op_sel_hi:[0,1,1] neg_lo:[1,0,0] neg_hi:[1,0,0]
	v_cvt_pk_bf16_f32 v50, v50, v51
	v_cndmask_b32_e64 v57, 0, 1.0, vcc
	v_cmp_eq_u32_e32 vcc, v109, v146
	s_nop 1
	v_cndmask_b32_e64 v56, 0, 1.0, vcc
	v_pk_fma_f32 v[52:53], v[54:55], v[52:53], v[56:57] op_sel_hi:[0,1,1] neg_lo:[1,0,0] neg_hi:[1,0,0]
	v_cvt_pk_bf16_f32 v51, v52, v53
	ds_write_b64 v186, v[50:51] offset:3808
	ds_read_b128 v[50:53], v1
	ds_read_b128 v[54:57], v1 offset:64
	ds_read_b128 v[58:61], v1 offset:128
	ds_read_b128 v[62:65], v1 offset:192
	v_lshl_add_u64 v[82:83], v[168:169], 0, s[8:9]
	v_lshl_add_u64 v[84:85], v[170:171], 0, s[8:9]
	v_lshl_add_u64 v[86:87], v[172:173], 0, s[8:9]
	v_lshl_add_u64 v[88:89], v[174:175], 0, s[8:9]
	v_lshl_add_u64 v[94:95], v[176:177], 0, s[8:9]
	v_lshl_add_u64 v[96:97], v[178:179], 0, s[8:9]
	v_lshl_add_u64 v[122:123], v[180:181], 0, s[8:9]
	v_lshl_add_u64 v[124:125], v[182:183], 0, s[8:9]
	global_load_dwordx4 v[134:137], v[82:83], off nt
	global_load_dwordx4 v[118:121], v[84:85], off nt
	global_load_dwordx4 v[110:113], v[86:87], off nt
	global_load_dwordx4 v[106:109], v[88:89], off nt
	global_load_dwordx4 v[98:101], v[94:95], off nt
	s_nop 0
	global_load_dwordx4 v[94:97], v[96:97], off nt
	s_nop 0
	global_load_dwordx4 v[86:89], v[122:123], off nt
	global_load_dwordx4 v[82:85], v[124:125], off nt
	v_mov_b32_e32 v132, v189
	s_waitcnt vmcnt(15)
	s_waitcnt vmcnt(14)
	s_waitcnt vmcnt(13)
	s_waitcnt vmcnt(12)
	s_waitcnt vmcnt(11)
	s_waitcnt vmcnt(10)
	s_waitcnt vmcnt(9)
	s_waitcnt vmcnt(8)
	ds_read_b32 v122, v187 offset:64
	v_add_u32_e32 v133, 1, v132
	v_cmp_eq_u32_e32 vcc, v132, v138
	v_add_u32_e32 v146, 3, v132
	v_add_u32_e32 v147, 2, v132
	v_cndmask_b32_e64 v124, 0, 1.0, vcc
	v_cmp_eq_u32_e32 vcc, v133, v138
	s_nop 1
	v_cndmask_b32_e64 v125, 0, 1.0, vcc
	v_cmp_eq_u32_e32 vcc, v146, v138
	s_waitcnt lgkmcnt(0)
	v_pk_fma_f32 v[124:125], v[122:123], v[126:127], v[124:125] op_sel_hi:[0,1,1] neg_lo:[1,0,0] neg_hi:[1,0,0]
	v_cvt_pk_bf16_f32 v124, v124, v125
	v_cndmask_b32_e64 v127, 0, 1.0, vcc
	v_cmp_eq_u32_e32 vcc, v147, v138
	s_nop 1
	v_cndmask_b32_e64 v126, 0, 1.0, vcc
	v_pk_fma_f32 v[122:123], v[122:123], v[128:129], v[126:127] op_sel_hi:[0,1,1] neg_lo:[1,0,0] neg_hi:[1,0,0]
	v_cvt_pk_bf16_f32 v125, v122, v123
	ds_write_b64 v186, v[124:125]
	ds_read_b32 v122, v187 offset:72
	v_cmp_eq_u32_e32 vcc, v132, v139
	s_nop 1
	v_cndmask_b32_e64 v124, 0, 1.0, vcc
	v_cmp_eq_u32_e32 vcc, v133, v139
	s_nop 1
	v_cndmask_b32_e64 v125, 0, 1.0, vcc
	v_cmp_eq_u32_e32 vcc, v146, v139
	s_waitcnt lgkmcnt(0)
	v_pk_fma_f32 v[114:115], v[122:123], v[114:115], v[124:125] op_sel_hi:[0,1,1] neg_lo:[1,0,0] neg_hi:[1,0,0]
	v_cvt_pk_bf16_f32 v114, v114, v115
	v_cndmask_b32_e64 v125, 0, 1.0, vcc
	v_cmp_eq_u32_e32 vcc, v147, v139
	s_nop 1
	v_cndmask_b32_e64 v124, 0, 1.0, vcc
	v_pk_fma_f32 v[116:117], v[122:123], v[116:117], v[124:125] op_sel_hi:[0,1,1] neg_lo:[1,0,0] neg_hi:[1,0,0]
	v_cvt_pk_bf16_f32 v115, v116, v117
	ds_write_b64 v186, v[114:115] offset:544
	ds_read_b32 v114, v187 offset:80
	v_cmp_eq_u32_e32 vcc, v132, v140
	s_nop 1
	v_cndmask_b32_e64 v116, 0, 1.0, vcc
	v_cmp_eq_u32_e32 vcc, v133, v140
	s_nop 1
	v_cndmask_b32_e64 v117, 0, 1.0, vcc
	v_cmp_eq_u32_e32 vcc, v146, v140
	s_waitcnt lgkmcnt(0)
	v_pk_fma_f32 v[102:103], v[114:115], v[102:103], v[116:117] op_sel_hi:[0,1,1] neg_lo:[1,0,0] neg_hi:[1,0,0]
	v_cvt_pk_bf16_f32 v102, v102, v103
	v_cndmask_b32_e64 v117, 0, 1.0, vcc
	v_cmp_eq_u32_e32 vcc, v147, v140
	s_nop 1
	v_cndmask_b32_e64 v116, 0, 1.0, vcc
	v_pk_fma_f32 v[104:105], v[114:115], v[104:105], v[116:117] op_sel_hi:[0,1,1] neg_lo:[1,0,0] neg_hi:[1,0,0]
	v_cvt_pk_bf16_f32 v103, v104, v105
	ds_write_b64 v186, v[102:103] offset:1088
	ds_read_b32 v102, v187 offset:88
	v_cmp_eq_u32_e32 vcc, v132, v141
	s_nop 1
	v_cndmask_b32_e64 v104, 0, 1.0, vcc
	v_cmp_eq_u32_e32 vcc, v133, v141
	s_nop 1
	v_cndmask_b32_e64 v105, 0, 1.0, vcc
	v_cmp_eq_u32_e32 vcc, v146, v141
	s_waitcnt lgkmcnt(0)
	v_pk_fma_f32 v[90:91], v[102:103], v[90:91], v[104:105] op_sel_hi:[0,1,1] neg_lo:[1,0,0] neg_hi:[1,0,0]
	v_cvt_pk_bf16_f32 v90, v90, v91
	v_cndmask_b32_e64 v105, 0, 1.0, vcc
	v_cmp_eq_u32_e32 vcc, v147, v141
	s_nop 1
	v_cndmask_b32_e64 v104, 0, 1.0, vcc
	v_pk_fma_f32 v[92:93], v[102:103], v[92:93], v[104:105] op_sel_hi:[0,1,1] neg_lo:[1,0,0] neg_hi:[1,0,0]
	v_cvt_pk_bf16_f32 v91, v92, v93
	ds_write_b64 v186, v[90:91] offset:1632
	ds_read_b32 v90, v187 offset:96
	v_cmp_eq_u32_e32 vcc, v132, v142
	s_nop 1
	v_cndmask_b32_e64 v92, 0, 1.0, vcc
	v_cmp_eq_u32_e32 vcc, v133, v142
	s_nop 1
	v_cndmask_b32_e64 v93, 0, 1.0, vcc
	v_cmp_eq_u32_e32 vcc, v146, v142
	s_waitcnt lgkmcnt(0)
	v_pk_fma_f32 v[78:79], v[90:91], v[78:79], v[92:93] op_sel_hi:[0,1,1] neg_lo:[1,0,0] neg_hi:[1,0,0]
	v_cvt_pk_bf16_f32 v78, v78, v79
	v_cndmask_b32_e64 v93, 0, 1.0, vcc
	v_cmp_eq_u32_e32 vcc, v147, v142
	s_nop 1
	v_cndmask_b32_e64 v92, 0, 1.0, vcc
	v_pk_fma_f32 v[80:81], v[90:91], v[80:81], v[92:93] op_sel_hi:[0,1,1] neg_lo:[1,0,0] neg_hi:[1,0,0]
	v_cvt_pk_bf16_f32 v79, v80, v81
	ds_write_b64 v186, v[78:79] offset:2176
	ds_read_b32 v78, v187 offset:104
	v_cmp_eq_u32_e32 vcc, v132, v143
	s_nop 1
	v_cndmask_b32_e64 v80, 0, 1.0, vcc
	v_cmp_eq_u32_e32 vcc, v133, v143
	s_nop 1
	v_cndmask_b32_e64 v81, 0, 1.0, vcc
	v_cmp_eq_u32_e32 vcc, v146, v143
	s_waitcnt lgkmcnt(0)
	v_pk_fma_f32 v[74:75], v[78:79], v[74:75], v[80:81] op_sel_hi:[0,1,1] neg_lo:[1,0,0] neg_hi:[1,0,0]
	v_cvt_pk_bf16_f32 v74, v74, v75
	v_cndmask_b32_e64 v81, 0, 1.0, vcc
	v_cmp_eq_u32_e32 vcc, v147, v143
	s_nop 1
	v_cndmask_b32_e64 v80, 0, 1.0, vcc
	v_pk_fma_f32 v[76:77], v[78:79], v[76:77], v[80:81] op_sel_hi:[0,1,1] neg_lo:[1,0,0] neg_hi:[1,0,0]
	v_cvt_pk_bf16_f32 v75, v76, v77
	ds_write_b64 v186, v[74:75] offset:2720
	ds_read_b32 v74, v187 offset:112
	v_cmp_eq_u32_e32 vcc, v132, v144
	s_nop 1
	v_cndmask_b32_e64 v76, 0, 1.0, vcc
	v_cmp_eq_u32_e32 vcc, v133, v144
	s_nop 1
	v_cndmask_b32_e64 v77, 0, 1.0, vcc
	v_cmp_eq_u32_e32 vcc, v146, v144
	s_waitcnt lgkmcnt(0)
	v_pk_fma_f32 v[70:71], v[74:75], v[70:71], v[76:77] op_sel_hi:[0,1,1] neg_lo:[1,0,0] neg_hi:[1,0,0]
	v_cvt_pk_bf16_f32 v70, v70, v71
	v_cndmask_b32_e64 v77, 0, 1.0, vcc
	v_cmp_eq_u32_e32 vcc, v147, v144
	s_nop 1
	v_cndmask_b32_e64 v76, 0, 1.0, vcc
	v_pk_fma_f32 v[72:73], v[74:75], v[72:73], v[76:77] op_sel_hi:[0,1,1] neg_lo:[1,0,0] neg_hi:[1,0,0]
	v_cvt_pk_bf16_f32 v71, v72, v73
	ds_write_b64 v186, v[70:71] offset:3264
	ds_read_b32 v70, v187 offset:120
	v_cmp_eq_u32_e32 vcc, v132, v145
	s_nop 1
	v_cndmask_b32_e64 v72, 0, 1.0, vcc
	v_cmp_eq_u32_e32 vcc, v133, v145
	s_nop 1
	v_cndmask_b32_e64 v73, 0, 1.0, vcc
	v_cmp_eq_u32_e32 vcc, v146, v145
	s_waitcnt lgkmcnt(0)
	v_pk_fma_f32 v[66:67], v[70:71], v[66:67], v[72:73] op_sel_hi:[0,1,1] neg_lo:[1,0,0] neg_hi:[1,0,0]
	v_cvt_pk_bf16_f32 v66, v66, v67
	v_cndmask_b32_e64 v73, 0, 1.0, vcc
	v_cmp_eq_u32_e32 vcc, v147, v145
	s_nop 1
	v_cndmask_b32_e64 v72, 0, 1.0, vcc
	v_pk_fma_f32 v[68:69], v[70:71], v[68:69], v[72:73] op_sel_hi:[0,1,1] neg_lo:[1,0,0] neg_hi:[1,0,0]
	v_cvt_pk_bf16_f32 v67, v68, v69
	ds_write_b64 v186, v[66:67] offset:3808
	ds_read_b128 v[66:69], v1
	ds_read_b128 v[70:73], v1 offset:64
	ds_read_b128 v[74:77], v1 offset:128
	ds_read_b128 v[78:81], v1 offset:192
	v_lshl_add_u64 v[90:91], v[130:131], 0, s[0:1]
	v_add_co_u32_e32 v92, vcc, s7, v90
	s_nop 1
	v_addc_co_u32_e32 v93, vcc, 0, v91, vcc
	global_load_dwordx4 v[146:149], v[90:91], off nt
	global_load_dwordx4 v[142:145], v[92:93], off nt
	v_add_co_u32_e32 v92, vcc, s36, v90
	s_nop 1
	v_addc_co_u32_e32 v93, vcc, 0, v91, vcc
	v_add_co_u32_e32 v102, vcc, s37, v90
	s_nop 1
	v_addc_co_u32_e32 v103, vcc, 0, v91, vcc
	global_load_dwordx4 v[138:141], v[92:93], off nt
	global_load_dwordx4 v[130:133], v[102:103], off nt
	v_add_co_u32_e32 v92, vcc, s38, v90
	s_nop 1
	v_addc_co_u32_e32 v93, vcc, 0, v91, vcc
	v_add_co_u32_e32 v102, vcc, s39, v90
	s_nop 1
	v_addc_co_u32_e32 v103, vcc, 0, v91, vcc
	global_load_dwordx4 v[126:129], v[92:93], off nt
	global_load_dwordx4 v[122:125], v[102:103], off nt
	v_add_co_u32_e32 v92, vcc, s41, v90
	s_nop 1
	v_addc_co_u32_e32 v93, vcc, 0, v91, vcc
	v_add_co_u32_e32 v90, vcc, s42, v90
	s_nop 1
	v_addc_co_u32_e32 v91, vcc, 0, v91, vcc
	global_load_dwordx4 v[114:117], v[92:93], off nt
	global_load_dwordx4 v[102:105], v[90:91], off nt
	s_waitcnt vmcnt(15)
	s_waitcnt vmcnt(14)
	s_waitcnt vmcnt(13)
	s_waitcnt vmcnt(12)
	s_waitcnt vmcnt(11)
	s_waitcnt vmcnt(10)
	s_waitcnt vmcnt(9)
	s_waitcnt vmcnt(8)
	ds_read_b32 v90, v187 offset:128
	v_add_u32_e32 v190, 1, v189
	v_cmp_eq_u32_e32 vcc, v189, v194
	v_add_u32_e32 v192, 3, v189
	v_add_u32_e32 v193, 2, v189
	v_cndmask_b32_e64 v92, 0, 1.0, vcc
	v_cmp_eq_u32_e32 vcc, v190, v194
	s_nop 1
	v_cndmask_b32_e64 v93, 0, 1.0, vcc
	v_cmp_eq_u32_e32 vcc, v192, v194
	s_waitcnt lgkmcnt(0)
	v_pk_fma_f32 v[92:93], v[90:91], v[134:135], v[92:93] op_sel_hi:[0,1,1] neg_lo:[1,0,0] neg_hi:[1,0,0]
	v_cvt_pk_bf16_f32 v92, v92, v93
	v_cndmask_b32_e64 v135, 0, 1.0, vcc
	v_cmp_eq_u32_e32 vcc, v193, v194
	s_nop 1
	v_cndmask_b32_e64 v134, 0, 1.0, vcc
	v_pk_fma_f32 v[90:91], v[90:91], v[136:137], v[134:135] op_sel_hi:[0,1,1] neg_lo:[1,0,0] neg_hi:[1,0,0]
	v_cvt_pk_bf16_f32 v93, v90, v91
	ds_write_b64 v186, v[92:93]
	ds_read_b32 v90, v187 offset:136
	v_cmp_eq_u32_e32 vcc, v189, v195
	s_nop 1
	v_cndmask_b32_e64 v92, 0, 1.0, vcc
	v_cmp_eq_u32_e32 vcc, v190, v195
	s_nop 1
	v_cndmask_b32_e64 v93, 0, 1.0, vcc
	v_cmp_eq_u32_e32 vcc, v192, v195
	s_waitcnt lgkmcnt(0)
	v_pk_fma_f32 v[92:93], v[90:91], v[118:119], v[92:93] op_sel_hi:[0,1,1] neg_lo:[1,0,0] neg_hi:[1,0,0]
	v_cvt_pk_bf16_f32 v92, v92, v93
	v_cndmask_b32_e64 v119, 0, 1.0, vcc
	v_cmp_eq_u32_e32 vcc, v193, v195
	s_nop 1
	v_cndmask_b32_e64 v118, 0, 1.0, vcc
	v_pk_fma_f32 v[90:91], v[90:91], v[120:121], v[118:119] op_sel_hi:[0,1,1] neg_lo:[1,0,0] neg_hi:[1,0,0]
	v_cvt_pk_bf16_f32 v93, v90, v91
	ds_write_b64 v186, v[92:93] offset:544
	ds_read_b32 v90, v187 offset:144
	v_cmp_eq_u32_e32 vcc, v189, v196
	s_nop 1
	v_cndmask_b32_e64 v92, 0, 1.0, vcc
	v_cmp_eq_u32_e32 vcc, v190, v196
	s_nop 1
	v_cndmask_b32_e64 v93, 0, 1.0, vcc
	v_cmp_eq_u32_e32 vcc, v192, v196
	s_waitcnt lgkmcnt(0)
	v_pk_fma_f32 v[92:93], v[90:91], v[110:111], v[92:93] op_sel_hi:[0,1,1] neg_lo:[1,0,0] neg_hi:[1,0,0]
	v_cvt_pk_bf16_f32 v92, v92, v93
	v_cndmask_b32_e64 v111, 0, 1.0, vcc
	v_cmp_eq_u32_e32 vcc, v193, v196
	s_nop 1
	v_cndmask_b32_e64 v110, 0, 1.0, vcc
	v_pk_fma_f32 v[90:91], v[90:91], v[112:113], v[110:111] op_sel_hi:[0,1,1] neg_lo:[1,0,0] neg_hi:[1,0,0]
	v_cvt_pk_bf16_f32 v93, v90, v91
	ds_write_b64 v186, v[92:93] offset:1088
	ds_read_b32 v90, v187 offset:152
	v_cmp_eq_u32_e32 vcc, v189, v197
	s_nop 1
	v_cndmask_b32_e64 v92, 0, 1.0, vcc
	v_cmp_eq_u32_e32 vcc, v190, v197
	s_nop 1
	v_cndmask_b32_e64 v93, 0, 1.0, vcc
	v_cmp_eq_u32_e32 vcc, v192, v197
	s_waitcnt lgkmcnt(0)
	v_pk_fma_f32 v[92:93], v[90:91], v[106:107], v[92:93] op_sel_hi:[0,1,1] neg_lo:[1,0,0] neg_hi:[1,0,0]
	v_cvt_pk_bf16_f32 v92, v92, v93
	v_cndmask_b32_e64 v107, 0, 1.0, vcc
	v_cmp_eq_u32_e32 vcc, v193, v197
	s_nop 1
	v_cndmask_b32_e64 v106, 0, 1.0, vcc
	v_pk_fma_f32 v[90:91], v[90:91], v[108:109], v[106:107] op_sel_hi:[0,1,1] neg_lo:[1,0,0] neg_hi:[1,0,0]
	v_cvt_pk_bf16_f32 v93, v90, v91
	ds_write_b64 v186, v[92:93] offset:1632
	ds_read_b32 v90, v187 offset:160
	v_cmp_eq_u32_e32 vcc, v189, v198
	s_nop 1
	v_cndmask_b32_e64 v92, 0, 1.0, vcc
	v_cmp_eq_u32_e32 vcc, v190, v198
	s_nop 1
	v_cndmask_b32_e64 v93, 0, 1.0, vcc
	v_cmp_eq_u32_e32 vcc, v192, v198
	s_waitcnt lgkmcnt(0)
	v_pk_fma_f32 v[92:93], v[90:91], v[98:99], v[92:93] op_sel_hi:[0,1,1] neg_lo:[1,0,0] neg_hi:[1,0,0]
	v_cvt_pk_bf16_f32 v92, v92, v93
	v_cndmask_b32_e64 v99, 0, 1.0, vcc
	v_cmp_eq_u32_e32 vcc, v193, v198
	s_nop 1
	v_cndmask_b32_e64 v98, 0, 1.0, vcc
	v_pk_fma_f32 v[90:91], v[90:91], v[100:101], v[98:99] op_sel_hi:[0,1,1] neg_lo:[1,0,0] neg_hi:[1,0,0]
	v_cvt_pk_bf16_f32 v93, v90, v91
	ds_write_b64 v186, v[92:93] offset:2176
	ds_read_b32 v90, v187 offset:168
	v_cmp_eq_u32_e32 vcc, v189, v199
	s_nop 1
	v_cndmask_b32_e64 v92, 0, 1.0, vcc
	v_cmp_eq_u32_e32 vcc, v190, v199
	s_nop 1
	v_cndmask_b32_e64 v93, 0, 1.0, vcc
	v_cmp_eq_u32_e32 vcc, v192, v199
	s_waitcnt lgkmcnt(0)
	v_pk_fma_f32 v[92:93], v[90:91], v[94:95], v[92:93] op_sel_hi:[0,1,1] neg_lo:[1,0,0] neg_hi:[1,0,0]
	v_cvt_pk_bf16_f32 v92, v92, v93
	v_cndmask_b32_e64 v95, 0, 1.0, vcc
	v_cmp_eq_u32_e32 vcc, v193, v199
	s_nop 1
	v_cndmask_b32_e64 v94, 0, 1.0, vcc
	v_pk_fma_f32 v[90:91], v[90:91], v[96:97], v[94:95] op_sel_hi:[0,1,1] neg_lo:[1,0,0] neg_hi:[1,0,0]
	v_cvt_pk_bf16_f32 v93, v90, v91
	ds_write_b64 v186, v[92:93] offset:2720
	ds_read_b32 v90, v187 offset:176
	v_cmp_eq_u32_e32 vcc, v189, v200
	s_nop 1
	v_cndmask_b32_e64 v92, 0, 1.0, vcc
	v_cmp_eq_u32_e32 vcc, v190, v200
	s_nop 1
	v_cndmask_b32_e64 v93, 0, 1.0, vcc
	v_cmp_eq_u32_e32 vcc, v192, v200
	s_waitcnt lgkmcnt(0)
	v_pk_fma_f32 v[86:87], v[90:91], v[86:87], v[92:93] op_sel_hi:[0,1,1] neg_lo:[1,0,0] neg_hi:[1,0,0]
	v_cvt_pk_bf16_f32 v86, v86, v87
	v_cndmask_b32_e64 v93, 0, 1.0, vcc
	v_cmp_eq_u32_e32 vcc, v193, v200
	s_nop 1
	v_cndmask_b32_e64 v92, 0, 1.0, vcc
	v_pk_fma_f32 v[88:89], v[90:91], v[88:89], v[92:93] op_sel_hi:[0,1,1] neg_lo:[1,0,0] neg_hi:[1,0,0]
	v_cvt_pk_bf16_f32 v87, v88, v89
	ds_write_b64 v186, v[86:87] offset:3264
	ds_read_b32 v86, v187 offset:184
	v_cmp_eq_u32_e32 vcc, v189, v201
	s_nop 1
	v_cndmask_b32_e64 v88, 0, 1.0, vcc
	v_cmp_eq_u32_e32 vcc, v190, v201
	s_nop 1
	v_cndmask_b32_e64 v89, 0, 1.0, vcc
	v_cmp_eq_u32_e32 vcc, v192, v201
	s_waitcnt lgkmcnt(0)
	v_pk_fma_f32 v[82:83], v[86:87], v[82:83], v[88:89] op_sel_hi:[0,1,1] neg_lo:[1,0,0] neg_hi:[1,0,0]
	v_cvt_pk_bf16_f32 v82, v82, v83
	v_cndmask_b32_e64 v89, 0, 1.0, vcc
	v_cmp_eq_u32_e32 vcc, v193, v201
	s_nop 1
	v_cndmask_b32_e64 v88, 0, 1.0, vcc
	v_pk_fma_f32 v[84:85], v[86:87], v[84:85], v[88:89] op_sel_hi:[0,1,1] neg_lo:[1,0,0] neg_hi:[1,0,0]
	v_cvt_pk_bf16_f32 v83, v84, v85
	ds_write_b64 v186, v[82:83] offset:3808
	ds_read_b128 v[82:85], v1
	ds_read_b128 v[86:89], v1 offset:64
	ds_read_b128 v[90:93], v1 offset:128
	ds_read_b128 v[94:97], v1 offset:192
	v_lshl_add_u64 v[98:99], v[150:151], 0, s[0:1]
	v_lshl_add_u64 v[192:193], v[164:165], 0, s[0:1]
	v_lshl_add_u64 v[196:197], v[166:167], 0, s[0:1]
	v_lshl_add_u64 v[100:101], v[152:153], 0, s[0:1]
	v_lshl_add_u64 v[106:107], v[156:157], 0, s[0:1]
	v_lshl_add_u64 v[108:109], v[158:159], 0, s[0:1]
	v_lshl_add_u64 v[110:111], v[160:161], 0, s[0:1]
	v_lshl_add_u64 v[112:113], v[162:163], 0, s[0:1]
	global_load_dwordx4 v[118:121], v[98:99], off nt
	global_load_dwordx4 v[134:137], v[100:101], off nt
	global_load_dwordx4 v[150:153], v[106:107], off nt
	global_load_dwordx4 v[156:159], v[108:109], off nt
	global_load_dwordx4 v[160:163], v[110:111], off nt
	global_load_dwordx4 v[164:167], v[112:113], off nt
	s_nop 0
	global_load_dwordx4 v[192:195], v[192:193], off nt
	s_nop 0
	global_load_dwordx4 v[196:199], v[196:197], off nt
	v_mov_b32_e32 v98, v188
	s_waitcnt vmcnt(15)
	s_waitcnt vmcnt(14)
	s_waitcnt vmcnt(13)
	s_waitcnt vmcnt(12)
	s_waitcnt vmcnt(11)
	s_waitcnt vmcnt(10)
	s_waitcnt vmcnt(9)
	s_waitcnt vmcnt(8)
	ds_read_b32 v98, v187
	s_waitcnt lgkmcnt(0)
	v_pk_fma_f32 v[100:101], v[98:99], v[146:147], 0 op_sel_hi:[0,1,0] neg_lo:[1,0,0] neg_hi:[1,0,0]
	v_pk_fma_f32 v[98:99], v[98:99], v[148:149], 0 op_sel_hi:[0,1,0] neg_lo:[1,0,0] neg_hi:[1,0,0]
	v_cvt_pk_bf16_f32 v100, v100, v101
	v_cvt_pk_bf16_f32 v101, v98, v99
	ds_write_b64 v186, v[100:101]
	ds_read_b32 v98, v187 offset:8
	s_waitcnt lgkmcnt(0)
	v_pk_fma_f32 v[100:101], v[98:99], v[142:143], 0 op_sel_hi:[0,1,0] neg_lo:[1,0,0] neg_hi:[1,0,0]
	v_pk_fma_f32 v[98:99], v[98:99], v[144:145], 0 op_sel_hi:[0,1,0] neg_lo:[1,0,0] neg_hi:[1,0,0]
	v_cvt_pk_bf16_f32 v100, v100, v101
	v_cvt_pk_bf16_f32 v101, v98, v99
	ds_write_b64 v186, v[100:101] offset:544
	ds_read_b32 v98, v187 offset:16
	s_waitcnt lgkmcnt(0)
	v_pk_fma_f32 v[100:101], v[98:99], v[138:139], 0 op_sel_hi:[0,1,0] neg_lo:[1,0,0] neg_hi:[1,0,0]
	v_pk_fma_f32 v[98:99], v[98:99], v[140:141], 0 op_sel_hi:[0,1,0] neg_lo:[1,0,0] neg_hi:[1,0,0]
	v_cvt_pk_bf16_f32 v100, v100, v101
	v_cvt_pk_bf16_f32 v101, v98, v99
	ds_write_b64 v186, v[100:101] offset:1088
	ds_read_b32 v98, v187 offset:24
	s_waitcnt lgkmcnt(0)
	v_pk_fma_f32 v[100:101], v[98:99], v[130:131], 0 op_sel_hi:[0,1,0] neg_lo:[1,0,0] neg_hi:[1,0,0]
	v_pk_fma_f32 v[98:99], v[98:99], v[132:133], 0 op_sel_hi:[0,1,0] neg_lo:[1,0,0] neg_hi:[1,0,0]
	v_cvt_pk_bf16_f32 v100, v100, v101
	v_cvt_pk_bf16_f32 v101, v98, v99
	ds_write_b64 v186, v[100:101] offset:1632
	ds_read_b32 v98, v187 offset:32
	s_waitcnt lgkmcnt(0)
	v_pk_fma_f32 v[100:101], v[98:99], v[126:127], 0 op_sel_hi:[0,1,0] neg_lo:[1,0,0] neg_hi:[1,0,0]
	v_pk_fma_f32 v[98:99], v[98:99], v[128:129], 0 op_sel_hi:[0,1,0] neg_lo:[1,0,0] neg_hi:[1,0,0]
	v_cvt_pk_bf16_f32 v100, v100, v101
	v_cvt_pk_bf16_f32 v101, v98, v99
	ds_write_b64 v186, v[100:101] offset:2176
	ds_read_b32 v98, v187 offset:40
	s_waitcnt lgkmcnt(0)
	v_pk_fma_f32 v[100:101], v[98:99], v[122:123], 0 op_sel_hi:[0,1,0] neg_lo:[1,0,0] neg_hi:[1,0,0]
	v_pk_fma_f32 v[98:99], v[98:99], v[124:125], 0 op_sel_hi:[0,1,0] neg_lo:[1,0,0] neg_hi:[1,0,0]
	v_cvt_pk_bf16_f32 v100, v100, v101
	v_cvt_pk_bf16_f32 v101, v98, v99
	ds_write_b64 v186, v[100:101] offset:2720
	ds_read_b32 v98, v187 offset:48
	s_waitcnt lgkmcnt(0)
	v_pk_fma_f32 v[100:101], v[98:99], v[114:115], 0 op_sel_hi:[0,1,0] neg_lo:[1,0,0] neg_hi:[1,0,0]
	v_pk_fma_f32 v[98:99], v[98:99], v[116:117], 0 op_sel_hi:[0,1,0] neg_lo:[1,0,0] neg_hi:[1,0,0]
	v_cvt_pk_bf16_f32 v100, v100, v101
	v_cvt_pk_bf16_f32 v101, v98, v99
	ds_write_b64 v186, v[100:101] offset:3264
	ds_read_b32 v98, v187 offset:56
	s_waitcnt lgkmcnt(0)
	v_pk_fma_f32 v[100:101], v[98:99], v[102:103], 0 op_sel_hi:[0,1,0] neg_lo:[1,0,0] neg_hi:[1,0,0]
	v_pk_fma_f32 v[98:99], v[98:99], v[104:105], 0 op_sel_hi:[0,1,0] neg_lo:[1,0,0] neg_hi:[1,0,0]
	v_cvt_pk_bf16_f32 v100, v100, v101
	v_cvt_pk_bf16_f32 v101, v98, v99
	ds_write_b64 v186, v[100:101] offset:3808
	ds_read_b128 v[98:101], v1
	ds_read_b128 v[102:105], v1 offset:64
	ds_read_b128 v[106:109], v1 offset:128
	ds_read_b128 v[110:113], v1 offset:192
	v_lshl_add_u64 v[114:115], v[168:169], 0, s[0:1]
	v_lshl_add_u64 v[126:127], v[176:177], 0, s[0:1]
	v_lshl_add_u64 v[176:177], v[180:181], 0, s[0:1]
	v_lshl_add_u64 v[180:181], v[182:183], 0, s[0:1]
	v_lshl_add_u64 v[116:117], v[170:171], 0, s[0:1]
	v_lshl_add_u64 v[122:123], v[172:173], 0, s[0:1]
	v_lshl_add_u64 v[124:125], v[174:175], 0, s[0:1]
	v_lshl_add_u64 v[128:129], v[178:179], 0, s[0:1]
	global_load_dwordx4 v[130:133], v[114:115], off nt
	global_load_dwordx4 v[138:141], v[116:117], off nt
	global_load_dwordx4 v[142:145], v[122:123], off nt
	global_load_dwordx4 v[146:149], v[124:125], off nt
	global_load_dwordx4 v[168:171], v[126:127], off nt
	global_load_dwordx4 v[172:175], v[128:129], off nt
	s_nop 0
	global_load_dwordx4 v[176:179], v[176:177], off nt
	s_nop 0
	global_load_dwordx4 v[180:183], v[180:181], off nt
	v_mov_b32_e32 v114, v188
	s_waitcnt vmcnt(15)
	s_waitcnt vmcnt(14)
	s_waitcnt vmcnt(13)
	s_waitcnt vmcnt(12)
	s_waitcnt vmcnt(11)
	s_waitcnt vmcnt(10)
	s_waitcnt vmcnt(9)
	s_waitcnt vmcnt(8)
	ds_read_b32 v114, v187 offset:64
	s_waitcnt lgkmcnt(0)
	v_pk_fma_f32 v[116:117], v[114:115], v[118:119], 0 op_sel_hi:[0,1,0] neg_lo:[1,0,0] neg_hi:[1,0,0]
	v_pk_fma_f32 v[114:115], v[114:115], v[120:121], 0 op_sel_hi:[0,1,0] neg_lo:[1,0,0] neg_hi:[1,0,0]
	v_cvt_pk_bf16_f32 v116, v116, v117
	v_cvt_pk_bf16_f32 v117, v114, v115
	ds_write_b64 v186, v[116:117]
	ds_read_b32 v114, v187 offset:72
	s_waitcnt lgkmcnt(0)
	v_pk_fma_f32 v[116:117], v[114:115], v[134:135], 0 op_sel_hi:[0,1,0] neg_lo:[1,0,0] neg_hi:[1,0,0]
	v_pk_fma_f32 v[114:115], v[114:115], v[136:137], 0 op_sel_hi:[0,1,0] neg_lo:[1,0,0] neg_hi:[1,0,0]
	v_cvt_pk_bf16_f32 v116, v116, v117
	v_cvt_pk_bf16_f32 v117, v114, v115
	ds_write_b64 v186, v[116:117] offset:544
	ds_read_b32 v114, v187 offset:80
	s_waitcnt lgkmcnt(0)
	v_pk_fma_f32 v[116:117], v[114:115], v[150:151], 0 op_sel_hi:[0,1,0] neg_lo:[1,0,0] neg_hi:[1,0,0]
	v_pk_fma_f32 v[114:115], v[114:115], v[152:153], 0 op_sel_hi:[0,1,0] neg_lo:[1,0,0] neg_hi:[1,0,0]
	v_cvt_pk_bf16_f32 v116, v116, v117
	v_cvt_pk_bf16_f32 v117, v114, v115
	ds_write_b64 v186, v[116:117] offset:1088
	ds_read_b32 v114, v187 offset:88
	s_waitcnt lgkmcnt(0)
	v_pk_fma_f32 v[116:117], v[114:115], v[156:157], 0 op_sel_hi:[0,1,0] neg_lo:[1,0,0] neg_hi:[1,0,0]
	v_pk_fma_f32 v[114:115], v[114:115], v[158:159], 0 op_sel_hi:[0,1,0] neg_lo:[1,0,0] neg_hi:[1,0,0]
	v_cvt_pk_bf16_f32 v116, v116, v117
	v_cvt_pk_bf16_f32 v117, v114, v115
	ds_write_b64 v186, v[116:117] offset:1632
	ds_read_b32 v114, v187 offset:96
	s_waitcnt lgkmcnt(0)
	v_pk_fma_f32 v[116:117], v[114:115], v[160:161], 0 op_sel_hi:[0,1,0] neg_lo:[1,0,0] neg_hi:[1,0,0]
	v_pk_fma_f32 v[114:115], v[114:115], v[162:163], 0 op_sel_hi:[0,1,0] neg_lo:[1,0,0] neg_hi:[1,0,0]
	v_cvt_pk_bf16_f32 v116, v116, v117
	v_cvt_pk_bf16_f32 v117, v114, v115
	ds_write_b64 v186, v[116:117] offset:2176
	ds_read_b32 v114, v187 offset:104
	s_waitcnt lgkmcnt(0)
	v_pk_fma_f32 v[116:117], v[114:115], v[164:165], 0 op_sel_hi:[0,1,0] neg_lo:[1,0,0] neg_hi:[1,0,0]
	v_pk_fma_f32 v[114:115], v[114:115], v[166:167], 0 op_sel_hi:[0,1,0] neg_lo:[1,0,0] neg_hi:[1,0,0]
	v_cvt_pk_bf16_f32 v116, v116, v117
	v_cvt_pk_bf16_f32 v117, v114, v115
	ds_write_b64 v186, v[116:117] offset:2720
	ds_read_b32 v114, v187 offset:112
	s_waitcnt lgkmcnt(0)
	v_pk_fma_f32 v[116:117], v[114:115], v[192:193], 0 op_sel_hi:[0,1,0] neg_lo:[1,0,0] neg_hi:[1,0,0]
	v_pk_fma_f32 v[114:115], v[114:115], v[194:195], 0 op_sel_hi:[0,1,0] neg_lo:[1,0,0] neg_hi:[1,0,0]
	v_cvt_pk_bf16_f32 v116, v116, v117
	v_cvt_pk_bf16_f32 v117, v114, v115
	ds_write_b64 v186, v[116:117] offset:3264
	ds_read_b32 v114, v187 offset:120
	s_waitcnt lgkmcnt(0)
	v_pk_fma_f32 v[116:117], v[114:115], v[196:197], 0 op_sel_hi:[0,1,0] neg_lo:[1,0,0] neg_hi:[1,0,0]
	v_pk_fma_f32 v[114:115], v[114:115], v[198:199], 0 op_sel_hi:[0,1,0] neg_lo:[1,0,0] neg_hi:[1,0,0]
	v_cvt_pk_bf16_f32 v116, v116, v117
	v_cvt_pk_bf16_f32 v117, v114, v115
	ds_write_b64 v186, v[116:117] offset:3808
	ds_read_b128 v[114:117], v1
	ds_read_b128 v[118:121], v1 offset:64
	ds_read_b128 v[122:125], v1 offset:128
	ds_read_b128 v[126:129], v1 offset:192
	s_waitcnt vmcnt(7)
	s_waitcnt vmcnt(6)
	s_waitcnt vmcnt(5)
	s_waitcnt vmcnt(4)
	s_waitcnt vmcnt(3)
	s_waitcnt vmcnt(2)
	s_waitcnt vmcnt(1)
	s_waitcnt vmcnt(0)
	ds_read_b32 v134, v187 offset:128
	s_waitcnt lgkmcnt(0)
	v_pk_fma_f32 v[130:131], v[134:135], v[130:131], 0 op_sel_hi:[0,1,0] neg_lo:[1,0,0] neg_hi:[1,0,0]
	v_pk_fma_f32 v[132:133], v[134:135], v[132:133], 0 op_sel_hi:[0,1,0] neg_lo:[1,0,0] neg_hi:[1,0,0]
	v_cvt_pk_bf16_f32 v130, v130, v131
	v_cvt_pk_bf16_f32 v131, v132, v133
	ds_write_b64 v186, v[130:131]
	ds_read_b32 v130, v187 offset:136
	s_waitcnt lgkmcnt(0)
	v_pk_fma_f32 v[132:133], v[130:131], v[138:139], 0 op_sel_hi:[0,1,0] neg_lo:[1,0,0] neg_hi:[1,0,0]
	v_pk_fma_f32 v[130:131], v[130:131], v[140:141], 0 op_sel_hi:[0,1,0] neg_lo:[1,0,0] neg_hi:[1,0,0]
	v_cvt_pk_bf16_f32 v132, v132, v133
	v_cvt_pk_bf16_f32 v133, v130, v131
	ds_write_b64 v186, v[132:133] offset:544
	ds_read_b32 v130, v187 offset:144
	s_waitcnt lgkmcnt(0)
	v_pk_fma_f32 v[132:133], v[130:131], v[142:143], 0 op_sel_hi:[0,1,0] neg_lo:[1,0,0] neg_hi:[1,0,0]
	v_pk_fma_f32 v[130:131], v[130:131], v[144:145], 0 op_sel_hi:[0,1,0] neg_lo:[1,0,0] neg_hi:[1,0,0]
	v_cvt_pk_bf16_f32 v132, v132, v133
	v_cvt_pk_bf16_f32 v133, v130, v131
	ds_write_b64 v186, v[132:133] offset:1088
	ds_read_b32 v130, v187 offset:152
	s_waitcnt lgkmcnt(0)
	v_pk_fma_f32 v[132:133], v[130:131], v[146:147], 0 op_sel_hi:[0,1,0] neg_lo:[1,0,0] neg_hi:[1,0,0]
	v_pk_fma_f32 v[130:131], v[130:131], v[148:149], 0 op_sel_hi:[0,1,0] neg_lo:[1,0,0] neg_hi:[1,0,0]
	v_cvt_pk_bf16_f32 v132, v132, v133
	v_cvt_pk_bf16_f32 v133, v130, v131
	ds_write_b64 v186, v[132:133] offset:1632
	ds_read_b32 v130, v187 offset:160
	s_waitcnt lgkmcnt(0)
	v_pk_fma_f32 v[132:133], v[130:131], v[168:169], 0 op_sel_hi:[0,1,0] neg_lo:[1,0,0] neg_hi:[1,0,0]
	v_pk_fma_f32 v[130:131], v[130:131], v[170:171], 0 op_sel_hi:[0,1,0] neg_lo:[1,0,0] neg_hi:[1,0,0]
	v_cvt_pk_bf16_f32 v132, v132, v133
	v_cvt_pk_bf16_f32 v133, v130, v131
	ds_write_b64 v186, v[132:133] offset:2176
	ds_read_b32 v130, v187 offset:168
	s_waitcnt lgkmcnt(0)
	v_pk_fma_f32 v[132:133], v[130:131], v[172:173], 0 op_sel_hi:[0,1,0] neg_lo:[1,0,0] neg_hi:[1,0,0]
	v_pk_fma_f32 v[130:131], v[130:131], v[174:175], 0 op_sel_hi:[0,1,0] neg_lo:[1,0,0] neg_hi:[1,0,0]
	v_cvt_pk_bf16_f32 v132, v132, v133
	v_cvt_pk_bf16_f32 v133, v130, v131
	ds_write_b64 v186, v[132:133] offset:2720
	ds_read_b32 v130, v187 offset:176
	s_waitcnt lgkmcnt(0)
	v_pk_fma_f32 v[132:133], v[130:131], v[176:177], 0 op_sel_hi:[0,1,0] neg_lo:[1,0,0] neg_hi:[1,0,0]
	v_pk_fma_f32 v[130:131], v[130:131], v[178:179], 0 op_sel_hi:[0,1,0] neg_lo:[1,0,0] neg_hi:[1,0,0]
	v_cvt_pk_bf16_f32 v132, v132, v133
	v_cvt_pk_bf16_f32 v133, v130, v131
	ds_write_b64 v186, v[132:133] offset:3264
	ds_read_b32 v130, v187 offset:184
	s_waitcnt lgkmcnt(0)
	v_pk_fma_f32 v[132:133], v[130:131], v[180:181], 0 op_sel_hi:[0,1,0] neg_lo:[1,0,0] neg_hi:[1,0,0]
	v_pk_fma_f32 v[130:131], v[130:131], v[182:183], 0 op_sel_hi:[0,1,0] neg_lo:[1,0,0] neg_hi:[1,0,0]
	v_cvt_pk_bf16_f32 v132, v132, v133
	v_cvt_pk_bf16_f32 v133, v130, v131
	ds_write_b64 v186, v[132:133] offset:3808
	ds_read_b128 v[130:133], v1
	ds_read_b128 v[134:137], v1 offset:64
	ds_read_b128 v[138:141], v1 offset:128
	ds_read_b128 v[142:145], v1 offset:192
	s_ashr_i32 s7, s6, 31
	s_lshl_b64 s[0:1], s[6:7], 2
	s_add_u32 s0, s4, s0
	s_addc_u32 s1, s5, s1
	v_lshlrev_b32_e32 v1, 4, v0
	v_mov_b32_e32 v146, v224
	v_mov_b32_e32 v147, v225
	v_mov_b32_e32 v148, v226
	v_mov_b32_e32 v149, v227
	s_add_i32 s20, s34, 1
	s_add_i32 s34, s34, -1
	v_or_b32_e32 v153, s10, v206
	s_xor_b32 s26, s3, 2
	s_lshl_b64 s[10:11], s[10:11], 3
	s_and_b32 s20, s20, 3
	s_and_b32 s27, s34, 3
	s_add_u32 s10, s14, s10
	s_addc_u32 s11, s15, s11
	s_lshl_b32 s42, s35, 2
	s_add_i32 s41, s42, 0x26a20
	s_add_i32 s42, s42, 0x26a00
	v_lshlrev_b32_e32 v190, 3, v206
	s_cmp_eq_u32 s35, 3
	v_lshlrev_b32_e32 v150, 3, v0
	v_and_b32_e32 v151, 1, v0
	v_lshl_add_u64 v[0:1], v[154:155], 3, s[14:15]
	v_lshl_add_u64 v[192:193], s[10:11], 0, v[190:191]
	s_cselect_b64 s[10:11], -1, 0
	s_lshl_b32 s14, s3, 2
	s_add_u32 s24, s16, s14
	v_or_b32_e32 v155, 0x20000, v150
	v_add_u32_e32 v156, 0x20880, v150
	v_lshlrev_b32_e32 v150, 1, v153
	s_addc_u32 s25, s17, 0
	s_lshl_b32 s43, s3, 9
	v_lshl_add_u32 v212, s26, 9, v150
	s_lshl_b32 s15, s26, 8
	s_add_i32 s26, s43, 0x200
	v_mov_b32_e32 v152, 0x880
	v_cmp_lt_u32_e64 s[0:1], 15, v206
	v_cmp_eq_u32_e32 vcc, 1, v151
	s_and_b32 s45, s26, 0x600
	s_add_i32 s26, s43, 0x500
	v_cndmask_b32_e32 v211, 0, v152, vcc
	s_and_b32 s56, s26, 0x700
	s_add_i32 s26, s43, 0x540
	v_lshl_add_u32 v213, s20, 9, v150
	v_lshl_add_u32 v214, s27, 9, v150
	s_and_b32 s57, s26, 0x740
	s_add_i32 s26, s43, 0x580
	s_and_b32 s58, s26, 0x780
	s_add_i32 s26, s43, 0x5c0
	s_and_b32 s59, s26, 0x7c0
	s_add_i32 s26, s43, 0x600
	s_and_b32 s60, s26, 0x600
	s_add_i32 s26, s43, 0x640
	s_and_b32 s61, s26, 0x640
	s_add_i32 s26, s43, 0x680
	s_and_b32 s62, s26, 0x680
	s_add_i32 s26, s43, 0x6c0
	s_and_b32 s63, s26, 0x6c0
	s_add_i32 s26, s43, 0x700
	s_and_b32 s64, s26, 0x700
	s_add_i32 s26, s43, 0x740
	s_and_b32 s65, s26, 0x740
	s_add_i32 s26, s43, 0x780
	s_lshl_b32 s14, s27, 8
	s_lshl_b32 s20, s20, 8
	s_add_i32 s27, s43, 0x240
	s_add_i32 s28, s43, 0x280
	s_add_i32 s29, s43, 0x2c0
	s_add_i32 s30, s43, 0x300
	s_add_i32 s31, s43, 0x340
	s_add_i32 s34, s43, 0x380
	s_add_i32 s35, s43, 0x3c0
	s_add_i32 s36, s43, 0x440
	s_add_i32 s37, s43, 0x480
	s_add_i32 s38, s43, 0x4c0
	s_and_b32 s66, s26, 0x780
	s_add_i32 s26, s43, 0x7c0
	s_mul_hi_i32 s23, s18, 0x65
	s_mul_i32 s22, s18, 0x65
	v_cmp_eq_u32_e64 s[4:5], 1, v185
	v_cmp_eq_u32_e64 s[6:7], 2, v185
	v_cmp_eq_u32_e64 s[8:9], 63, v206
	s_xor_b32 s44, s43, 0x400
	s_and_b32 s46, s27, 0x640
	s_and_b32 s47, s28, 0x680
	v_and_b32_e32 v248, 2, v206
	v_cmp_ne_u32_e32 vcc, 0, v248
	v_mov_b32_e32 v249, 0x44444444
	v_mov_b32_e32 v250, 0xeeeeeeee
	s_nop 1
	v_cndmask_b32_e32 v223, v249, v250, vcc
	v_lshrrev_b32_e32 v248, 4, v206
	v_lshl_add_u32 v248, v248, 4, 1
	v_add_u32_e32 v249, 0, v248
	v_cvt_f32_u32_e32 v249, v249
	v_add_u32_e32 v250, 1, v248
	v_cvt_f32_u32_e32 v250, v250
	v_cvt_pk_bf16_f32 v232, v249, v250
	v_add_u32_e32 v249, 2, v248
	v_cvt_f32_u32_e32 v249, v249
	v_add_u32_e32 v250, 3, v248
	v_cvt_f32_u32_e32 v250, v250
	v_cvt_pk_bf16_f32 v233, v249, v250
	v_add_u32_e32 v249, 4, v248
	v_cvt_f32_u32_e32 v249, v249
	v_add_u32_e32 v250, 5, v248
	v_cvt_f32_u32_e32 v250, v250
	v_cvt_pk_bf16_f32 v234, v249, v250
	v_add_u32_e32 v249, 6, v248
	v_cvt_f32_u32_e32 v249, v249
	v_add_u32_e32 v250, 7, v248
	v_cvt_f32_u32_e32 v250, v250
	v_cvt_pk_bf16_f32 v235, v249, v250
	v_add_u32_e32 v249, 8, v248
	v_cvt_f32_u32_e32 v249, v249
	v_add_u32_e32 v250, 9, v248
	v_cvt_f32_u32_e32 v250, v250
	v_cvt_pk_bf16_f32 v236, v249, v250
	v_add_u32_e32 v249, 10, v248
	v_cvt_f32_u32_e32 v249, v249
	v_add_u32_e32 v250, 11, v248
	v_cvt_f32_u32_e32 v250, v250
	v_cvt_pk_bf16_f32 v237, v249, v250
	v_add_u32_e32 v249, 12, v248
	v_cvt_f32_u32_e32 v249, v249
	v_add_u32_e32 v250, 13, v248
	v_cvt_f32_u32_e32 v250, v250
	v_cvt_pk_bf16_f32 v238, v249, v250
	v_add_u32_e32 v249, 14, v248
	v_cvt_f32_u32_e32 v249, v249
	v_add_u32_e32 v250, 15, v248
	v_cvt_f32_u32_e32 v250, v250
	v_cvt_pk_bf16_f32 v239, v249, v250
	v_and_b32_e32 v248, 15, v206
	v_lshrrev_b32_e32 v249, 2, v248
	v_and_b32_e32 v250, 1, v248
	v_lshl_add_u32 v249, v249, 1, v250
	v_and_b32_e32 v250, 3, v249
	v_lshrrev_b32_e32 v251, 4, v206
	v_cmp_eq_u32_e32 vcc, v250, v251
	v_lshrrev_b32_e32 v249, 2, v249
	v_cmp_ne_u32_e64 s[78:79], 0, v249
	v_mov_b32_e32 v250, 0x3f80
	v_mov_b32_e32 v251, 0x3f800000
	s_nop 1
	v_cndmask_b32_e64 v250, v250, v251, s[78:79]
	v_cndmask_b32_e32 v252, 0, v250, vcc
	s_lshr_b32 s77, s19, 15
	s_mulk_i32 s77, 0x1100
	s_add_i32 s77, s77, 0x22200
	v_lshrrev_b32_e32 v248, 4, v206
	v_and_b32_e32 v249, 1, v248
	v_lshrrev_b32_e32 v250, 1, v248
	v_lshlrev_b32_e32 v249, 6, v249
	v_lshl_add_u32 v253, v250, 1, v249
	v_and_b32_e32 v248, 15, v206
	v_cmp_eq_u32_e64 s[78:79], 0, v248
	v_mov_b32_e32 v244, v252
	v_mov_b32_e32 v245, 0
	v_mov_b32_e32 v246, 0
	v_mov_b32_e32 v247, 0
	v_mov_b64_e32 v[240:241], 0
	v_mov_b64_e32 v[242:243], 0
	s_nop 1
	v_smfmac_f32_16x16x64_bf16 v[240:243], v[244:247], v[232:239], v223
	s_nop 15
	s_nop 3
	s_and_saveexec_b64 s[80:81], s[78:79]
	v_cvt_u32_f32_e32 v248, v240
	v_add_u32_e32 v248, -1, v248
	v_lshl_add_u32 v248, v248, 2, s77
	v_add_u32_e32 v249, 0, v253
	ds_write_b32 v248, v249
	v_cvt_u32_f32_e32 v248, v241
	v_add_u32_e32 v248, -1, v248
	v_lshl_add_u32 v248, v248, 2, s77
	v_add_u32_e32 v249, 32, v253
	ds_write_b32 v248, v249
	v_cvt_u32_f32_e32 v248, v242
	v_add_u32_e32 v248, -1, v248
	v_lshl_add_u32 v248, v248, 2, s77
	v_add_u32_e32 v249, 16, v253
	ds_write_b32 v248, v249
	v_cvt_u32_f32_e32 v248, v243
	v_add_u32_e32 v248, -1, v248
	v_lshl_add_u32 v248, v248, 2, s77
	v_add_u32_e32 v249, 48, v253
	ds_write_b32 v248, v249
	s_or_b64 exec, exec, s[80:81]
	v_mov_b32_e32 v244, 0
	v_mov_b32_e32 v245, v252
	v_mov_b32_e32 v246, 0
	v_mov_b32_e32 v247, 0
	v_mov_b64_e32 v[240:241], 0
	v_mov_b64_e32 v[242:243], 0
	s_nop 1
	v_smfmac_f32_16x16x64_bf16 v[240:243], v[244:247], v[232:239], v223
	s_nop 15
	s_nop 3
	s_and_saveexec_b64 s[80:81], s[78:79]
	v_cvt_u32_f32_e32 v248, v240
	v_add_u32_e32 v248, -1, v248
	v_lshl_add_u32 v248, v248, 2, s77
	v_add_u32_e32 v249, 4, v253
	ds_write_b32 v248, v249
	v_cvt_u32_f32_e32 v248, v241
	v_add_u32_e32 v248, -1, v248
	v_lshl_add_u32 v248, v248, 2, s77
	v_add_u32_e32 v249, 36, v253
	ds_write_b32 v248, v249
	v_cvt_u32_f32_e32 v248, v242
	v_add_u32_e32 v248, -1, v248
	v_lshl_add_u32 v248, v248, 2, s77
	v_add_u32_e32 v249, 20, v253
	ds_write_b32 v248, v249
	v_cvt_u32_f32_e32 v248, v243
	v_add_u32_e32 v248, -1, v248
	v_lshl_add_u32 v248, v248, 2, s77
	v_add_u32_e32 v249, 52, v253
	ds_write_b32 v248, v249
	s_or_b64 exec, exec, s[80:81]
	v_mov_b32_e32 v244, 0
	v_mov_b32_e32 v245, 0
	v_mov_b32_e32 v246, v252
	v_mov_b32_e32 v247, 0
	v_mov_b64_e32 v[240:241], 0
	v_mov_b64_e32 v[242:243], 0
	s_nop 1
	v_smfmac_f32_16x16x64_bf16 v[240:243], v[244:247], v[232:239], v223
	s_nop 15
	s_nop 3
	s_and_saveexec_b64 s[80:81], s[78:79]
	v_cvt_u32_f32_e32 v248, v240
	v_add_u32_e32 v248, -1, v248
	v_lshl_add_u32 v248, v248, 2, s77
	v_add_u32_e32 v249, 8, v253
	ds_write_b32 v248, v249
	v_cvt_u32_f32_e32 v248, v241
	v_add_u32_e32 v248, -1, v248
	v_lshl_add_u32 v248, v248, 2, s77
	v_add_u32_e32 v249, 40, v253
	ds_write_b32 v248, v249
	v_cvt_u32_f32_e32 v248, v242
	v_add_u32_e32 v248, -1, v248
	v_lshl_add_u32 v248, v248, 2, s77
	v_add_u32_e32 v249, 24, v253
	ds_write_b32 v248, v249
	v_cvt_u32_f32_e32 v248, v243
	v_add_u32_e32 v248, -1, v248
	v_lshl_add_u32 v248, v248, 2, s77
	v_add_u32_e32 v249, 56, v253
	ds_write_b32 v248, v249
	s_or_b64 exec, exec, s[80:81]
	v_mov_b32_e32 v244, 0
	v_mov_b32_e32 v245, 0
	v_mov_b32_e32 v246, 0
	v_mov_b32_e32 v247, v252
	v_mov_b64_e32 v[240:241], 0
	v_mov_b64_e32 v[242:243], 0
	s_nop 1
	v_smfmac_f32_16x16x64_bf16 v[240:243], v[244:247], v[232:239], v223
	s_nop 15
	s_nop 3
	s_and_saveexec_b64 s[80:81], s[78:79]
	v_cvt_u32_f32_e32 v248, v240
	v_add_u32_e32 v248, -1, v248
	v_lshl_add_u32 v248, v248, 2, s77
	v_add_u32_e32 v249, 12, v253
	ds_write_b32 v248, v249
	v_cvt_u32_f32_e32 v248, v241
	v_add_u32_e32 v248, -1, v248
	v_lshl_add_u32 v248, v248, 2, s77
	v_add_u32_e32 v249, 44, v253
	ds_write_b32 v248, v249
	v_cvt_u32_f32_e32 v248, v242
	v_add_u32_e32 v248, -1, v248
	v_lshl_add_u32 v248, v248, 2, s77
	v_add_u32_e32 v249, 28, v253
	ds_write_b32 v248, v249
	v_cvt_u32_f32_e32 v248, v243
	v_add_u32_e32 v248, -1, v248
	v_lshl_add_u32 v248, v248, 2, s77
	v_add_u32_e32 v249, 60, v253
	ds_write_b32 v248, v249
	s_or_b64 exec, exec, s[80:81]
	v_bfe_u32 v248, v206, 3, 2
	v_lshrrev_b32_e32 v249, 5, v206
	v_lshlrev_b32_e32 v248, 4, v248
	v_lshl_or_b32 v248, v249, 3, v248
	v_and_b32_e32 v249, 7, v206
	v_or_b32_e32 v248, v248, v249
	v_lshl_add_u32 v248, v248, 2, s77
	s_waitcnt lgkmcnt(0)
	ds_read_b32 v254, v248
	v_and_b32_e32 v248, 15, v206
	v_bfe_u32 v249, v248, 1, 2
	v_lshrrev_b32_e32 v250, 3, v248
	v_lshlrev_b32_e32 v249, 4, v249
	v_lshl_or_b32 v249, v250, 3, v249
	v_and_b32_e32 v250, 1, v248
	v_lshl_or_b32 v249, v250, 2, v249
	v_lshl_add_u32 v249, v249, 2, s77
	ds_read_b128 v[248:251], v249
	s_lshr_b32 s76, s19, 6
	s_add_i32 s76, s76, 0x20000
	v_lshrrev_b32_e32 v252, 4, v206
	v_lshl_add_u32 v252, v252, 7, s76
	s_waitcnt lgkmcnt(0)
	v_add_u32_e32 v248, v252, v248
	v_add_u32_e32 v249, v252, v249
	v_add_u32_e32 v250, v252, v250
	v_add_u32_e32 v251, v252, v251
	s_waitcnt vmcnt(0)
	v_cvt_pk_bf16_f32 v152, v147, s0
	v_cvt_pk_bf16_f32 v153, v146, s0
	v_cvt_pk_bf16_f32 v157, v149, s0
	v_cvt_pk_bf16_f32 v158, v148, s0
	v_cvt_pk_bf16_f32 v151, v148, v149
	v_cvt_pk_bf16_f32 v150, v146, v147
	v_lshlrev_b32_e32 v158, 16, v158
	v_lshlrev_b32_e32 v157, 16, v157
	v_lshlrev_b32_e32 v153, 16, v153
	v_lshlrev_b32_e32 v152, 16, v152
	ds_write_b16 v248, v150
	ds_write_b16_d16_hi v249, v150
	ds_write_b16 v250, v151
	ds_write_b16_d16_hi v251, v151
	v_sub_f32_e32 v150, v147, v152
	v_sub_f32_e32 v146, v146, v153
	v_sub_f32_e32 v147, v149, v157
	v_sub_f32_e32 v148, v148, v158
	v_cvt_pk_bf16_f32 v147, v148, v147
	v_cvt_pk_bf16_f32 v146, v146, v150
	ds_write_b16 v248, v146 offset:2176
	ds_write_b16_d16_hi v249, v146 offset:2176
	ds_write_b16 v250, v147 offset:2176
	ds_write_b16_d16_hi v251, v147 offset:2176
	s_waitcnt lgkmcnt(0)
	v_mov_b32_e32 v146, 0x20000
	s_and_b32 s48, s29, 0x6c0
	s_and_b32 s49, s30, 0x700
	s_and_b32 s50, s31, 0x740
	s_and_b32 s51, s34, 0x780
	s_and_b32 s52, s35, 0x7c0
	s_and_b32 s53, s36, 0x640
	s_and_b32 s54, s37, 0x680
	s_and_b32 s55, s38, 0x6c0
	s_and_b32 s67, s26, 0x7c0
	s_and_b64 s[26:27], s[10:11], s[12:13]
	v_lshl_add_u32 v215, v154, 1, v146
	v_mov_b32_e32 v216, 1
	s_lshl_b32 s28, s14, 3
	s_lshl_b32 s30, s15, 3
	s_lshl_b32 s34, s20, 3
	s_movk_i32 s68, 0x7fff
	s_mov_b32 s69, 0
	v_and_b32_e32 v220, 24, v206
	v_lshlrev_b32_e32 v220, 2, v220
	v_and_b32_e32 v221, 2, v206
	v_lshl_or_b32 v220, v221, 3, v220
	v_and_b32_e32 v221, 32, v206
	v_lshrrev_b32_e32 v221, 2, v221
	v_or_b32_e32 v220, v220, v221
	v_and_b32_e32 v221, 4, v206
	v_or_b32_e32 v220, v220, v221
	v_and_b32_e32 v221, 1, v206
	v_lshl_or_b32 v220, v221, 1, v220
	v_mov_b32_e32 v220, v254
	s_lshr_b32 s76, s19, 8
	s_add_i32 s76, s76, 0x20000
	v_add_u32_e32 v220, s76, v220
	v_add_u32_e32 v225, s45, v220
	v_add_u32_e32 v226, s44, v220
	v_add_u32_e32 v227, s60, v220
	v_add_u32_e32 v228, s43, v220
	v_and_b32_e32 v221, 1, v206
	v_mul_u32_u24_e32 v221, 0x880, v221
	v_lshrrev_b32_e32 v220, 4, v206
	v_lshl_add_u32 v221, v220, 5, v221
	v_and_b32_e32 v220, 2, v206
	v_lshl_add_u32 v221, v220, 3, v221
	v_add_u32_e32 v222, 0x20000, v221
	v_cmp_ne_u32_e32 vcc, 0, v220
	v_mov_b32_e32 v220, 0x44444444
	v_mov_b32_e32 v221, 0xeeeeeeee
	s_nop 1
	v_cndmask_b32_e32 v223, v220, v221, vcc
	v_cmp_lt_u32_e64 s[74:75], 47, v206
	v_mov_b32_e32 v224, v184
	ds_read_b128 v[166:169], v224 offset:0
	ds_read_b128 v[170:173], v224 offset:1024
	ds_read_b128 v[174:177], v224 offset:2048
	ds_read_b128 v[178:181], v224 offset:3072
	ds_read_b128 v[182:185], v224 offset:4096
	ds_read_b128 v[186:189], v224 offset:5120
	s_mov_b32 s20, 0

.Lj_gdone:
	s_waitcnt lgkmcnt(0)
	s_barrier
	v_add_u32_e32 v240, s45, v229
	v_add_u32_e32 v241, s44, v229
	v_add_u32_e32 v242, s60, v229
	ds_read_b128 v[150:153], v240 offset:0
	ds_read_b128 v[194:197], v240 offset:128
	ds_read_b128 v[198:201], v240 offset:256
	ds_read_b128 v[232:235], v240 offset:384
	s_cmp_eq_u32 s20, 0
	s_cselect_b64 s[36:37], -1, 0
	s_add_i32 s29, s20, 1
	s_and_b32 s14, s29, 1
	s_lshl_b32 s10, s14, 13
	s_mov_b32 s11, 0
	v_lshl_add_u64 v[250:251], v[0:1], 0, s[10:11]
	s_mul_i32 s15, s14, 0x1100
	v_add_u32_e32 v243, s15, v228
	v_mov_b32_e32 v253, s29
	s_waitcnt lgkmcnt(3)
	v_smfmac_f32_16x16x64_bf16 v[146:149], v[150:153], v[98:105], v223
	v_smfmac_f32_16x16x64_bf16 v[154:157], v[150:153], v[114:121], v223
	v_smfmac_f32_16x16x64_bf16 v[158:161], v[150:153], v[130:137], v223
	v_smfmac_f32_16x16x64_bf16 v[162:165], v[150:153], v[174:181], v223
	v_or3_b32 v231, v150, v151, v231
	v_or3_b32 v231, v152, v153, v231
	ds_read_b128 v[174:177], v224 offset:14336
	ds_read_b128 v[178:181], v224 offset:15360
	ds_read_b128 v[150:153], v241 offset:0
	s_waitcnt lgkmcnt(5)
	v_smfmac_f32_16x16x64_bf16 v[146:149], v[194:197], v[106:113], v223
	v_smfmac_f32_16x16x64_bf16 v[154:157], v[194:197], v[122:129], v223
	v_smfmac_f32_16x16x64_bf16 v[158:161], v[194:197], v[138:145], v223
	v_smfmac_f32_16x16x64_bf16 v[162:165], v[194:197], v[182:189], v223
	v_or3_b32 v231, v194, v195, v231
	v_or3_b32 v231, v196, v197, v231
	ds_read_b128 v[182:185], v224 offset:16384
	ds_read_b128 v[186:189], v224 offset:17408
	ds_read_b128 v[194:197], v241 offset:128
	s_waitcnt lgkmcnt(7)
	v_smfmac_f32_16x16x64_bf16 v[146:149], v[198:201], a[0:7], v223
	v_smfmac_f32_16x16x64_bf16 v[154:157], v[198:201], a[16:23], v223
	v_smfmac_f32_16x16x64_bf16 v[158:161], v[198:201], a[32:39], v223
	v_smfmac_f32_16x16x64_bf16 v[162:165], v[198:201], v[166:173], v223
	v_or3_b32 v231, v198, v199, v231
	v_or3_b32 v231, v200, v201, v231
	ds_read_b128 v[166:169], v224 offset:18432
	ds_read_b128 v[170:173], v224 offset:19456
	ds_read_b128 v[198:201], v241 offset:256
	s_waitcnt lgkmcnt(9)
	v_smfmac_f32_16x16x64_bf16 v[146:149], v[232:235], a[8:15], v223
	v_smfmac_f32_16x16x64_bf16 v[154:157], v[232:235], a[24:31], v223
	v_smfmac_f32_16x16x64_bf16 v[158:161], v[232:235], a[40:47], v223
	s_waitcnt lgkmcnt(7)
	v_smfmac_f32_16x16x64_bf16 v[162:165], v[232:235], v[174:181], v223
	v_or3_b32 v231, v232, v233, v231
	v_or3_b32 v231, v234, v235, v231
	ds_read_b128 v[174:177], v224 offset:20480
	ds_read_b128 v[178:181], v224 offset:21504
	ds_read_b128 v[232:235], v241 offset:384
	s_waitcnt lgkmcnt(9)
	v_smfmac_f32_16x16x64_bf16 v[146:149], v[150:153], a[48:55], v223
	v_smfmac_f32_16x16x64_bf16 v[154:157], v[150:153], a[64:71], v223
	v_smfmac_f32_16x16x64_bf16 v[158:161], v[150:153], a[80:87], v223
	s_waitcnt lgkmcnt(7)
	v_smfmac_f32_16x16x64_bf16 v[162:165], v[150:153], v[182:189], v223
	v_or3_b32 v231, v150, v151, v231
	v_or3_b32 v231, v152, v153, v231
	ds_read_b128 v[182:185], v224 offset:22528
	ds_read_b128 v[186:189], v224 offset:23552
	ds_read_b128 v[150:153], v242 offset:0
	s_waitcnt lgkmcnt(9)
	v_smfmac_f32_16x16x64_bf16 v[146:149], v[194:197], a[56:63], v223
	v_smfmac_f32_16x16x64_bf16 v[154:157], v[194:197], a[72:79], v223
	v_smfmac_f32_16x16x64_bf16 v[158:161], v[194:197], a[88:95], v223
	s_waitcnt lgkmcnt(7)
	v_smfmac_f32_16x16x64_bf16 v[162:165], v[194:197], v[166:173], v223
	v_or3_b32 v231, v194, v195, v231
	v_or3_b32 v231, v196, v197, v231
	ds_read_b128 v[166:169], v224 offset:24576
	ds_read_b128 v[170:173], v224 offset:25600
	ds_read_b128 v[194:197], v242 offset:128
	s_waitcnt lgkmcnt(9)
	v_smfmac_f32_16x16x64_bf16 v[146:149], v[198:201], a[96:103], v223
	v_smfmac_f32_16x16x64_bf16 v[154:157], v[198:201], a[112:119], v223
	v_smfmac_f32_16x16x64_bf16 v[158:161], v[198:201], a[128:135], v223
	s_waitcnt lgkmcnt(7)
	v_smfmac_f32_16x16x64_bf16 v[162:165], v[198:201], v[174:181], v223
	v_or3_b32 v231, v198, v199, v231
	v_or3_b32 v231, v200, v201, v231
	ds_read_b128 v[174:177], v224 offset:26624
	ds_read_b128 v[178:181], v224 offset:27648
	ds_read_b128 v[198:201], v242 offset:256
	s_waitcnt lgkmcnt(9)
	v_smfmac_f32_16x16x64_bf16 v[146:149], v[232:235], a[104:111], v223
	v_smfmac_f32_16x16x64_bf16 v[154:157], v[232:235], a[120:127], v223
	v_smfmac_f32_16x16x64_bf16 v[158:161], v[232:235], a[136:143], v223
	s_waitcnt lgkmcnt(7)
	v_smfmac_f32_16x16x64_bf16 v[162:165], v[232:235], v[182:189], v223
	v_or3_b32 v231, v232, v233, v231
	v_or3_b32 v231, v234, v235, v231
	ds_read_b128 v[182:185], v224 offset:28672
	ds_read_b128 v[186:189], v224 offset:29696
	ds_read_b128 v[232:235], v242 offset:384
	s_waitcnt lgkmcnt(9)
	v_smfmac_f32_16x16x64_bf16 v[146:149], v[150:153], a[144:151], v223
	v_smfmac_f32_16x16x64_bf16 v[154:157], v[150:153], a[160:167], v223
	v_smfmac_f32_16x16x64_bf16 v[158:161], v[150:153], a[176:183], v223
	s_waitcnt lgkmcnt(7)
	v_smfmac_f32_16x16x64_bf16 v[162:165], v[150:153], v[166:173], v223
	v_or3_b32 v231, v150, v151, v231
	v_or3_b32 v231, v152, v153, v231
	ds_read_b128 v[166:169], v224 offset:30720
	ds_read_b128 v[170:173], v224 offset:31744
	s_waitcnt lgkmcnt(8)
	v_smfmac_f32_16x16x64_bf16 v[146:149], v[194:197], a[152:159], v223
	v_smfmac_f32_16x16x64_bf16 v[154:157], v[194:197], a[168:175], v223
	v_smfmac_f32_16x16x64_bf16 v[158:161], v[194:197], a[184:191], v223
	s_waitcnt lgkmcnt(6)
	v_smfmac_f32_16x16x64_bf16 v[162:165], v[194:197], v[174:181], v223
	v_or3_b32 v231, v194, v195, v231
	v_or3_b32 v231, v196, v197, v231
	ds_read_b128 v[174:177], v224 offset:2048
	ds_read_b128 v[178:181], v224 offset:3072
	s_waitcnt lgkmcnt(7)
	v_smfmac_f32_16x16x64_bf16 v[146:149], v[198:201], a[192:199], v223
	v_smfmac_f32_16x16x64_bf16 v[154:157], v[198:201], a[208:215], v223
	v_smfmac_f32_16x16x64_bf16 v[158:161], v[198:201], a[224:231], v223
	s_waitcnt lgkmcnt(5)
	v_smfmac_f32_16x16x64_bf16 v[162:165], v[198:201], v[182:189], v223
	v_or3_b32 v231, v198, v199, v231
	v_or3_b32 v231, v200, v201, v231
	ds_read_b128 v[182:185], v224 offset:4096
	ds_read_b128 v[186:189], v224 offset:5120
	s_waitcnt lgkmcnt(6)
	v_smfmac_f32_16x16x64_bf16 v[146:149], v[232:235], a[200:207], v223
	v_smfmac_f32_16x16x64_bf16 v[154:157], v[232:235], a[216:223], v223
	v_smfmac_f32_16x16x64_bf16 v[158:161], v[232:235], a[232:239], v223
	s_waitcnt lgkmcnt(4)
	v_smfmac_f32_16x16x64_bf16 v[162:165], v[232:235], v[166:173], v223
	v_or3_b32 v231, v232, v233, v231
	v_or3_b32 v231, v234, v235, v231
	ds_read_b128 v[166:169], v224 offset:0
	ds_read_b128 v[170:173], v224 offset:1024
	v_and_b32_e32 v231, 0x7fff7fff, v231
	v_cmp_ne_u32_e32 vcc, 0, v231
	s_nop 1
	v_pk_add_f32 v[236:237], v[146:147], v[148:149]
	v_pk_add_f32 v[238:239], v[154:155], v[156:157]
	v_pk_add_f32 v[240:241], v[158:159], v[160:161]
	v_pk_add_f32 v[146:147], v[162:163], v[164:165]
	s_cmp_eq_u64 vcc, 0
	s_cbranch_scc0 .Lj_nz
	s_cmp_lg_u32 s20, 0
	s_cbranch_scc1 .Lj_stop
.Lj_nz:
	v_add_f32_e32 v236, v236, v237
	v_add_f32_e32 v237, v238, v239
	v_add_f32_e32 v238, v240, v241
	v_add_f32_e32 v239, v146, v147
	v_cndmask_b32_e64 v236, v236, v237, s[4:5]
	v_cndmask_b32_e64 v236, v236, v238, s[6:7]
	v_cndmask_b32_e64 v156, v236, v239, s[74:75]
	s_cmpk_eq_i32 s20, 0x64
	s_cbranch_scc1 .Lj_nopub
	v_add_f32_e32 v236, v208, v156
	v_cndmask_b32_e64 v252, v156, v236, s[36:37]
	global_store_dwordx2 v[250:251], v[252:253], off sc1
	v_cvt_pk_bf16_f32 v237, v252, v252
	v_lshlrev_b32_e32 v238, 16, v237
	v_sub_f32_e32 v238, v252, v238
	v_cvt_pk_bf16_f32 v238, v238, v238
	ds_write_b16 v243, v237
	ds_write_b16 v243, v238 offset:2176
